# GEMM peel+trim + all K-loop LDS-DMA in saddr form (no 64-bit VALU address adds)
# baseline (speedup 1.0000x reference)
.LBB0_210:
	s_ashr_i32 s49, s48, 31
	s_lshl_b64 s[4:5], s[48:49], 19
	s_add_u32 s50, s6, s4
	s_addc_u32 s51, s7, s5
	s_and_b64 s[4:5], s[38:39], exec
	s_cselect_b32 s49, s51, s41
	s_cselect_b32 s64, s50, s40
	s_ashr_i32 s45, s44, 31
	s_lshl_b64 s[4:5], s[44:45], 19
	s_add_u32 s52, s8, s4
	s_addc_u32 s53, s9, s5
	s_and_b64 s[4:5], s[38:39], exec
	s_cselect_b32 s45, s53, s43
	s_cselect_b32 s65, s52, s42
	s_add_u32 s70, s64, 0x80
	s_addc_u32 s71, s49, 0
	s_add_u32 s4, s40, 0x40080
	s_addc_u32 s5, s41, 0
	s_add_u32 s78, s42, 0x100
	v_lshl_add_u64 v[144:145], s[4:5], 0, v[140:141]
	v_lshl_add_u64 v[146:147], s[4:5], 0, v[142:143]
	s_addc_u32 s79, s43, 0
	s_mov_b32 s80, -2
	s_mov_b64 s[42:43], 0
	s_waitcnt lgkmcnt(0)
	s_add_u32 s4, s40, s42
	s_addc_u32 s5, s41, s43
	s_add_u32 s98, s4, 0x40080
	s_addc_u32 s99, s5, 0
	s_add_u32 s81, s4, 0x100
	s_addc_u32 s82, s5, 0
	s_add_u32 s60, s78, s42
	s_addc_u32 s61, s79, s43
	s_add_u32 s4, s4, 0x180
	s_addc_u32 s5, s5, 0
	s_add_i32 s83, 0, 0x10000
	s_add_i32 s84, 0, 0x14000
	v_add_u32_e32 v2, s83, v151
	s_waitcnt vmcnt(0)
	ds_read_b128 v[154:157], v2
	ds_read_b128 v[158:161], v2 offset:1024
	ds_read_b128 v[162:165], v2 offset:2048
	ds_read_b128 v[166:169], v2 offset:3072
	v_add_u32_e32 v2, s84, v151
	ds_read_b128 v[170:173], v2
	ds_read_b128 v[174:177], v2 offset:1024
	ds_read_b128 v[178:181], v2 offset:2048
	ds_read_b128 v[182:185], v2 offset:3072
	s_cmpk_eq_i32 s42, 0x700
	s_cselect_b32 s13, s71, s5
	s_cselect_b32 s12, s70, s4
	s_cselect_b32 s61, s45, s61
	s_cselect_b32 s60, s65, s60
	s_cselect_b32 s5, s49, s82
	s_cselect_b32 s4, s64, s81
	s_add_i32 m0, s17, 0xc000
	ds_read_b128 v[186:189], v153
	ds_read_b128 v[190:193], v153 offset:1024
	ds_read_b128 v[204:207], v153 offset:2048
	ds_read_b128 v[208:211], v153 offset:3072
	ds_read_b128 v[212:215], v153 offset:4096
	ds_read_b128 v[216:219], v153 offset:5120
	ds_read_b128 v[220:223], v153 offset:6144
	ds_read_b128 v[224:227], v153 offset:7168
	global_load_lds_dwordx4 v140, s[98:99]
	s_add_i32 m0, s17, 0xe000
	s_nop 0
	global_load_lds_dwordx4 v142, s[98:99]
	s_waitcnt vmcnt(8)
	s_waitcnt lgkmcnt(0)
	s_barrier
	s_setprio 1
	v_mfma_f32_16x16x32_bf16 v[128:131], v[154:157], v[186:189], 0
	v_mfma_f32_16x16x32_bf16 v[124:127], v[162:165], v[186:189], 0
	v_mfma_f32_16x16x32_bf16 v[112:115], v[154:157], v[204:207], 0
	v_mfma_f32_16x16x32_bf16 v[108:111], v[162:165], v[204:207], 0
	v_mfma_f32_16x16x32_bf16 v[96:99], v[154:157], v[212:215], 0
	v_mfma_f32_16x16x32_bf16 v[92:95], v[162:165], v[212:215], 0
	v_mfma_f32_16x16x32_bf16 v[80:83], v[154:157], v[220:223], 0
	v_mfma_f32_16x16x32_bf16 v[76:79], v[162:165], v[220:223], 0
	v_mfma_f32_16x16x32_bf16 v[128:131], v[158:161], v[190:193], v[128:131]
	v_mfma_f32_16x16x32_bf16 v[124:127], v[166:169], v[190:193], v[124:127]
	v_mfma_f32_16x16x32_bf16 v[112:115], v[158:161], v[208:211], v[112:115]
	v_mfma_f32_16x16x32_bf16 v[108:111], v[166:169], v[208:211], v[108:111]
	v_mfma_f32_16x16x32_bf16 v[96:99], v[158:161], v[216:219], v[96:99]
	v_mfma_f32_16x16x32_bf16 v[92:95], v[166:169], v[216:219], v[92:95]
	v_mfma_f32_16x16x32_bf16 v[80:83], v[158:161], v[224:227], v[80:83]
	v_mfma_f32_16x16x32_bf16 v[76:79], v[166:169], v[224:227], v[76:79]
	v_mfma_f32_16x16x32_bf16 v[120:123], v[170:173], v[186:189], 0
	v_mfma_f32_16x16x32_bf16 v[116:119], v[178:181], v[186:189], 0
	v_mfma_f32_16x16x32_bf16 v[104:107], v[170:173], v[204:207], 0
	v_mfma_f32_16x16x32_bf16 v[100:103], v[178:181], v[204:207], 0
	v_mfma_f32_16x16x32_bf16 v[88:91], v[170:173], v[212:215], 0
	v_mfma_f32_16x16x32_bf16 v[84:87], v[178:181], v[212:215], 0
	v_mfma_f32_16x16x32_bf16 v[72:75], v[170:173], v[220:223], 0
	v_mfma_f32_16x16x32_bf16 v[68:71], v[178:181], v[220:223], 0
	v_mfma_f32_16x16x32_bf16 v[120:123], v[174:177], v[190:193], v[120:123]
	v_mfma_f32_16x16x32_bf16 v[116:119], v[182:185], v[190:193], v[116:119]
	v_mfma_f32_16x16x32_bf16 v[104:107], v[174:177], v[208:211], v[104:107]
	v_mfma_f32_16x16x32_bf16 v[100:103], v[182:185], v[208:211], v[100:103]
	v_mfma_f32_16x16x32_bf16 v[88:91], v[174:177], v[216:219], v[88:91]
	v_mfma_f32_16x16x32_bf16 v[84:87], v[182:185], v[216:219], v[84:87]
	v_mfma_f32_16x16x32_bf16 v[72:75], v[174:177], v[224:227], v[72:75]
	v_mfma_f32_16x16x32_bf16 v[68:71], v[182:185], v[224:227], v[68:71]
	s_setprio 0
	s_barrier
	s_add_i32 s81, s83, s16
	s_mov_b32 m0, s81
	ds_read_b128 v[186:189], v153 offset:16384
	ds_read_b128 v[190:193], v153 offset:17408
	ds_read_b128 v[204:207], v153 offset:18432
	ds_read_b128 v[208:211], v153 offset:19456
	ds_read_b128 v[212:215], v153 offset:20480
	ds_read_b128 v[216:219], v153 offset:21504
	ds_read_b128 v[220:223], v153 offset:22528
	ds_read_b128 v[224:227], v153 offset:23552
	global_load_lds_dwordx4 v136, s[60:61]
	s_add_i32 m0, s81, 0x2000
	s_add_u32 s82, s60, 0x40000
	s_addc_u32 s83, s61, 0
	s_add_i32 s81, s84, s16
	global_load_lds_dwordx4 v132, s[60:61]
	s_mov_b32 m0, s81
	s_nop 0
	global_load_lds_dwordx4 v136, s[82:83]
	s_add_i32 m0, s81, 0x2000
	s_nop 0
	global_load_lds_dwordx4 v132, s[82:83]
	s_mov_b32 m0, s17
	s_nop 0
	global_load_lds_dwordx4 v138, s[4:5]
	s_mov_b32 m0, s46
	s_nop 0
	global_load_lds_dwordx4 v134, s[4:5]
	s_waitcnt vmcnt(8)
	s_waitcnt lgkmcnt(0)
	s_barrier
	s_setprio 1
	v_mfma_f32_16x16x32_bf16 v[64:67], v[154:157], v[186:189], 0
	v_mfma_f32_16x16x32_bf16 v[60:63], v[162:165], v[186:189], 0
	v_mfma_f32_16x16x32_bf16 v[48:51], v[154:157], v[204:207], 0
	v_mfma_f32_16x16x32_bf16 v[44:47], v[162:165], v[204:207], 0
	v_mfma_f32_16x16x32_bf16 v[32:35], v[154:157], v[212:215], 0
	v_mfma_f32_16x16x32_bf16 v[28:31], v[162:165], v[212:215], 0
	v_mfma_f32_16x16x32_bf16 v[16:19], v[154:157], v[220:223], 0
	v_mfma_f32_16x16x32_bf16 v[12:15], v[162:165], v[220:223], 0
	v_mfma_f32_16x16x32_bf16 v[64:67], v[158:161], v[190:193], v[64:67]
	v_mfma_f32_16x16x32_bf16 v[60:63], v[166:169], v[190:193], v[60:63]
	v_mfma_f32_16x16x32_bf16 v[48:51], v[158:161], v[208:211], v[48:51]
	v_mfma_f32_16x16x32_bf16 v[44:47], v[166:169], v[208:211], v[44:47]
	v_mfma_f32_16x16x32_bf16 v[32:35], v[158:161], v[216:219], v[32:35]
	v_mfma_f32_16x16x32_bf16 v[28:31], v[166:169], v[216:219], v[28:31]
	v_mfma_f32_16x16x32_bf16 v[16:19], v[158:161], v[224:227], v[16:19]
	v_mfma_f32_16x16x32_bf16 v[12:15], v[166:169], v[224:227], v[12:15]
	v_mfma_f32_16x16x32_bf16 v[56:59], v[170:173], v[186:189], 0
	v_mfma_f32_16x16x32_bf16 v[52:55], v[178:181], v[186:189], 0
	v_mfma_f32_16x16x32_bf16 v[40:43], v[170:173], v[204:207], 0
	v_mfma_f32_16x16x32_bf16 v[36:39], v[178:181], v[204:207], 0
	v_mfma_f32_16x16x32_bf16 v[24:27], v[170:173], v[212:215], 0
	v_mfma_f32_16x16x32_bf16 v[20:23], v[178:181], v[212:215], 0
	v_mfma_f32_16x16x32_bf16 v[8:11], v[170:173], v[220:223], 0
	v_mfma_f32_16x16x32_bf16 v[4:7], v[178:181], v[220:223], 0
	v_mfma_f32_16x16x32_bf16 v[56:59], v[174:177], v[190:193], v[56:59]
	v_mfma_f32_16x16x32_bf16 v[52:55], v[182:185], v[190:193], v[52:55]
	v_mfma_f32_16x16x32_bf16 v[40:43], v[174:177], v[208:211], v[40:43]
	v_mfma_f32_16x16x32_bf16 v[36:39], v[182:185], v[208:211], v[36:39]
	v_mfma_f32_16x16x32_bf16 v[24:27], v[174:177], v[216:219], v[24:27]
	v_mfma_f32_16x16x32_bf16 v[20:23], v[182:185], v[216:219], v[20:23]
	v_mfma_f32_16x16x32_bf16 v[8:11], v[174:177], v[224:227], v[8:11]
	v_mfma_f32_16x16x32_bf16 v[4:7], v[182:185], v[224:227], v[4:7]
	s_setprio 0
	s_barrier
	s_add_i32 s81, 0, 0x18000
	v_add_u32_e32 v2, s81, v151
	s_add_i32 s82, 0, 0x1c000
	ds_read_b128 v[154:157], v2
	ds_read_b128 v[158:161], v2 offset:1024
	ds_read_b128 v[162:165], v2 offset:2048
	ds_read_b128 v[166:169], v2 offset:3072
	v_add_u32_e32 v2, s82, v151
	ds_read_b128 v[170:173], v2
	ds_read_b128 v[174:177], v2 offset:1024
	ds_read_b128 v[178:181], v2 offset:2048
	ds_read_b128 v[182:185], v2 offset:3072
	s_add_u32 s4, s4, 0x40000
	s_addc_u32 s5, s5, 0
	s_mov_b32 m0, s47
	ds_read_b128 v[186:189], v153 offset:32768
	ds_read_b128 v[190:193], v153 offset:33792
	ds_read_b128 v[204:207], v153 offset:34816
	ds_read_b128 v[208:211], v153 offset:35840
	ds_read_b128 v[212:215], v153 offset:36864
	ds_read_b128 v[216:219], v153 offset:37888
	ds_read_b128 v[220:223], v153 offset:38912
	ds_read_b128 v[224:227], v153 offset:39936
	global_load_lds_dwordx4 v138, s[4:5]
	s_mov_b32 m0, s58
	s_nop 0
	global_load_lds_dwordx4 v134, s[4:5]
	s_waitcnt vmcnt(8)
	s_waitcnt lgkmcnt(0)
	s_barrier
	s_setprio 1
	v_mfma_f32_16x16x32_bf16 v[128:131], v[154:157], v[186:189], v[128:131]
	v_mfma_f32_16x16x32_bf16 v[124:127], v[162:165], v[186:189], v[124:127]
	v_mfma_f32_16x16x32_bf16 v[112:115], v[154:157], v[204:207], v[112:115]
	v_mfma_f32_16x16x32_bf16 v[108:111], v[162:165], v[204:207], v[108:111]
	v_mfma_f32_16x16x32_bf16 v[96:99], v[154:157], v[212:215], v[96:99]
	v_mfma_f32_16x16x32_bf16 v[92:95], v[162:165], v[212:215], v[92:95]
	v_mfma_f32_16x16x32_bf16 v[80:83], v[154:157], v[220:223], v[80:83]
	v_mfma_f32_16x16x32_bf16 v[76:79], v[162:165], v[220:223], v[76:79]
	v_mfma_f32_16x16x32_bf16 v[128:131], v[158:161], v[190:193], v[128:131]
	v_mfma_f32_16x16x32_bf16 v[124:127], v[166:169], v[190:193], v[124:127]
	v_mfma_f32_16x16x32_bf16 v[112:115], v[158:161], v[208:211], v[112:115]
	v_mfma_f32_16x16x32_bf16 v[108:111], v[166:169], v[208:211], v[108:111]
	v_mfma_f32_16x16x32_bf16 v[96:99], v[158:161], v[216:219], v[96:99]
	v_mfma_f32_16x16x32_bf16 v[92:95], v[166:169], v[216:219], v[92:95]
	v_mfma_f32_16x16x32_bf16 v[80:83], v[158:161], v[224:227], v[80:83]
	v_mfma_f32_16x16x32_bf16 v[76:79], v[166:169], v[224:227], v[76:79]
	v_mfma_f32_16x16x32_bf16 v[120:123], v[170:173], v[186:189], v[120:123]
	v_mfma_f32_16x16x32_bf16 v[116:119], v[178:181], v[186:189], v[116:119]
	v_mfma_f32_16x16x32_bf16 v[104:107], v[170:173], v[204:207], v[104:107]
	v_mfma_f32_16x16x32_bf16 v[100:103], v[178:181], v[204:207], v[100:103]
	v_mfma_f32_16x16x32_bf16 v[88:91], v[170:173], v[212:215], v[88:91]
	v_mfma_f32_16x16x32_bf16 v[84:87], v[178:181], v[212:215], v[84:87]
	v_mfma_f32_16x16x32_bf16 v[72:75], v[170:173], v[220:223], v[72:75]
	v_mfma_f32_16x16x32_bf16 v[68:71], v[178:181], v[220:223], v[68:71]
	v_mfma_f32_16x16x32_bf16 v[120:123], v[174:177], v[190:193], v[120:123]
	v_mfma_f32_16x16x32_bf16 v[116:119], v[182:185], v[190:193], v[116:119]
	v_mfma_f32_16x16x32_bf16 v[104:107], v[174:177], v[208:211], v[104:107]
	v_mfma_f32_16x16x32_bf16 v[100:103], v[182:185], v[208:211], v[100:103]
	v_mfma_f32_16x16x32_bf16 v[88:91], v[174:177], v[216:219], v[88:91]
	v_mfma_f32_16x16x32_bf16 v[84:87], v[182:185], v[216:219], v[84:87]
	v_mfma_f32_16x16x32_bf16 v[72:75], v[174:177], v[224:227], v[72:75]
	v_mfma_f32_16x16x32_bf16 v[68:71], v[182:185], v[224:227], v[68:71]
	s_setprio 0
	s_barrier
	s_add_i32 s4, s81, s16
	s_add_u32 s98, s60, 0x80
	s_addc_u32 s99, s61, 0
	s_mov_b32 m0, s4
	ds_read_b128 v[186:189], v153 offset:49152
	ds_read_b128 v[190:193], v153 offset:50176
	ds_read_b128 v[204:207], v153 offset:51200
	ds_read_b128 v[208:211], v153 offset:52224
	ds_read_b128 v[212:215], v153 offset:53248
	ds_read_b128 v[216:219], v153 offset:54272
	ds_read_b128 v[220:223], v153 offset:55296
	ds_read_b128 v[224:227], v153 offset:56320
	global_load_lds_dwordx4 v136, s[98:99]
	s_add_i32 m0, s4, 0x2000
	s_add_u32 s4, s60, 0x40080
	s_addc_u32 s5, s61, 0
	s_add_i32 s60, s82, s16
	global_load_lds_dwordx4 v132, s[98:99]
	s_mov_b32 m0, s60
	s_nop 0
	global_load_lds_dwordx4 v136, s[4:5]
	s_add_i32 m0, s60, 0x2000
	s_nop 0
	global_load_lds_dwordx4 v132, s[4:5]
	s_mov_b32 m0, s74
	s_nop 0
	global_load_lds_dwordx4 v138, s[12:13]
	s_mov_b32 m0, s75
	s_nop 0
	global_load_lds_dwordx4 v134, s[12:13]
	s_waitcnt vmcnt(8)
	s_waitcnt lgkmcnt(0)
	s_barrier
	s_setprio 1
	v_mfma_f32_16x16x32_bf16 v[64:67], v[154:157], v[186:189], v[64:67]
	v_mfma_f32_16x16x32_bf16 v[60:63], v[162:165], v[186:189], v[60:63]
	v_mfma_f32_16x16x32_bf16 v[48:51], v[154:157], v[204:207], v[48:51]
	v_mfma_f32_16x16x32_bf16 v[44:47], v[162:165], v[204:207], v[44:47]
	v_mfma_f32_16x16x32_bf16 v[32:35], v[154:157], v[212:215], v[32:35]
	v_mfma_f32_16x16x32_bf16 v[28:31], v[162:165], v[212:215], v[28:31]
	v_mfma_f32_16x16x32_bf16 v[16:19], v[154:157], v[220:223], v[16:19]
	v_mfma_f32_16x16x32_bf16 v[12:15], v[162:165], v[220:223], v[12:15]
	v_mfma_f32_16x16x32_bf16 v[64:67], v[158:161], v[190:193], v[64:67]
	v_mfma_f32_16x16x32_bf16 v[60:63], v[166:169], v[190:193], v[60:63]
	v_mfma_f32_16x16x32_bf16 v[48:51], v[158:161], v[208:211], v[48:51]
	v_mfma_f32_16x16x32_bf16 v[44:47], v[166:169], v[208:211], v[44:47]
	v_mfma_f32_16x16x32_bf16 v[32:35], v[158:161], v[216:219], v[32:35]
	v_mfma_f32_16x16x32_bf16 v[28:31], v[166:169], v[216:219], v[28:31]
	v_mfma_f32_16x16x32_bf16 v[16:19], v[158:161], v[224:227], v[16:19]
	v_mfma_f32_16x16x32_bf16 v[12:15], v[166:169], v[224:227], v[12:15]
	v_mfma_f32_16x16x32_bf16 v[56:59], v[170:173], v[186:189], v[56:59]
	v_mfma_f32_16x16x32_bf16 v[52:55], v[178:181], v[186:189], v[52:55]
	v_mfma_f32_16x16x32_bf16 v[40:43], v[170:173], v[204:207], v[40:43]
	v_mfma_f32_16x16x32_bf16 v[36:39], v[178:181], v[204:207], v[36:39]
	v_mfma_f32_16x16x32_bf16 v[24:27], v[170:173], v[212:215], v[24:27]
	v_mfma_f32_16x16x32_bf16 v[20:23], v[178:181], v[212:215], v[20:23]
	v_mfma_f32_16x16x32_bf16 v[8:11], v[170:173], v[220:223], v[8:11]
	v_mfma_f32_16x16x32_bf16 v[4:7], v[178:181], v[220:223], v[4:7]
	v_mfma_f32_16x16x32_bf16 v[56:59], v[174:177], v[190:193], v[56:59]
	v_mfma_f32_16x16x32_bf16 v[52:55], v[182:185], v[190:193], v[52:55]
	v_mfma_f32_16x16x32_bf16 v[40:43], v[174:177], v[208:211], v[40:43]
	v_mfma_f32_16x16x32_bf16 v[36:39], v[182:185], v[208:211], v[36:39]
	v_mfma_f32_16x16x32_bf16 v[24:27], v[174:177], v[216:219], v[24:27]
	v_mfma_f32_16x16x32_bf16 v[20:23], v[182:185], v[216:219], v[20:23]
	v_mfma_f32_16x16x32_bf16 v[8:11], v[174:177], v[224:227], v[8:11]
	v_mfma_f32_16x16x32_bf16 v[4:7], v[182:185], v[224:227], v[4:7]
	s_setprio 0
	s_barrier
	s_add_i32 s80, s80, 2
	s_add_u32 s42, s42, 0x100
	s_addc_u32 s43, s43, 0
	s_cmp_gt_u32 s80, 13
.LBB0_211:
	s_add_u32 s4, s40, s42
	s_addc_u32 s5, s41, s43
	s_add_u32 s98, s4, 0x40080
	s_addc_u32 s99, s5, 0
	s_add_u32 s81, s4, 0x100
	s_addc_u32 s82, s5, 0
	s_add_u32 s60, s78, s42
	s_addc_u32 s61, s79, s43
	s_add_u32 s4, s4, 0x180
	s_addc_u32 s5, s5, 0
	s_add_i32 s83, 0, 0x10000
	s_add_i32 s84, 0, 0x14000
	v_add_u32_e32 v2, s83, v151
	s_waitcnt vmcnt(0)
	ds_read_b128 v[154:157], v2
	ds_read_b128 v[158:161], v2 offset:1024
	ds_read_b128 v[162:165], v2 offset:2048
	ds_read_b128 v[166:169], v2 offset:3072
	v_add_u32_e32 v2, s84, v151
	ds_read_b128 v[170:173], v2
	ds_read_b128 v[174:177], v2 offset:1024
	ds_read_b128 v[178:181], v2 offset:2048
	ds_read_b128 v[182:185], v2 offset:3072
	s_cmpk_eq_i32 s42, 0x700
	s_cselect_b32 s13, s71, s5
	s_cselect_b32 s12, s70, s4
	s_cselect_b32 s61, s45, s61
	s_cselect_b32 s60, s65, s60
	s_cselect_b32 s5, s49, s82
	s_cselect_b32 s4, s64, s81
	s_add_i32 m0, s17, 0xc000
	ds_read_b128 v[186:189], v153
	ds_read_b128 v[190:193], v153 offset:1024
	ds_read_b128 v[204:207], v153 offset:2048
	ds_read_b128 v[208:211], v153 offset:3072
	ds_read_b128 v[212:215], v153 offset:4096
	ds_read_b128 v[216:219], v153 offset:5120
	ds_read_b128 v[220:223], v153 offset:6144
	ds_read_b128 v[224:227], v153 offset:7168
	global_load_lds_dwordx4 v140, s[98:99]
	s_add_i32 m0, s17, 0xe000
	s_nop 0
	global_load_lds_dwordx4 v142, s[98:99]
	s_waitcnt vmcnt(8)
	s_waitcnt lgkmcnt(0)
	s_barrier
	s_setprio 1
	v_mfma_f32_16x16x32_bf16 v[128:131], v[154:157], v[186:189], v[128:131]
	v_mfma_f32_16x16x32_bf16 v[124:127], v[162:165], v[186:189], v[124:127]
	v_mfma_f32_16x16x32_bf16 v[112:115], v[154:157], v[204:207], v[112:115]
	v_mfma_f32_16x16x32_bf16 v[108:111], v[162:165], v[204:207], v[108:111]
	v_mfma_f32_16x16x32_bf16 v[96:99], v[154:157], v[212:215], v[96:99]
	v_mfma_f32_16x16x32_bf16 v[92:95], v[162:165], v[212:215], v[92:95]
	v_mfma_f32_16x16x32_bf16 v[80:83], v[154:157], v[220:223], v[80:83]
	v_mfma_f32_16x16x32_bf16 v[76:79], v[162:165], v[220:223], v[76:79]
	v_mfma_f32_16x16x32_bf16 v[128:131], v[158:161], v[190:193], v[128:131]
	v_mfma_f32_16x16x32_bf16 v[124:127], v[166:169], v[190:193], v[124:127]
	v_mfma_f32_16x16x32_bf16 v[112:115], v[158:161], v[208:211], v[112:115]
	v_mfma_f32_16x16x32_bf16 v[108:111], v[166:169], v[208:211], v[108:111]
	v_mfma_f32_16x16x32_bf16 v[96:99], v[158:161], v[216:219], v[96:99]
	v_mfma_f32_16x16x32_bf16 v[92:95], v[166:169], v[216:219], v[92:95]
	v_mfma_f32_16x16x32_bf16 v[80:83], v[158:161], v[224:227], v[80:83]
	v_mfma_f32_16x16x32_bf16 v[76:79], v[166:169], v[224:227], v[76:79]
	v_mfma_f32_16x16x32_bf16 v[120:123], v[170:173], v[186:189], v[120:123]
	v_mfma_f32_16x16x32_bf16 v[116:119], v[178:181], v[186:189], v[116:119]
	v_mfma_f32_16x16x32_bf16 v[104:107], v[170:173], v[204:207], v[104:107]
	v_mfma_f32_16x16x32_bf16 v[100:103], v[178:181], v[204:207], v[100:103]
	v_mfma_f32_16x16x32_bf16 v[88:91], v[170:173], v[212:215], v[88:91]
	v_mfma_f32_16x16x32_bf16 v[84:87], v[178:181], v[212:215], v[84:87]
	v_mfma_f32_16x16x32_bf16 v[72:75], v[170:173], v[220:223], v[72:75]
	v_mfma_f32_16x16x32_bf16 v[68:71], v[178:181], v[220:223], v[68:71]
	v_mfma_f32_16x16x32_bf16 v[120:123], v[174:177], v[190:193], v[120:123]
	v_mfma_f32_16x16x32_bf16 v[116:119], v[182:185], v[190:193], v[116:119]
	v_mfma_f32_16x16x32_bf16 v[104:107], v[174:177], v[208:211], v[104:107]
	v_mfma_f32_16x16x32_bf16 v[100:103], v[182:185], v[208:211], v[100:103]
	v_mfma_f32_16x16x32_bf16 v[88:91], v[174:177], v[216:219], v[88:91]
	v_mfma_f32_16x16x32_bf16 v[84:87], v[182:185], v[216:219], v[84:87]
	v_mfma_f32_16x16x32_bf16 v[72:75], v[174:177], v[224:227], v[72:75]
	v_mfma_f32_16x16x32_bf16 v[68:71], v[182:185], v[224:227], v[68:71]
	s_setprio 0
	s_barrier
	s_add_i32 s81, s83, s16
	s_mov_b32 m0, s81
	ds_read_b128 v[186:189], v153 offset:16384
	ds_read_b128 v[190:193], v153 offset:17408
	ds_read_b128 v[204:207], v153 offset:18432
	ds_read_b128 v[208:211], v153 offset:19456
	ds_read_b128 v[212:215], v153 offset:20480
	ds_read_b128 v[216:219], v153 offset:21504
	ds_read_b128 v[220:223], v153 offset:22528
	ds_read_b128 v[224:227], v153 offset:23552
	global_load_lds_dwordx4 v136, s[60:61]
	s_add_i32 m0, s81, 0x2000
	s_add_u32 s82, s60, 0x40000
	s_addc_u32 s83, s61, 0
	s_add_i32 s81, s84, s16
	global_load_lds_dwordx4 v132, s[60:61]
	s_mov_b32 m0, s81
	s_nop 0
	global_load_lds_dwordx4 v136, s[82:83]
	s_add_i32 m0, s81, 0x2000
	s_nop 0
	global_load_lds_dwordx4 v132, s[82:83]
	s_mov_b32 m0, s17
	s_nop 0
	global_load_lds_dwordx4 v138, s[4:5]
	s_mov_b32 m0, s46
	s_nop 0
	global_load_lds_dwordx4 v134, s[4:5]
	s_waitcnt vmcnt(8)
	s_waitcnt lgkmcnt(0)
	s_barrier
	s_setprio 1
	v_mfma_f32_16x16x32_bf16 v[64:67], v[154:157], v[186:189], v[64:67]
	v_mfma_f32_16x16x32_bf16 v[60:63], v[162:165], v[186:189], v[60:63]
	v_mfma_f32_16x16x32_bf16 v[48:51], v[154:157], v[204:207], v[48:51]
	v_mfma_f32_16x16x32_bf16 v[44:47], v[162:165], v[204:207], v[44:47]
	v_mfma_f32_16x16x32_bf16 v[32:35], v[154:157], v[212:215], v[32:35]
	v_mfma_f32_16x16x32_bf16 v[28:31], v[162:165], v[212:215], v[28:31]
	v_mfma_f32_16x16x32_bf16 v[16:19], v[154:157], v[220:223], v[16:19]
	v_mfma_f32_16x16x32_bf16 v[12:15], v[162:165], v[220:223], v[12:15]
	v_mfma_f32_16x16x32_bf16 v[64:67], v[158:161], v[190:193], v[64:67]
	v_mfma_f32_16x16x32_bf16 v[60:63], v[166:169], v[190:193], v[60:63]
	v_mfma_f32_16x16x32_bf16 v[48:51], v[158:161], v[208:211], v[48:51]
	v_mfma_f32_16x16x32_bf16 v[44:47], v[166:169], v[208:211], v[44:47]
	v_mfma_f32_16x16x32_bf16 v[32:35], v[158:161], v[216:219], v[32:35]
	v_mfma_f32_16x16x32_bf16 v[28:31], v[166:169], v[216:219], v[28:31]
	v_mfma_f32_16x16x32_bf16 v[16:19], v[158:161], v[224:227], v[16:19]
	v_mfma_f32_16x16x32_bf16 v[12:15], v[166:169], v[224:227], v[12:15]
	v_mfma_f32_16x16x32_bf16 v[56:59], v[170:173], v[186:189], v[56:59]
	v_mfma_f32_16x16x32_bf16 v[52:55], v[178:181], v[186:189], v[52:55]
	v_mfma_f32_16x16x32_bf16 v[40:43], v[170:173], v[204:207], v[40:43]
	v_mfma_f32_16x16x32_bf16 v[36:39], v[178:181], v[204:207], v[36:39]
	v_mfma_f32_16x16x32_bf16 v[24:27], v[170:173], v[212:215], v[24:27]
	v_mfma_f32_16x16x32_bf16 v[20:23], v[178:181], v[212:215], v[20:23]
	v_mfma_f32_16x16x32_bf16 v[8:11], v[170:173], v[220:223], v[8:11]
	v_mfma_f32_16x16x32_bf16 v[4:7], v[178:181], v[220:223], v[4:7]
	v_mfma_f32_16x16x32_bf16 v[56:59], v[174:177], v[190:193], v[56:59]
	v_mfma_f32_16x16x32_bf16 v[52:55], v[182:185], v[190:193], v[52:55]
	v_mfma_f32_16x16x32_bf16 v[40:43], v[174:177], v[208:211], v[40:43]
	v_mfma_f32_16x16x32_bf16 v[36:39], v[182:185], v[208:211], v[36:39]
	v_mfma_f32_16x16x32_bf16 v[24:27], v[174:177], v[216:219], v[24:27]
	v_mfma_f32_16x16x32_bf16 v[20:23], v[182:185], v[216:219], v[20:23]
	v_mfma_f32_16x16x32_bf16 v[8:11], v[174:177], v[224:227], v[8:11]
	v_mfma_f32_16x16x32_bf16 v[4:7], v[182:185], v[224:227], v[4:7]
	s_setprio 0
	s_barrier
	s_add_i32 s81, 0, 0x18000
	v_add_u32_e32 v2, s81, v151
	s_add_i32 s82, 0, 0x1c000
	ds_read_b128 v[154:157], v2
	ds_read_b128 v[158:161], v2 offset:1024
	ds_read_b128 v[162:165], v2 offset:2048
	ds_read_b128 v[166:169], v2 offset:3072
	v_add_u32_e32 v2, s82, v151
	ds_read_b128 v[170:173], v2
	ds_read_b128 v[174:177], v2 offset:1024
	ds_read_b128 v[178:181], v2 offset:2048
	ds_read_b128 v[182:185], v2 offset:3072
	s_add_u32 s4, s4, 0x40000
	s_addc_u32 s5, s5, 0
	s_mov_b32 m0, s47
	ds_read_b128 v[186:189], v153 offset:32768
	ds_read_b128 v[190:193], v153 offset:33792
	ds_read_b128 v[204:207], v153 offset:34816
	ds_read_b128 v[208:211], v153 offset:35840
	ds_read_b128 v[212:215], v153 offset:36864
	ds_read_b128 v[216:219], v153 offset:37888
	ds_read_b128 v[220:223], v153 offset:38912
	ds_read_b128 v[224:227], v153 offset:39936
	global_load_lds_dwordx4 v138, s[4:5]
	s_mov_b32 m0, s58
	s_nop 0
	global_load_lds_dwordx4 v134, s[4:5]
	s_waitcnt vmcnt(8)
	s_waitcnt lgkmcnt(0)
	s_barrier
	s_setprio 1
	v_mfma_f32_16x16x32_bf16 v[128:131], v[154:157], v[186:189], v[128:131]
	v_mfma_f32_16x16x32_bf16 v[124:127], v[162:165], v[186:189], v[124:127]
	v_mfma_f32_16x16x32_bf16 v[112:115], v[154:157], v[204:207], v[112:115]
	v_mfma_f32_16x16x32_bf16 v[108:111], v[162:165], v[204:207], v[108:111]
	v_mfma_f32_16x16x32_bf16 v[96:99], v[154:157], v[212:215], v[96:99]
	v_mfma_f32_16x16x32_bf16 v[92:95], v[162:165], v[212:215], v[92:95]
	v_mfma_f32_16x16x32_bf16 v[80:83], v[154:157], v[220:223], v[80:83]
	v_mfma_f32_16x16x32_bf16 v[76:79], v[162:165], v[220:223], v[76:79]
	v_mfma_f32_16x16x32_bf16 v[128:131], v[158:161], v[190:193], v[128:131]
	v_mfma_f32_16x16x32_bf16 v[124:127], v[166:169], v[190:193], v[124:127]
	v_mfma_f32_16x16x32_bf16 v[112:115], v[158:161], v[208:211], v[112:115]
	v_mfma_f32_16x16x32_bf16 v[108:111], v[166:169], v[208:211], v[108:111]
	v_mfma_f32_16x16x32_bf16 v[96:99], v[158:161], v[216:219], v[96:99]
	v_mfma_f32_16x16x32_bf16 v[92:95], v[166:169], v[216:219], v[92:95]
	v_mfma_f32_16x16x32_bf16 v[80:83], v[158:161], v[224:227], v[80:83]
	v_mfma_f32_16x16x32_bf16 v[76:79], v[166:169], v[224:227], v[76:79]
	v_mfma_f32_16x16x32_bf16 v[120:123], v[170:173], v[186:189], v[120:123]
	v_mfma_f32_16x16x32_bf16 v[116:119], v[178:181], v[186:189], v[116:119]
	v_mfma_f32_16x16x32_bf16 v[104:107], v[170:173], v[204:207], v[104:107]
	v_mfma_f32_16x16x32_bf16 v[100:103], v[178:181], v[204:207], v[100:103]
	v_mfma_f32_16x16x32_bf16 v[88:91], v[170:173], v[212:215], v[88:91]
	v_mfma_f32_16x16x32_bf16 v[84:87], v[178:181], v[212:215], v[84:87]
	v_mfma_f32_16x16x32_bf16 v[72:75], v[170:173], v[220:223], v[72:75]
	v_mfma_f32_16x16x32_bf16 v[68:71], v[178:181], v[220:223], v[68:71]
	v_mfma_f32_16x16x32_bf16 v[120:123], v[174:177], v[190:193], v[120:123]
	v_mfma_f32_16x16x32_bf16 v[116:119], v[182:185], v[190:193], v[116:119]
	v_mfma_f32_16x16x32_bf16 v[104:107], v[174:177], v[208:211], v[104:107]
	v_mfma_f32_16x16x32_bf16 v[100:103], v[182:185], v[208:211], v[100:103]
	v_mfma_f32_16x16x32_bf16 v[88:91], v[174:177], v[216:219], v[88:91]
	v_mfma_f32_16x16x32_bf16 v[84:87], v[182:185], v[216:219], v[84:87]
	v_mfma_f32_16x16x32_bf16 v[72:75], v[174:177], v[224:227], v[72:75]
	v_mfma_f32_16x16x32_bf16 v[68:71], v[182:185], v[224:227], v[68:71]
	s_setprio 0
	s_barrier
	s_add_i32 s4, s81, s16
	s_add_u32 s98, s60, 0x80
	s_addc_u32 s99, s61, 0
	s_mov_b32 m0, s4
	ds_read_b128 v[186:189], v153 offset:49152
	ds_read_b128 v[190:193], v153 offset:50176
	ds_read_b128 v[204:207], v153 offset:51200
	ds_read_b128 v[208:211], v153 offset:52224
	ds_read_b128 v[212:215], v153 offset:53248
	ds_read_b128 v[216:219], v153 offset:54272
	ds_read_b128 v[220:223], v153 offset:55296
	ds_read_b128 v[224:227], v153 offset:56320
	global_load_lds_dwordx4 v136, s[98:99]
	s_add_i32 m0, s4, 0x2000
	s_add_u32 s4, s60, 0x40080
	s_addc_u32 s5, s61, 0
	s_add_i32 s60, s82, s16
	global_load_lds_dwordx4 v132, s[98:99]
	s_mov_b32 m0, s60
	s_nop 0
	global_load_lds_dwordx4 v136, s[4:5]
	s_add_i32 m0, s60, 0x2000
	s_nop 0
	global_load_lds_dwordx4 v132, s[4:5]
	s_mov_b32 m0, s74
	s_nop 0
	global_load_lds_dwordx4 v138, s[12:13]
	s_mov_b32 m0, s75
	s_nop 0
	global_load_lds_dwordx4 v134, s[12:13]
	s_waitcnt vmcnt(8)
	s_waitcnt lgkmcnt(0)
	s_barrier
	s_setprio 1
	v_mfma_f32_16x16x32_bf16 v[64:67], v[154:157], v[186:189], v[64:67]
	v_mfma_f32_16x16x32_bf16 v[60:63], v[162:165], v[186:189], v[60:63]
	v_mfma_f32_16x16x32_bf16 v[48:51], v[154:157], v[204:207], v[48:51]
	v_mfma_f32_16x16x32_bf16 v[44:47], v[162:165], v[204:207], v[44:47]
	v_mfma_f32_16x16x32_bf16 v[32:35], v[154:157], v[212:215], v[32:35]
	v_mfma_f32_16x16x32_bf16 v[28:31], v[162:165], v[212:215], v[28:31]
	v_mfma_f32_16x16x32_bf16 v[16:19], v[154:157], v[220:223], v[16:19]
	v_mfma_f32_16x16x32_bf16 v[12:15], v[162:165], v[220:223], v[12:15]
	v_mfma_f32_16x16x32_bf16 v[64:67], v[158:161], v[190:193], v[64:67]
	v_mfma_f32_16x16x32_bf16 v[60:63], v[166:169], v[190:193], v[60:63]
	v_mfma_f32_16x16x32_bf16 v[48:51], v[158:161], v[208:211], v[48:51]
	v_mfma_f32_16x16x32_bf16 v[44:47], v[166:169], v[208:211], v[44:47]
	v_mfma_f32_16x16x32_bf16 v[32:35], v[158:161], v[216:219], v[32:35]
	v_mfma_f32_16x16x32_bf16 v[28:31], v[166:169], v[216:219], v[28:31]
	v_mfma_f32_16x16x32_bf16 v[16:19], v[158:161], v[224:227], v[16:19]
	v_mfma_f32_16x16x32_bf16 v[12:15], v[166:169], v[224:227], v[12:15]
	v_mfma_f32_16x16x32_bf16 v[56:59], v[170:173], v[186:189], v[56:59]
	v_mfma_f32_16x16x32_bf16 v[52:55], v[178:181], v[186:189], v[52:55]
	v_mfma_f32_16x16x32_bf16 v[40:43], v[170:173], v[204:207], v[40:43]
	v_mfma_f32_16x16x32_bf16 v[36:39], v[178:181], v[204:207], v[36:39]
	v_mfma_f32_16x16x32_bf16 v[24:27], v[170:173], v[212:215], v[24:27]
	v_mfma_f32_16x16x32_bf16 v[20:23], v[178:181], v[212:215], v[20:23]
	v_mfma_f32_16x16x32_bf16 v[8:11], v[170:173], v[220:223], v[8:11]
	v_mfma_f32_16x16x32_bf16 v[4:7], v[178:181], v[220:223], v[4:7]
	v_mfma_f32_16x16x32_bf16 v[56:59], v[174:177], v[190:193], v[56:59]
	v_mfma_f32_16x16x32_bf16 v[52:55], v[182:185], v[190:193], v[52:55]
	v_mfma_f32_16x16x32_bf16 v[40:43], v[174:177], v[208:211], v[40:43]
	v_mfma_f32_16x16x32_bf16 v[36:39], v[182:185], v[208:211], v[36:39]
	v_mfma_f32_16x16x32_bf16 v[24:27], v[174:177], v[216:219], v[24:27]
	v_mfma_f32_16x16x32_bf16 v[20:23], v[182:185], v[216:219], v[20:23]
	v_mfma_f32_16x16x32_bf16 v[8:11], v[174:177], v[224:227], v[8:11]
	v_mfma_f32_16x16x32_bf16 v[4:7], v[182:185], v[224:227], v[4:7]
	s_setprio 0
	s_barrier
	s_add_i32 s80, s80, 2
	s_add_u32 s42, s42, 0x100
	s_addc_u32 s43, s43, 0
	s_cmp_gt_u32 s80, 13
	s_cbranch_scc0 .LBB0_211
	s_and_b64 vcc, exec, s[22:23]
	s_cbranch_vccz .LBB0_214
	s_barrier

.LBB0_288:
	s_ashr_i32 s41, s40, 31
	s_lshl_b64 s[4:5], s[40:41], 19
	s_add_u32 s42, s6, s4
	s_addc_u32 s43, s7, s5
	s_and_b64 s[4:5], s[22:23], exec
	s_cselect_b32 s41, s43, s37
	s_cselect_b32 s61, s42, s36
	s_ashr_i32 s39, s38, 31
	s_lshl_b64 s[4:5], s[38:39], 19
	s_add_u32 s44, s8, s4
	s_addc_u32 s45, s9, s5
	s_and_b64 s[4:5], s[22:23], exec
	s_cselect_b32 s39, s45, s49
	s_cselect_b32 s62, s44, s48
	s_add_u32 s63, s61, 0x80
	s_addc_u32 s64, s41, 0
	s_add_u32 s4, s36, 0x40080
	s_addc_u32 s5, s37, 0
	s_add_u32 s65, s48, 0x100
	v_lshl_add_u64 v[142:143], s[4:5], 0, v[138:139]
	v_lshl_add_u64 v[144:145], s[4:5], 0, v[140:141]
	s_addc_u32 s68, s49, 0
	s_mov_b32 s69, -2
	s_mov_b64 s[48:49], 0
	s_add_u32 s4, s36, s48
	s_addc_u32 s5, s37, s49
	s_add_u32 s98, s4, 0x40080
	s_addc_u32 s99, s5, 0
	s_add_u32 s70, s4, 0x100
	s_addc_u32 s71, s5, 0
	s_add_u32 s50, s65, s48
	s_addc_u32 s51, s68, s49
	s_add_u32 s4, s4, 0x180
	s_addc_u32 s5, s5, 0
	s_add_i32 s72, 0, 0x10000
	s_add_i32 s73, 0, 0x14000
	v_add_u32_e32 v160, s72, v146
	s_waitcnt vmcnt(0)
	v_add_u32_e32 v176, s73, v146
	ds_read_b128 v[148:151], v160
	ds_read_b128 v[152:155], v160 offset:1024
	ds_read_b128 v[156:159], v160 offset:2048
	ds_read_b128 v[160:163], v160 offset:3072
	ds_read_b128 v[164:167], v176
	ds_read_b128 v[168:171], v176 offset:1024
	ds_read_b128 v[172:175], v176 offset:2048
	ds_read_b128 v[176:179], v176 offset:3072
	s_cmpk_eq_i32 s48, 0x700
	s_cselect_b32 s13, s64, s5
	s_cselect_b32 s12, s63, s4
	s_cselect_b32 s51, s39, s51
	s_cselect_b32 s50, s62, s50
	s_cselect_b32 s5, s41, s71
	s_cselect_b32 s4, s61, s70
	s_add_i32 m0, s17, 0xc000
	ds_read_b128 v[180:183], v147
	ds_read_b128 v[184:187], v147 offset:1024
	ds_read_b128 v[188:191], v147 offset:2048
	ds_read_b128 v[192:195], v147 offset:3072
	ds_read_b128 v[204:207], v147 offset:4096
	ds_read_b128 v[208:211], v147 offset:5120
	ds_read_b128 v[212:215], v147 offset:6144
	ds_read_b128 v[216:219], v147 offset:7168
	global_load_lds_dwordx4 v138, s[98:99]
	s_add_i32 m0, s17, 0xe000
	s_nop 0
	global_load_lds_dwordx4 v140, s[98:99]
	s_waitcnt vmcnt(8)
	s_waitcnt lgkmcnt(0)
	s_barrier
	s_setprio 1
	v_mfma_f32_16x16x32_bf16 v[128:131], v[148:151], v[180:183], 0
	v_mfma_f32_16x16x32_bf16 v[124:127], v[156:159], v[180:183], 0
	v_mfma_f32_16x16x32_bf16 v[120:123], v[148:151], v[188:191], 0
	v_mfma_f32_16x16x32_bf16 v[116:119], v[156:159], v[188:191], 0
	v_mfma_f32_16x16x32_bf16 v[104:107], v[148:151], v[204:207], 0
	v_mfma_f32_16x16x32_bf16 v[100:103], v[156:159], v[204:207], 0
	v_mfma_f32_16x16x32_bf16 v[88:91], v[148:151], v[212:215], 0
	v_mfma_f32_16x16x32_bf16 v[84:87], v[156:159], v[212:215], 0
	v_mfma_f32_16x16x32_bf16 v[128:131], v[152:155], v[184:187], v[128:131]
	v_mfma_f32_16x16x32_bf16 v[124:127], v[160:163], v[184:187], v[124:127]
	v_mfma_f32_16x16x32_bf16 v[120:123], v[152:155], v[192:195], v[120:123]
	v_mfma_f32_16x16x32_bf16 v[116:119], v[160:163], v[192:195], v[116:119]
	v_mfma_f32_16x16x32_bf16 v[104:107], v[152:155], v[208:211], v[104:107]
	v_mfma_f32_16x16x32_bf16 v[100:103], v[160:163], v[208:211], v[100:103]
	v_mfma_f32_16x16x32_bf16 v[88:91], v[152:155], v[216:219], v[88:91]
	v_mfma_f32_16x16x32_bf16 v[84:87], v[160:163], v[216:219], v[84:87]
	v_mfma_f32_16x16x32_bf16 v[112:115], v[164:167], v[180:183], 0
	v_mfma_f32_16x16x32_bf16 v[108:111], v[172:175], v[180:183], 0
	v_mfma_f32_16x16x32_bf16 v[96:99], v[164:167], v[188:191], 0
	v_mfma_f32_16x16x32_bf16 v[92:95], v[172:175], v[188:191], 0
	v_mfma_f32_16x16x32_bf16 v[80:83], v[164:167], v[204:207], 0
	v_mfma_f32_16x16x32_bf16 v[76:79], v[172:175], v[204:207], 0
	v_mfma_f32_16x16x32_bf16 v[72:75], v[164:167], v[212:215], 0
	v_mfma_f32_16x16x32_bf16 v[68:71], v[172:175], v[212:215], 0
	v_mfma_f32_16x16x32_bf16 v[112:115], v[168:171], v[184:187], v[112:115]
	v_mfma_f32_16x16x32_bf16 v[108:111], v[176:179], v[184:187], v[108:111]
	v_mfma_f32_16x16x32_bf16 v[96:99], v[168:171], v[192:195], v[96:99]
	v_mfma_f32_16x16x32_bf16 v[92:95], v[176:179], v[192:195], v[92:95]
	v_mfma_f32_16x16x32_bf16 v[80:83], v[168:171], v[208:211], v[80:83]
	v_mfma_f32_16x16x32_bf16 v[76:79], v[176:179], v[208:211], v[76:79]
	v_mfma_f32_16x16x32_bf16 v[72:75], v[168:171], v[216:219], v[72:75]
	v_mfma_f32_16x16x32_bf16 v[68:71], v[176:179], v[216:219], v[68:71]
	s_setprio 0
	s_barrier
	s_add_i32 s70, s72, s16
	s_mov_b32 m0, s70
	ds_read_b128 v[180:183], v147 offset:16384
	ds_read_b128 v[184:187], v147 offset:17408
	ds_read_b128 v[188:191], v147 offset:18432
	ds_read_b128 v[192:195], v147 offset:19456
	ds_read_b128 v[204:207], v147 offset:20480
	ds_read_b128 v[208:211], v147 offset:21504
	ds_read_b128 v[212:215], v147 offset:22528
	ds_read_b128 v[216:219], v147 offset:23552
	global_load_lds_dwordx4 v2, s[50:51]
	s_add_i32 m0, s70, 0x2000
	s_add_u32 s70, s50, 0x40000
	s_addc_u32 s71, s51, 0
	s_add_i32 s72, s73, s16
	global_load_lds_dwordx4 v136, s[50:51]
	s_mov_b32 m0, s72
	s_nop 0
	global_load_lds_dwordx4 v2, s[70:71]
	s_add_i32 m0, s72, 0x2000
	s_nop 0
	global_load_lds_dwordx4 v136, s[70:71]
	s_mov_b32 m0, s17
	s_nop 0
	global_load_lds_dwordx4 v132, s[4:5]
	s_mov_b32 m0, s21
	s_nop 0
	global_load_lds_dwordx4 v134, s[4:5]
	s_waitcnt vmcnt(8)
	s_waitcnt lgkmcnt(0)
	s_barrier
	s_setprio 1
	v_mfma_f32_16x16x32_bf16 v[64:67], v[148:151], v[180:183], 0
	v_mfma_f32_16x16x32_bf16 v[60:63], v[156:159], v[180:183], 0
	v_mfma_f32_16x16x32_bf16 v[56:59], v[148:151], v[188:191], 0
	v_mfma_f32_16x16x32_bf16 v[52:55], v[156:159], v[188:191], 0
	v_mfma_f32_16x16x32_bf16 v[40:43], v[148:151], v[204:207], 0
	v_mfma_f32_16x16x32_bf16 v[36:39], v[156:159], v[204:207], 0
	v_mfma_f32_16x16x32_bf16 v[24:27], v[148:151], v[212:215], 0
	v_mfma_f32_16x16x32_bf16 v[20:23], v[156:159], v[212:215], 0
	v_mfma_f32_16x16x32_bf16 v[64:67], v[152:155], v[184:187], v[64:67]
	v_mfma_f32_16x16x32_bf16 v[60:63], v[160:163], v[184:187], v[60:63]
	v_mfma_f32_16x16x32_bf16 v[56:59], v[152:155], v[192:195], v[56:59]
	v_mfma_f32_16x16x32_bf16 v[52:55], v[160:163], v[192:195], v[52:55]
	v_mfma_f32_16x16x32_bf16 v[40:43], v[152:155], v[208:211], v[40:43]
	v_mfma_f32_16x16x32_bf16 v[36:39], v[160:163], v[208:211], v[36:39]
	v_mfma_f32_16x16x32_bf16 v[24:27], v[152:155], v[216:219], v[24:27]
	v_mfma_f32_16x16x32_bf16 v[20:23], v[160:163], v[216:219], v[20:23]
	v_mfma_f32_16x16x32_bf16 v[48:51], v[164:167], v[180:183], 0
	v_mfma_f32_16x16x32_bf16 v[44:47], v[172:175], v[180:183], 0
	v_mfma_f32_16x16x32_bf16 v[32:35], v[164:167], v[188:191], 0
	v_mfma_f32_16x16x32_bf16 v[28:31], v[172:175], v[188:191], 0
	v_mfma_f32_16x16x32_bf16 v[16:19], v[164:167], v[204:207], 0
	v_mfma_f32_16x16x32_bf16 v[12:15], v[172:175], v[204:207], 0
	v_mfma_f32_16x16x32_bf16 v[8:11], v[164:167], v[212:215], 0
	v_mfma_f32_16x16x32_bf16 v[4:7], v[172:175], v[212:215], 0
	v_mfma_f32_16x16x32_bf16 v[48:51], v[168:171], v[184:187], v[48:51]
	v_mfma_f32_16x16x32_bf16 v[44:47], v[176:179], v[184:187], v[44:47]
	v_mfma_f32_16x16x32_bf16 v[32:35], v[168:171], v[192:195], v[32:35]
	v_mfma_f32_16x16x32_bf16 v[28:31], v[176:179], v[192:195], v[28:31]
	v_mfma_f32_16x16x32_bf16 v[16:19], v[168:171], v[208:211], v[16:19]
	v_mfma_f32_16x16x32_bf16 v[12:15], v[176:179], v[208:211], v[12:15]
	v_mfma_f32_16x16x32_bf16 v[8:11], v[168:171], v[216:219], v[8:11]
	v_mfma_f32_16x16x32_bf16 v[4:7], v[176:179], v[216:219], v[4:7]
	s_setprio 0
	s_barrier
	s_add_i32 s70, 0, 0x18000
	s_add_i32 s71, 0, 0x1c000
	v_add_u32_e32 v160, s70, v146
	v_add_u32_e32 v176, s71, v146
	ds_read_b128 v[148:151], v160
	ds_read_b128 v[152:155], v160 offset:1024
	ds_read_b128 v[156:159], v160 offset:2048
	ds_read_b128 v[160:163], v160 offset:3072
	ds_read_b128 v[164:167], v176
	ds_read_b128 v[168:171], v176 offset:1024
	ds_read_b128 v[172:175], v176 offset:2048
	ds_read_b128 v[176:179], v176 offset:3072
	s_add_u32 s4, s4, 0x40000
	s_addc_u32 s5, s5, 0
	s_mov_b32 m0, s46
	ds_read_b128 v[180:183], v147 offset:32768
	ds_read_b128 v[184:187], v147 offset:33792
	ds_read_b128 v[188:191], v147 offset:34816
	ds_read_b128 v[192:195], v147 offset:35840
	ds_read_b128 v[204:207], v147 offset:36864
	ds_read_b128 v[208:211], v147 offset:37888
	ds_read_b128 v[212:215], v147 offset:38912
	ds_read_b128 v[216:219], v147 offset:39936
	global_load_lds_dwordx4 v132, s[4:5]
	s_mov_b32 m0, s47
	s_nop 0
	global_load_lds_dwordx4 v134, s[4:5]
	s_waitcnt vmcnt(8)
	s_waitcnt lgkmcnt(0)
	s_barrier
	s_setprio 1
	v_mfma_f32_16x16x32_bf16 v[128:131], v[148:151], v[180:183], v[128:131]
	v_mfma_f32_16x16x32_bf16 v[124:127], v[156:159], v[180:183], v[124:127]
	v_mfma_f32_16x16x32_bf16 v[120:123], v[148:151], v[188:191], v[120:123]
	v_mfma_f32_16x16x32_bf16 v[116:119], v[156:159], v[188:191], v[116:119]
	v_mfma_f32_16x16x32_bf16 v[104:107], v[148:151], v[204:207], v[104:107]
	v_mfma_f32_16x16x32_bf16 v[100:103], v[156:159], v[204:207], v[100:103]
	v_mfma_f32_16x16x32_bf16 v[88:91], v[148:151], v[212:215], v[88:91]
	v_mfma_f32_16x16x32_bf16 v[84:87], v[156:159], v[212:215], v[84:87]
	v_mfma_f32_16x16x32_bf16 v[128:131], v[152:155], v[184:187], v[128:131]
	v_mfma_f32_16x16x32_bf16 v[124:127], v[160:163], v[184:187], v[124:127]
	v_mfma_f32_16x16x32_bf16 v[120:123], v[152:155], v[192:195], v[120:123]
	v_mfma_f32_16x16x32_bf16 v[116:119], v[160:163], v[192:195], v[116:119]
	v_mfma_f32_16x16x32_bf16 v[104:107], v[152:155], v[208:211], v[104:107]
	v_mfma_f32_16x16x32_bf16 v[100:103], v[160:163], v[208:211], v[100:103]
	v_mfma_f32_16x16x32_bf16 v[88:91], v[152:155], v[216:219], v[88:91]
	v_mfma_f32_16x16x32_bf16 v[84:87], v[160:163], v[216:219], v[84:87]
	v_mfma_f32_16x16x32_bf16 v[112:115], v[164:167], v[180:183], v[112:115]
	v_mfma_f32_16x16x32_bf16 v[108:111], v[172:175], v[180:183], v[108:111]
	v_mfma_f32_16x16x32_bf16 v[96:99], v[164:167], v[188:191], v[96:99]
	v_mfma_f32_16x16x32_bf16 v[92:95], v[172:175], v[188:191], v[92:95]
	v_mfma_f32_16x16x32_bf16 v[80:83], v[164:167], v[204:207], v[80:83]
	v_mfma_f32_16x16x32_bf16 v[76:79], v[172:175], v[204:207], v[76:79]
	v_mfma_f32_16x16x32_bf16 v[72:75], v[164:167], v[212:215], v[72:75]
	v_mfma_f32_16x16x32_bf16 v[68:71], v[172:175], v[212:215], v[68:71]
	v_mfma_f32_16x16x32_bf16 v[112:115], v[168:171], v[184:187], v[112:115]
	v_mfma_f32_16x16x32_bf16 v[108:111], v[176:179], v[184:187], v[108:111]
	v_mfma_f32_16x16x32_bf16 v[96:99], v[168:171], v[192:195], v[96:99]
	v_mfma_f32_16x16x32_bf16 v[92:95], v[176:179], v[192:195], v[92:95]
	v_mfma_f32_16x16x32_bf16 v[80:83], v[168:171], v[208:211], v[80:83]
	v_mfma_f32_16x16x32_bf16 v[76:79], v[176:179], v[208:211], v[76:79]
	v_mfma_f32_16x16x32_bf16 v[72:75], v[168:171], v[216:219], v[72:75]
	v_mfma_f32_16x16x32_bf16 v[68:71], v[176:179], v[216:219], v[68:71]
	s_setprio 0
	s_barrier
	s_add_i32 s4, s70, s16
	s_add_u32 s98, s50, 0x80
	s_addc_u32 s99, s51, 0
	s_mov_b32 m0, s4
	ds_read_b128 v[180:183], v147 offset:49152
	ds_read_b128 v[184:187], v147 offset:50176
	ds_read_b128 v[188:191], v147 offset:51200
	ds_read_b128 v[192:195], v147 offset:52224
	ds_read_b128 v[204:207], v147 offset:53248
	ds_read_b128 v[208:211], v147 offset:54272
	ds_read_b128 v[212:215], v147 offset:55296
	ds_read_b128 v[216:219], v147 offset:56320
	global_load_lds_dwordx4 v2, s[98:99]
	s_add_i32 m0, s4, 0x2000
	s_add_u32 s4, s50, 0x40080
	s_addc_u32 s5, s51, 0
	s_add_i32 s50, s71, s16
	global_load_lds_dwordx4 v136, s[98:99]
	s_mov_b32 m0, s50
	s_nop 0
	global_load_lds_dwordx4 v2, s[4:5]
	s_add_i32 m0, s50, 0x2000
	s_nop 0
	global_load_lds_dwordx4 v136, s[4:5]
	s_mov_b32 m0, s56
	s_nop 0
	global_load_lds_dwordx4 v132, s[12:13]
	s_mov_b32 m0, s58
	s_nop 0
	global_load_lds_dwordx4 v134, s[12:13]
	s_waitcnt vmcnt(8)
	s_waitcnt lgkmcnt(0)
	s_barrier
	s_setprio 1
	v_mfma_f32_16x16x32_bf16 v[64:67], v[148:151], v[180:183], v[64:67]
	v_mfma_f32_16x16x32_bf16 v[60:63], v[156:159], v[180:183], v[60:63]
	v_mfma_f32_16x16x32_bf16 v[56:59], v[148:151], v[188:191], v[56:59]
	v_mfma_f32_16x16x32_bf16 v[52:55], v[156:159], v[188:191], v[52:55]
	v_mfma_f32_16x16x32_bf16 v[40:43], v[148:151], v[204:207], v[40:43]
	v_mfma_f32_16x16x32_bf16 v[36:39], v[156:159], v[204:207], v[36:39]
	v_mfma_f32_16x16x32_bf16 v[24:27], v[148:151], v[212:215], v[24:27]
	v_mfma_f32_16x16x32_bf16 v[20:23], v[156:159], v[212:215], v[20:23]
	v_mfma_f32_16x16x32_bf16 v[64:67], v[152:155], v[184:187], v[64:67]
	v_mfma_f32_16x16x32_bf16 v[60:63], v[160:163], v[184:187], v[60:63]
	v_mfma_f32_16x16x32_bf16 v[56:59], v[152:155], v[192:195], v[56:59]
	v_mfma_f32_16x16x32_bf16 v[52:55], v[160:163], v[192:195], v[52:55]
	v_mfma_f32_16x16x32_bf16 v[40:43], v[152:155], v[208:211], v[40:43]
	v_mfma_f32_16x16x32_bf16 v[36:39], v[160:163], v[208:211], v[36:39]
	v_mfma_f32_16x16x32_bf16 v[24:27], v[152:155], v[216:219], v[24:27]
	v_mfma_f32_16x16x32_bf16 v[20:23], v[160:163], v[216:219], v[20:23]
	v_mfma_f32_16x16x32_bf16 v[48:51], v[164:167], v[180:183], v[48:51]
	v_mfma_f32_16x16x32_bf16 v[44:47], v[172:175], v[180:183], v[44:47]
	v_mfma_f32_16x16x32_bf16 v[32:35], v[164:167], v[188:191], v[32:35]
	v_mfma_f32_16x16x32_bf16 v[28:31], v[172:175], v[188:191], v[28:31]
	v_mfma_f32_16x16x32_bf16 v[16:19], v[164:167], v[204:207], v[16:19]
	v_mfma_f32_16x16x32_bf16 v[12:15], v[172:175], v[204:207], v[12:15]
	v_mfma_f32_16x16x32_bf16 v[8:11], v[164:167], v[212:215], v[8:11]
	v_mfma_f32_16x16x32_bf16 v[4:7], v[172:175], v[212:215], v[4:7]
	v_mfma_f32_16x16x32_bf16 v[48:51], v[168:171], v[184:187], v[48:51]
	v_mfma_f32_16x16x32_bf16 v[44:47], v[176:179], v[184:187], v[44:47]
	v_mfma_f32_16x16x32_bf16 v[32:35], v[168:171], v[192:195], v[32:35]
	v_mfma_f32_16x16x32_bf16 v[28:31], v[176:179], v[192:195], v[28:31]
	v_mfma_f32_16x16x32_bf16 v[16:19], v[168:171], v[208:211], v[16:19]
	v_mfma_f32_16x16x32_bf16 v[12:15], v[176:179], v[208:211], v[12:15]
	v_mfma_f32_16x16x32_bf16 v[8:11], v[168:171], v[216:219], v[8:11]
	v_mfma_f32_16x16x32_bf16 v[4:7], v[176:179], v[216:219], v[4:7]
	s_setprio 0
	s_barrier
	s_add_i32 s69, s69, 2
	s_add_u32 s48, s48, 0x100
	s_addc_u32 s49, s49, 0
	s_cmp_gt_u32 s69, 13
.LBB0_289:
	s_add_u32 s4, s36, s48
	s_addc_u32 s5, s37, s49
	s_add_u32 s98, s4, 0x40080
	s_addc_u32 s99, s5, 0
	s_add_u32 s70, s4, 0x100
	s_addc_u32 s71, s5, 0
	s_add_u32 s50, s65, s48
	s_addc_u32 s51, s68, s49
	s_add_u32 s4, s4, 0x180
	s_addc_u32 s5, s5, 0
	s_add_i32 s72, 0, 0x10000
	s_add_i32 s73, 0, 0x14000
	v_add_u32_e32 v160, s72, v146
	s_waitcnt vmcnt(0)
	v_add_u32_e32 v176, s73, v146
	ds_read_b128 v[148:151], v160
	ds_read_b128 v[152:155], v160 offset:1024
	ds_read_b128 v[156:159], v160 offset:2048
	ds_read_b128 v[160:163], v160 offset:3072
	ds_read_b128 v[164:167], v176
	ds_read_b128 v[168:171], v176 offset:1024
	ds_read_b128 v[172:175], v176 offset:2048
	ds_read_b128 v[176:179], v176 offset:3072
	s_cmpk_eq_i32 s48, 0x700
	s_cselect_b32 s13, s64, s5
	s_cselect_b32 s12, s63, s4
	s_cselect_b32 s51, s39, s51
	s_cselect_b32 s50, s62, s50
	s_cselect_b32 s5, s41, s71
	s_cselect_b32 s4, s61, s70
	s_add_i32 m0, s17, 0xc000
	ds_read_b128 v[180:183], v147
	ds_read_b128 v[184:187], v147 offset:1024
	ds_read_b128 v[188:191], v147 offset:2048
	ds_read_b128 v[192:195], v147 offset:3072
	ds_read_b128 v[204:207], v147 offset:4096
	ds_read_b128 v[208:211], v147 offset:5120
	ds_read_b128 v[212:215], v147 offset:6144
	ds_read_b128 v[216:219], v147 offset:7168
	global_load_lds_dwordx4 v138, s[98:99]
	s_add_i32 m0, s17, 0xe000
	s_nop 0
	global_load_lds_dwordx4 v140, s[98:99]
	s_waitcnt vmcnt(8)
	s_waitcnt lgkmcnt(0)
	s_barrier
	s_setprio 1
	v_mfma_f32_16x16x32_bf16 v[128:131], v[148:151], v[180:183], v[128:131]
	v_mfma_f32_16x16x32_bf16 v[124:127], v[156:159], v[180:183], v[124:127]
	v_mfma_f32_16x16x32_bf16 v[120:123], v[148:151], v[188:191], v[120:123]
	v_mfma_f32_16x16x32_bf16 v[116:119], v[156:159], v[188:191], v[116:119]
	v_mfma_f32_16x16x32_bf16 v[104:107], v[148:151], v[204:207], v[104:107]
	v_mfma_f32_16x16x32_bf16 v[100:103], v[156:159], v[204:207], v[100:103]
	v_mfma_f32_16x16x32_bf16 v[88:91], v[148:151], v[212:215], v[88:91]
	v_mfma_f32_16x16x32_bf16 v[84:87], v[156:159], v[212:215], v[84:87]
	v_mfma_f32_16x16x32_bf16 v[128:131], v[152:155], v[184:187], v[128:131]
	v_mfma_f32_16x16x32_bf16 v[124:127], v[160:163], v[184:187], v[124:127]
	v_mfma_f32_16x16x32_bf16 v[120:123], v[152:155], v[192:195], v[120:123]
	v_mfma_f32_16x16x32_bf16 v[116:119], v[160:163], v[192:195], v[116:119]
	v_mfma_f32_16x16x32_bf16 v[104:107], v[152:155], v[208:211], v[104:107]
	v_mfma_f32_16x16x32_bf16 v[100:103], v[160:163], v[208:211], v[100:103]
	v_mfma_f32_16x16x32_bf16 v[88:91], v[152:155], v[216:219], v[88:91]
	v_mfma_f32_16x16x32_bf16 v[84:87], v[160:163], v[216:219], v[84:87]
	v_mfma_f32_16x16x32_bf16 v[112:115], v[164:167], v[180:183], v[112:115]
	v_mfma_f32_16x16x32_bf16 v[108:111], v[172:175], v[180:183], v[108:111]
	v_mfma_f32_16x16x32_bf16 v[96:99], v[164:167], v[188:191], v[96:99]
	v_mfma_f32_16x16x32_bf16 v[92:95], v[172:175], v[188:191], v[92:95]
	v_mfma_f32_16x16x32_bf16 v[80:83], v[164:167], v[204:207], v[80:83]
	v_mfma_f32_16x16x32_bf16 v[76:79], v[172:175], v[204:207], v[76:79]
	v_mfma_f32_16x16x32_bf16 v[72:75], v[164:167], v[212:215], v[72:75]
	v_mfma_f32_16x16x32_bf16 v[68:71], v[172:175], v[212:215], v[68:71]
	v_mfma_f32_16x16x32_bf16 v[112:115], v[168:171], v[184:187], v[112:115]
	v_mfma_f32_16x16x32_bf16 v[108:111], v[176:179], v[184:187], v[108:111]
	v_mfma_f32_16x16x32_bf16 v[96:99], v[168:171], v[192:195], v[96:99]
	v_mfma_f32_16x16x32_bf16 v[92:95], v[176:179], v[192:195], v[92:95]
	v_mfma_f32_16x16x32_bf16 v[80:83], v[168:171], v[208:211], v[80:83]
	v_mfma_f32_16x16x32_bf16 v[76:79], v[176:179], v[208:211], v[76:79]
	v_mfma_f32_16x16x32_bf16 v[72:75], v[168:171], v[216:219], v[72:75]
	v_mfma_f32_16x16x32_bf16 v[68:71], v[176:179], v[216:219], v[68:71]
	s_setprio 0
	s_barrier
	s_add_i32 s70, s72, s16
	s_mov_b32 m0, s70
	ds_read_b128 v[180:183], v147 offset:16384
	ds_read_b128 v[184:187], v147 offset:17408
	ds_read_b128 v[188:191], v147 offset:18432
	ds_read_b128 v[192:195], v147 offset:19456
	ds_read_b128 v[204:207], v147 offset:20480
	ds_read_b128 v[208:211], v147 offset:21504
	ds_read_b128 v[212:215], v147 offset:22528
	ds_read_b128 v[216:219], v147 offset:23552
	global_load_lds_dwordx4 v2, s[50:51]
	s_add_i32 m0, s70, 0x2000
	s_add_u32 s70, s50, 0x40000
	s_addc_u32 s71, s51, 0
	s_add_i32 s72, s73, s16
	global_load_lds_dwordx4 v136, s[50:51]
	s_mov_b32 m0, s72
	s_nop 0
	global_load_lds_dwordx4 v2, s[70:71]
	s_add_i32 m0, s72, 0x2000
	s_nop 0
	global_load_lds_dwordx4 v136, s[70:71]
	s_mov_b32 m0, s17
	s_nop 0
	global_load_lds_dwordx4 v132, s[4:5]
	s_mov_b32 m0, s21
	s_nop 0
	global_load_lds_dwordx4 v134, s[4:5]
	s_waitcnt vmcnt(8)
	s_waitcnt lgkmcnt(0)
	s_barrier
	s_setprio 1
	v_mfma_f32_16x16x32_bf16 v[64:67], v[148:151], v[180:183], v[64:67]
	v_mfma_f32_16x16x32_bf16 v[60:63], v[156:159], v[180:183], v[60:63]
	v_mfma_f32_16x16x32_bf16 v[56:59], v[148:151], v[188:191], v[56:59]
	v_mfma_f32_16x16x32_bf16 v[52:55], v[156:159], v[188:191], v[52:55]
	v_mfma_f32_16x16x32_bf16 v[40:43], v[148:151], v[204:207], v[40:43]
	v_mfma_f32_16x16x32_bf16 v[36:39], v[156:159], v[204:207], v[36:39]
	v_mfma_f32_16x16x32_bf16 v[24:27], v[148:151], v[212:215], v[24:27]
	v_mfma_f32_16x16x32_bf16 v[20:23], v[156:159], v[212:215], v[20:23]
	v_mfma_f32_16x16x32_bf16 v[64:67], v[152:155], v[184:187], v[64:67]
	v_mfma_f32_16x16x32_bf16 v[60:63], v[160:163], v[184:187], v[60:63]
	v_mfma_f32_16x16x32_bf16 v[56:59], v[152:155], v[192:195], v[56:59]
	v_mfma_f32_16x16x32_bf16 v[52:55], v[160:163], v[192:195], v[52:55]
	v_mfma_f32_16x16x32_bf16 v[40:43], v[152:155], v[208:211], v[40:43]
	v_mfma_f32_16x16x32_bf16 v[36:39], v[160:163], v[208:211], v[36:39]
	v_mfma_f32_16x16x32_bf16 v[24:27], v[152:155], v[216:219], v[24:27]
	v_mfma_f32_16x16x32_bf16 v[20:23], v[160:163], v[216:219], v[20:23]
	v_mfma_f32_16x16x32_bf16 v[48:51], v[164:167], v[180:183], v[48:51]
	v_mfma_f32_16x16x32_bf16 v[44:47], v[172:175], v[180:183], v[44:47]
	v_mfma_f32_16x16x32_bf16 v[32:35], v[164:167], v[188:191], v[32:35]
	v_mfma_f32_16x16x32_bf16 v[28:31], v[172:175], v[188:191], v[28:31]
	v_mfma_f32_16x16x32_bf16 v[16:19], v[164:167], v[204:207], v[16:19]
	v_mfma_f32_16x16x32_bf16 v[12:15], v[172:175], v[204:207], v[12:15]
	v_mfma_f32_16x16x32_bf16 v[8:11], v[164:167], v[212:215], v[8:11]
	v_mfma_f32_16x16x32_bf16 v[4:7], v[172:175], v[212:215], v[4:7]
	v_mfma_f32_16x16x32_bf16 v[48:51], v[168:171], v[184:187], v[48:51]
	v_mfma_f32_16x16x32_bf16 v[44:47], v[176:179], v[184:187], v[44:47]
	v_mfma_f32_16x16x32_bf16 v[32:35], v[168:171], v[192:195], v[32:35]
	v_mfma_f32_16x16x32_bf16 v[28:31], v[176:179], v[192:195], v[28:31]
	v_mfma_f32_16x16x32_bf16 v[16:19], v[168:171], v[208:211], v[16:19]
	v_mfma_f32_16x16x32_bf16 v[12:15], v[176:179], v[208:211], v[12:15]
	v_mfma_f32_16x16x32_bf16 v[8:11], v[168:171], v[216:219], v[8:11]
	v_mfma_f32_16x16x32_bf16 v[4:7], v[176:179], v[216:219], v[4:7]
	s_setprio 0
	s_barrier
	s_add_i32 s70, 0, 0x18000
	s_add_i32 s71, 0, 0x1c000
	v_add_u32_e32 v160, s70, v146
	v_add_u32_e32 v176, s71, v146
	ds_read_b128 v[148:151], v160
	ds_read_b128 v[152:155], v160 offset:1024
	ds_read_b128 v[156:159], v160 offset:2048
	ds_read_b128 v[160:163], v160 offset:3072
	ds_read_b128 v[164:167], v176
	ds_read_b128 v[168:171], v176 offset:1024
	ds_read_b128 v[172:175], v176 offset:2048
	ds_read_b128 v[176:179], v176 offset:3072
	s_add_u32 s4, s4, 0x40000
	s_addc_u32 s5, s5, 0
	s_mov_b32 m0, s46
	ds_read_b128 v[180:183], v147 offset:32768
	ds_read_b128 v[184:187], v147 offset:33792
	ds_read_b128 v[188:191], v147 offset:34816
	ds_read_b128 v[192:195], v147 offset:35840
	ds_read_b128 v[204:207], v147 offset:36864
	ds_read_b128 v[208:211], v147 offset:37888
	ds_read_b128 v[212:215], v147 offset:38912
	ds_read_b128 v[216:219], v147 offset:39936
	global_load_lds_dwordx4 v132, s[4:5]
	s_mov_b32 m0, s47
	s_nop 0
	global_load_lds_dwordx4 v134, s[4:5]
	s_waitcnt vmcnt(8)
	s_waitcnt lgkmcnt(0)
	s_barrier
	s_setprio 1
	v_mfma_f32_16x16x32_bf16 v[128:131], v[148:151], v[180:183], v[128:131]
	v_mfma_f32_16x16x32_bf16 v[124:127], v[156:159], v[180:183], v[124:127]
	v_mfma_f32_16x16x32_bf16 v[120:123], v[148:151], v[188:191], v[120:123]
	v_mfma_f32_16x16x32_bf16 v[116:119], v[156:159], v[188:191], v[116:119]
	v_mfma_f32_16x16x32_bf16 v[104:107], v[148:151], v[204:207], v[104:107]
	v_mfma_f32_16x16x32_bf16 v[100:103], v[156:159], v[204:207], v[100:103]
	v_mfma_f32_16x16x32_bf16 v[88:91], v[148:151], v[212:215], v[88:91]
	v_mfma_f32_16x16x32_bf16 v[84:87], v[156:159], v[212:215], v[84:87]
	v_mfma_f32_16x16x32_bf16 v[128:131], v[152:155], v[184:187], v[128:131]
	v_mfma_f32_16x16x32_bf16 v[124:127], v[160:163], v[184:187], v[124:127]
	v_mfma_f32_16x16x32_bf16 v[120:123], v[152:155], v[192:195], v[120:123]
	v_mfma_f32_16x16x32_bf16 v[116:119], v[160:163], v[192:195], v[116:119]
	v_mfma_f32_16x16x32_bf16 v[104:107], v[152:155], v[208:211], v[104:107]
	v_mfma_f32_16x16x32_bf16 v[100:103], v[160:163], v[208:211], v[100:103]
	v_mfma_f32_16x16x32_bf16 v[88:91], v[152:155], v[216:219], v[88:91]
	v_mfma_f32_16x16x32_bf16 v[84:87], v[160:163], v[216:219], v[84:87]
	v_mfma_f32_16x16x32_bf16 v[112:115], v[164:167], v[180:183], v[112:115]
	v_mfma_f32_16x16x32_bf16 v[108:111], v[172:175], v[180:183], v[108:111]
	v_mfma_f32_16x16x32_bf16 v[96:99], v[164:167], v[188:191], v[96:99]
	v_mfma_f32_16x16x32_bf16 v[92:95], v[172:175], v[188:191], v[92:95]
	v_mfma_f32_16x16x32_bf16 v[80:83], v[164:167], v[204:207], v[80:83]
	v_mfma_f32_16x16x32_bf16 v[76:79], v[172:175], v[204:207], v[76:79]
	v_mfma_f32_16x16x32_bf16 v[72:75], v[164:167], v[212:215], v[72:75]
	v_mfma_f32_16x16x32_bf16 v[68:71], v[172:175], v[212:215], v[68:71]
	v_mfma_f32_16x16x32_bf16 v[112:115], v[168:171], v[184:187], v[112:115]
	v_mfma_f32_16x16x32_bf16 v[108:111], v[176:179], v[184:187], v[108:111]
	v_mfma_f32_16x16x32_bf16 v[96:99], v[168:171], v[192:195], v[96:99]
	v_mfma_f32_16x16x32_bf16 v[92:95], v[176:179], v[192:195], v[92:95]
	v_mfma_f32_16x16x32_bf16 v[80:83], v[168:171], v[208:211], v[80:83]
	v_mfma_f32_16x16x32_bf16 v[76:79], v[176:179], v[208:211], v[76:79]
	v_mfma_f32_16x16x32_bf16 v[72:75], v[168:171], v[216:219], v[72:75]
	v_mfma_f32_16x16x32_bf16 v[68:71], v[176:179], v[216:219], v[68:71]
	s_setprio 0
	s_barrier
	s_add_i32 s4, s70, s16
	s_add_u32 s98, s50, 0x80
	s_addc_u32 s99, s51, 0
	s_mov_b32 m0, s4
	ds_read_b128 v[180:183], v147 offset:49152
	ds_read_b128 v[184:187], v147 offset:50176
	ds_read_b128 v[188:191], v147 offset:51200
	ds_read_b128 v[192:195], v147 offset:52224
	ds_read_b128 v[204:207], v147 offset:53248
	ds_read_b128 v[208:211], v147 offset:54272
	ds_read_b128 v[212:215], v147 offset:55296
	ds_read_b128 v[216:219], v147 offset:56320
	global_load_lds_dwordx4 v2, s[98:99]
	s_add_i32 m0, s4, 0x2000
	s_add_u32 s4, s50, 0x40080
	s_addc_u32 s5, s51, 0
	s_add_i32 s50, s71, s16
	global_load_lds_dwordx4 v136, s[98:99]
	s_mov_b32 m0, s50
	s_nop 0
	global_load_lds_dwordx4 v2, s[4:5]
	s_add_i32 m0, s50, 0x2000
	s_nop 0
	global_load_lds_dwordx4 v136, s[4:5]
	s_mov_b32 m0, s56
	s_nop 0
	global_load_lds_dwordx4 v132, s[12:13]
	s_mov_b32 m0, s58
	s_nop 0
	global_load_lds_dwordx4 v134, s[12:13]
	s_waitcnt vmcnt(8)
	s_waitcnt lgkmcnt(0)
	s_barrier
	s_setprio 1
	v_mfma_f32_16x16x32_bf16 v[64:67], v[148:151], v[180:183], v[64:67]
	v_mfma_f32_16x16x32_bf16 v[60:63], v[156:159], v[180:183], v[60:63]
	v_mfma_f32_16x16x32_bf16 v[56:59], v[148:151], v[188:191], v[56:59]
	v_mfma_f32_16x16x32_bf16 v[52:55], v[156:159], v[188:191], v[52:55]
	v_mfma_f32_16x16x32_bf16 v[40:43], v[148:151], v[204:207], v[40:43]
	v_mfma_f32_16x16x32_bf16 v[36:39], v[156:159], v[204:207], v[36:39]
	v_mfma_f32_16x16x32_bf16 v[24:27], v[148:151], v[212:215], v[24:27]
	v_mfma_f32_16x16x32_bf16 v[20:23], v[156:159], v[212:215], v[20:23]
	v_mfma_f32_16x16x32_bf16 v[64:67], v[152:155], v[184:187], v[64:67]
	v_mfma_f32_16x16x32_bf16 v[60:63], v[160:163], v[184:187], v[60:63]
	v_mfma_f32_16x16x32_bf16 v[56:59], v[152:155], v[192:195], v[56:59]
	v_mfma_f32_16x16x32_bf16 v[52:55], v[160:163], v[192:195], v[52:55]
	v_mfma_f32_16x16x32_bf16 v[40:43], v[152:155], v[208:211], v[40:43]
	v_mfma_f32_16x16x32_bf16 v[36:39], v[160:163], v[208:211], v[36:39]
	v_mfma_f32_16x16x32_bf16 v[24:27], v[152:155], v[216:219], v[24:27]
	v_mfma_f32_16x16x32_bf16 v[20:23], v[160:163], v[216:219], v[20:23]
	v_mfma_f32_16x16x32_bf16 v[48:51], v[164:167], v[180:183], v[48:51]
	v_mfma_f32_16x16x32_bf16 v[44:47], v[172:175], v[180:183], v[44:47]
	v_mfma_f32_16x16x32_bf16 v[32:35], v[164:167], v[188:191], v[32:35]
	v_mfma_f32_16x16x32_bf16 v[28:31], v[172:175], v[188:191], v[28:31]
	v_mfma_f32_16x16x32_bf16 v[16:19], v[164:167], v[204:207], v[16:19]
	v_mfma_f32_16x16x32_bf16 v[12:15], v[172:175], v[204:207], v[12:15]
	v_mfma_f32_16x16x32_bf16 v[8:11], v[164:167], v[212:215], v[8:11]
	v_mfma_f32_16x16x32_bf16 v[4:7], v[172:175], v[212:215], v[4:7]
	v_mfma_f32_16x16x32_bf16 v[48:51], v[168:171], v[184:187], v[48:51]
	v_mfma_f32_16x16x32_bf16 v[44:47], v[176:179], v[184:187], v[44:47]
	v_mfma_f32_16x16x32_bf16 v[32:35], v[168:171], v[192:195], v[32:35]
	v_mfma_f32_16x16x32_bf16 v[28:31], v[176:179], v[192:195], v[28:31]
	v_mfma_f32_16x16x32_bf16 v[16:19], v[168:171], v[208:211], v[16:19]
	v_mfma_f32_16x16x32_bf16 v[12:15], v[176:179], v[208:211], v[12:15]
	v_mfma_f32_16x16x32_bf16 v[8:11], v[168:171], v[216:219], v[8:11]
	v_mfma_f32_16x16x32_bf16 v[4:7], v[176:179], v[216:219], v[4:7]
	s_setprio 0
	s_barrier
	s_add_i32 s69, s69, 2
	s_add_u32 s48, s48, 0x100
	s_addc_u32 s49, s49, 0
	s_cmp_gt_u32 s69, 13
	s_cbranch_scc0 .LBB0_289
	s_and_b64 vcc, exec, s[18:19]
	s_mov_b32 s62, 0x18000
	s_mov_b32 s63, 0x1a000
	s_cbranch_vccz .LBB0_292
	s_barrier

.LBB0_310:
	s_ashr_i32 s41, s40, 31
	s_lshl_b64 s[4:5], s[40:41], 19
	s_add_u32 s42, s6, s4
	s_addc_u32 s43, s7, s5
	s_and_b64 s[4:5], s[22:23], exec
	s_cselect_b32 s41, s43, s39
	s_cselect_b32 s60, s42, s38
	s_ashr_i32 s37, s36, 31
	s_lshl_b64 s[4:5], s[36:37], 19
	s_add_u32 s44, s8, s4
	s_addc_u32 s45, s9, s5
	s_and_b64 s[4:5], s[22:23], exec
	s_cselect_b32 s37, s45, s49
	s_cselect_b32 s61, s44, s48
	s_add_u32 s62, s60, 0x80
	s_addc_u32 s63, s41, 0
	s_add_u32 s4, s38, 0x40080
	s_addc_u32 s5, s39, 0
	s_add_u32 s64, s48, 0x100
	v_lshl_add_u64 v[144:145], s[4:5], 0, v[140:141]
	v_lshl_add_u64 v[146:147], s[4:5], 0, v[142:143]
	s_addc_u32 s65, s49, 0
	s_mov_b32 s68, -2
	s_mov_b64 s[48:49], 0
	s_add_u32 s4, s38, s48
	s_addc_u32 s5, s39, s49
	s_add_u32 s98, s4, 0x40080
	s_addc_u32 s99, s5, 0
	s_add_u32 s69, s4, 0x100
	s_addc_u32 s70, s5, 0
	s_add_u32 s50, s64, s48
	s_addc_u32 s51, s65, s49
	s_add_u32 s4, s4, 0x180
	s_addc_u32 s5, s5, 0
	s_add_i32 s71, 0, 0x10000
	s_add_i32 s72, 0, 0x14000
	v_add_u32_e32 v2, s71, v149
	ds_read_b128 v[152:155], v2
	s_waitcnt vmcnt(0)
	ds_read_b128 v[156:159], v2 offset:1024
	ds_read_b128 v[160:163], v2 offset:2048
	ds_read_b128 v[164:167], v2 offset:3072
	v_add_u32_e32 v2, s72, v149
	ds_read_b128 v[168:171], v2
	ds_read_b128 v[172:175], v2 offset:1024
	ds_read_b128 v[176:179], v2 offset:2048
	ds_read_b128 v[180:183], v2 offset:3072
	s_cmpk_eq_i32 s48, 0x700
	s_cselect_b32 s13, s63, s5
	s_cselect_b32 s12, s62, s4
	s_cselect_b32 s51, s37, s51
	s_cselect_b32 s50, s61, s50
	s_cselect_b32 s5, s41, s70
	s_cselect_b32 s4, s60, s69
	s_add_i32 m0, s17, 0xc000
	ds_read_b128 v[184:187], v151
	ds_read_b128 v[188:191], v151 offset:1024
	ds_read_b128 v[192:195], v151 offset:2048
	ds_read_b128 v[204:207], v151 offset:3072
	ds_read_b128 v[208:211], v151 offset:4096
	ds_read_b128 v[212:215], v151 offset:5120
	ds_read_b128 v[216:219], v151 offset:6144
	ds_read_b128 v[220:223], v151 offset:7168
	global_load_lds_dwordx4 v140, s[98:99]
	s_add_i32 m0, s17, 0xe000
	s_nop 0
	global_load_lds_dwordx4 v142, s[98:99]
	s_waitcnt vmcnt(8)
	s_waitcnt lgkmcnt(0)
	s_barrier
	s_setprio 1
	v_mfma_f32_16x16x32_bf16 v[128:131], v[152:155], v[184:187], 0
	v_mfma_f32_16x16x32_bf16 v[124:127], v[160:163], v[184:187], 0
	v_mfma_f32_16x16x32_bf16 v[120:123], v[152:155], v[192:195], 0
	v_mfma_f32_16x16x32_bf16 v[116:119], v[160:163], v[192:195], 0
	v_mfma_f32_16x16x32_bf16 v[104:107], v[152:155], v[208:211], 0
	v_mfma_f32_16x16x32_bf16 v[100:103], v[160:163], v[208:211], 0
	v_mfma_f32_16x16x32_bf16 v[88:91], v[152:155], v[216:219], 0
	v_mfma_f32_16x16x32_bf16 v[84:87], v[160:163], v[216:219], 0
	v_mfma_f32_16x16x32_bf16 v[128:131], v[156:159], v[188:191], v[128:131]
	v_mfma_f32_16x16x32_bf16 v[124:127], v[164:167], v[188:191], v[124:127]
	v_mfma_f32_16x16x32_bf16 v[120:123], v[156:159], v[204:207], v[120:123]
	v_mfma_f32_16x16x32_bf16 v[116:119], v[164:167], v[204:207], v[116:119]
	v_mfma_f32_16x16x32_bf16 v[104:107], v[156:159], v[212:215], v[104:107]
	v_mfma_f32_16x16x32_bf16 v[100:103], v[164:167], v[212:215], v[100:103]
	v_mfma_f32_16x16x32_bf16 v[88:91], v[156:159], v[220:223], v[88:91]
	v_mfma_f32_16x16x32_bf16 v[84:87], v[164:167], v[220:223], v[84:87]
	v_mfma_f32_16x16x32_bf16 v[112:115], v[168:171], v[184:187], 0
	v_mfma_f32_16x16x32_bf16 v[108:111], v[176:179], v[184:187], 0
	v_mfma_f32_16x16x32_bf16 v[96:99], v[168:171], v[192:195], 0
	v_mfma_f32_16x16x32_bf16 v[92:95], v[176:179], v[192:195], 0
	v_mfma_f32_16x16x32_bf16 v[80:83], v[168:171], v[208:211], 0
	v_mfma_f32_16x16x32_bf16 v[76:79], v[176:179], v[208:211], 0
	v_mfma_f32_16x16x32_bf16 v[72:75], v[168:171], v[216:219], 0
	v_mfma_f32_16x16x32_bf16 v[68:71], v[176:179], v[216:219], 0
	v_mfma_f32_16x16x32_bf16 v[112:115], v[172:175], v[188:191], v[112:115]
	v_mfma_f32_16x16x32_bf16 v[108:111], v[180:183], v[188:191], v[108:111]
	v_mfma_f32_16x16x32_bf16 v[96:99], v[172:175], v[204:207], v[96:99]
	v_mfma_f32_16x16x32_bf16 v[92:95], v[180:183], v[204:207], v[92:95]
	v_mfma_f32_16x16x32_bf16 v[80:83], v[172:175], v[212:215], v[80:83]
	v_mfma_f32_16x16x32_bf16 v[76:79], v[180:183], v[212:215], v[76:79]
	v_mfma_f32_16x16x32_bf16 v[72:75], v[172:175], v[220:223], v[72:75]
	v_mfma_f32_16x16x32_bf16 v[68:71], v[180:183], v[220:223], v[68:71]
	s_setprio 0
	s_barrier
	s_add_i32 s69, s71, s16
	s_mov_b32 m0, s69
	ds_read_b128 v[184:187], v151 offset:16384
	ds_read_b128 v[188:191], v151 offset:17408
	ds_read_b128 v[192:195], v151 offset:18432
	ds_read_b128 v[204:207], v151 offset:19456
	ds_read_b128 v[208:211], v151 offset:20480
	ds_read_b128 v[212:215], v151 offset:21504
	ds_read_b128 v[216:219], v151 offset:22528
	ds_read_b128 v[220:223], v151 offset:23552
	global_load_lds_dwordx4 v134, s[50:51]
	s_add_i32 m0, s69, 0x2000
	s_add_u32 s70, s50, 0x40000
	s_addc_u32 s71, s51, 0
	s_add_i32 s69, s72, s16
	global_load_lds_dwordx4 v138, s[50:51]
	s_mov_b32 m0, s69
	s_nop 0
	global_load_lds_dwordx4 v134, s[70:71]
	s_add_i32 m0, s69, 0x2000
	s_nop 0
	global_load_lds_dwordx4 v138, s[70:71]
	s_mov_b32 m0, s17
	s_nop 0
	global_load_lds_dwordx4 v132, s[4:5]
	s_mov_b32 m0, s21
	s_nop 0
	global_load_lds_dwordx4 v136, s[4:5]
	s_waitcnt vmcnt(8)
	s_waitcnt lgkmcnt(0)
	s_barrier
	s_setprio 1
	v_mfma_f32_16x16x32_bf16 v[64:67], v[152:155], v[184:187], 0
	v_mfma_f32_16x16x32_bf16 v[60:63], v[160:163], v[184:187], 0
	v_mfma_f32_16x16x32_bf16 v[56:59], v[152:155], v[192:195], 0
	v_mfma_f32_16x16x32_bf16 v[52:55], v[160:163], v[192:195], 0
	v_mfma_f32_16x16x32_bf16 v[40:43], v[152:155], v[208:211], 0
	v_mfma_f32_16x16x32_bf16 v[36:39], v[160:163], v[208:211], 0
	v_mfma_f32_16x16x32_bf16 v[24:27], v[152:155], v[216:219], 0
	v_mfma_f32_16x16x32_bf16 v[20:23], v[160:163], v[216:219], 0
	v_mfma_f32_16x16x32_bf16 v[64:67], v[156:159], v[188:191], v[64:67]
	v_mfma_f32_16x16x32_bf16 v[60:63], v[164:167], v[188:191], v[60:63]
	v_mfma_f32_16x16x32_bf16 v[56:59], v[156:159], v[204:207], v[56:59]
	v_mfma_f32_16x16x32_bf16 v[52:55], v[164:167], v[204:207], v[52:55]
	v_mfma_f32_16x16x32_bf16 v[40:43], v[156:159], v[212:215], v[40:43]
	v_mfma_f32_16x16x32_bf16 v[36:39], v[164:167], v[212:215], v[36:39]
	v_mfma_f32_16x16x32_bf16 v[24:27], v[156:159], v[220:223], v[24:27]
	v_mfma_f32_16x16x32_bf16 v[20:23], v[164:167], v[220:223], v[20:23]
	v_mfma_f32_16x16x32_bf16 v[48:51], v[168:171], v[184:187], 0
	v_mfma_f32_16x16x32_bf16 v[44:47], v[176:179], v[184:187], 0
	v_mfma_f32_16x16x32_bf16 v[32:35], v[168:171], v[192:195], 0
	v_mfma_f32_16x16x32_bf16 v[28:31], v[176:179], v[192:195], 0
	v_mfma_f32_16x16x32_bf16 v[16:19], v[168:171], v[208:211], 0
	v_mfma_f32_16x16x32_bf16 v[12:15], v[176:179], v[208:211], 0
	v_mfma_f32_16x16x32_bf16 v[8:11], v[168:171], v[216:219], 0
	v_mfma_f32_16x16x32_bf16 v[4:7], v[176:179], v[216:219], 0
	v_mfma_f32_16x16x32_bf16 v[48:51], v[172:175], v[188:191], v[48:51]
	v_mfma_f32_16x16x32_bf16 v[44:47], v[180:183], v[188:191], v[44:47]
	v_mfma_f32_16x16x32_bf16 v[32:35], v[172:175], v[204:207], v[32:35]
	v_mfma_f32_16x16x32_bf16 v[28:31], v[180:183], v[204:207], v[28:31]
	v_mfma_f32_16x16x32_bf16 v[16:19], v[172:175], v[212:215], v[16:19]
	v_mfma_f32_16x16x32_bf16 v[12:15], v[180:183], v[212:215], v[12:15]
	v_mfma_f32_16x16x32_bf16 v[8:11], v[172:175], v[220:223], v[8:11]
	v_mfma_f32_16x16x32_bf16 v[4:7], v[180:183], v[220:223], v[4:7]
	s_setprio 0
	s_barrier
	s_add_i32 s69, 0, 0x18000
	v_add_u32_e32 v2, s69, v149
	s_add_i32 s70, 0, 0x1c000
	ds_read_b128 v[152:155], v2
	ds_read_b128 v[156:159], v2 offset:1024
	ds_read_b128 v[160:163], v2 offset:2048
	ds_read_b128 v[164:167], v2 offset:3072
	v_add_u32_e32 v2, s70, v149
	ds_read_b128 v[168:171], v2
	ds_read_b128 v[172:175], v2 offset:1024
	ds_read_b128 v[176:179], v2 offset:2048
	ds_read_b128 v[180:183], v2 offset:3072
	s_add_u32 s4, s4, 0x40000
	s_addc_u32 s5, s5, 0
	s_mov_b32 m0, s46
	ds_read_b128 v[184:187], v151 offset:32768
	ds_read_b128 v[188:191], v151 offset:33792
	ds_read_b128 v[192:195], v151 offset:34816
	ds_read_b128 v[204:207], v151 offset:35840
	ds_read_b128 v[208:211], v151 offset:36864
	ds_read_b128 v[212:215], v151 offset:37888
	ds_read_b128 v[216:219], v151 offset:38912
	ds_read_b128 v[220:223], v151 offset:39936
	global_load_lds_dwordx4 v132, s[4:5]
	s_mov_b32 m0, s47
	s_nop 0
	global_load_lds_dwordx4 v136, s[4:5]
	s_waitcnt vmcnt(8)
	s_waitcnt lgkmcnt(0)
	s_barrier
	s_setprio 1
	v_mfma_f32_16x16x32_bf16 v[128:131], v[152:155], v[184:187], v[128:131]
	v_mfma_f32_16x16x32_bf16 v[124:127], v[160:163], v[184:187], v[124:127]
	v_mfma_f32_16x16x32_bf16 v[120:123], v[152:155], v[192:195], v[120:123]
	v_mfma_f32_16x16x32_bf16 v[116:119], v[160:163], v[192:195], v[116:119]
	v_mfma_f32_16x16x32_bf16 v[104:107], v[152:155], v[208:211], v[104:107]
	v_mfma_f32_16x16x32_bf16 v[100:103], v[160:163], v[208:211], v[100:103]
	v_mfma_f32_16x16x32_bf16 v[88:91], v[152:155], v[216:219], v[88:91]
	v_mfma_f32_16x16x32_bf16 v[84:87], v[160:163], v[216:219], v[84:87]
	v_mfma_f32_16x16x32_bf16 v[128:131], v[156:159], v[188:191], v[128:131]
	v_mfma_f32_16x16x32_bf16 v[124:127], v[164:167], v[188:191], v[124:127]
	v_mfma_f32_16x16x32_bf16 v[120:123], v[156:159], v[204:207], v[120:123]
	v_mfma_f32_16x16x32_bf16 v[116:119], v[164:167], v[204:207], v[116:119]
	v_mfma_f32_16x16x32_bf16 v[104:107], v[156:159], v[212:215], v[104:107]
	v_mfma_f32_16x16x32_bf16 v[100:103], v[164:167], v[212:215], v[100:103]
	v_mfma_f32_16x16x32_bf16 v[88:91], v[156:159], v[220:223], v[88:91]
	v_mfma_f32_16x16x32_bf16 v[84:87], v[164:167], v[220:223], v[84:87]
	v_mfma_f32_16x16x32_bf16 v[112:115], v[168:171], v[184:187], v[112:115]
	v_mfma_f32_16x16x32_bf16 v[108:111], v[176:179], v[184:187], v[108:111]
	v_mfma_f32_16x16x32_bf16 v[96:99], v[168:171], v[192:195], v[96:99]
	v_mfma_f32_16x16x32_bf16 v[92:95], v[176:179], v[192:195], v[92:95]
	v_mfma_f32_16x16x32_bf16 v[80:83], v[168:171], v[208:211], v[80:83]
	v_mfma_f32_16x16x32_bf16 v[76:79], v[176:179], v[208:211], v[76:79]
	v_mfma_f32_16x16x32_bf16 v[72:75], v[168:171], v[216:219], v[72:75]
	v_mfma_f32_16x16x32_bf16 v[68:71], v[176:179], v[216:219], v[68:71]
	v_mfma_f32_16x16x32_bf16 v[112:115], v[172:175], v[188:191], v[112:115]
	v_mfma_f32_16x16x32_bf16 v[108:111], v[180:183], v[188:191], v[108:111]
	v_mfma_f32_16x16x32_bf16 v[96:99], v[172:175], v[204:207], v[96:99]
	v_mfma_f32_16x16x32_bf16 v[92:95], v[180:183], v[204:207], v[92:95]
	v_mfma_f32_16x16x32_bf16 v[80:83], v[172:175], v[212:215], v[80:83]
	v_mfma_f32_16x16x32_bf16 v[76:79], v[180:183], v[212:215], v[76:79]
	v_mfma_f32_16x16x32_bf16 v[72:75], v[172:175], v[220:223], v[72:75]
	v_mfma_f32_16x16x32_bf16 v[68:71], v[180:183], v[220:223], v[68:71]
	s_setprio 0
	s_barrier
	s_add_i32 s4, s69, s16
	s_add_u32 s98, s50, 0x80
	s_addc_u32 s99, s51, 0
	s_mov_b32 m0, s4
	ds_read_b128 v[184:187], v151 offset:49152
	ds_read_b128 v[188:191], v151 offset:50176
	ds_read_b128 v[192:195], v151 offset:51200
	ds_read_b128 v[204:207], v151 offset:52224
	ds_read_b128 v[208:211], v151 offset:53248
	ds_read_b128 v[212:215], v151 offset:54272
	ds_read_b128 v[216:219], v151 offset:55296
	ds_read_b128 v[220:223], v151 offset:56320
	global_load_lds_dwordx4 v134, s[98:99]
	s_add_i32 m0, s4, 0x2000
	s_add_u32 s4, s50, 0x40080
	s_addc_u32 s5, s51, 0
	s_add_i32 s50, s70, s16
	global_load_lds_dwordx4 v138, s[98:99]
	s_mov_b32 m0, s50
	s_nop 0
	global_load_lds_dwordx4 v134, s[4:5]
	s_add_i32 m0, s50, 0x2000
	s_nop 0
	global_load_lds_dwordx4 v138, s[4:5]
	s_mov_b32 m0, s53
	s_nop 0
	global_load_lds_dwordx4 v132, s[12:13]
	s_mov_b32 m0, s56
	s_nop 0
	global_load_lds_dwordx4 v136, s[12:13]
	s_waitcnt vmcnt(8)
	s_waitcnt lgkmcnt(0)
	s_barrier
	s_setprio 1
	v_mfma_f32_16x16x32_bf16 v[64:67], v[152:155], v[184:187], v[64:67]
	v_mfma_f32_16x16x32_bf16 v[60:63], v[160:163], v[184:187], v[60:63]
	v_mfma_f32_16x16x32_bf16 v[56:59], v[152:155], v[192:195], v[56:59]
	v_mfma_f32_16x16x32_bf16 v[52:55], v[160:163], v[192:195], v[52:55]
	v_mfma_f32_16x16x32_bf16 v[40:43], v[152:155], v[208:211], v[40:43]
	v_mfma_f32_16x16x32_bf16 v[36:39], v[160:163], v[208:211], v[36:39]
	v_mfma_f32_16x16x32_bf16 v[24:27], v[152:155], v[216:219], v[24:27]
	v_mfma_f32_16x16x32_bf16 v[20:23], v[160:163], v[216:219], v[20:23]
	v_mfma_f32_16x16x32_bf16 v[64:67], v[156:159], v[188:191], v[64:67]
	v_mfma_f32_16x16x32_bf16 v[60:63], v[164:167], v[188:191], v[60:63]
	v_mfma_f32_16x16x32_bf16 v[56:59], v[156:159], v[204:207], v[56:59]
	v_mfma_f32_16x16x32_bf16 v[52:55], v[164:167], v[204:207], v[52:55]
	v_mfma_f32_16x16x32_bf16 v[40:43], v[156:159], v[212:215], v[40:43]
	v_mfma_f32_16x16x32_bf16 v[36:39], v[164:167], v[212:215], v[36:39]
	v_mfma_f32_16x16x32_bf16 v[24:27], v[156:159], v[220:223], v[24:27]
	v_mfma_f32_16x16x32_bf16 v[20:23], v[164:167], v[220:223], v[20:23]
	v_mfma_f32_16x16x32_bf16 v[48:51], v[168:171], v[184:187], v[48:51]
	v_mfma_f32_16x16x32_bf16 v[44:47], v[176:179], v[184:187], v[44:47]
	v_mfma_f32_16x16x32_bf16 v[32:35], v[168:171], v[192:195], v[32:35]
	v_mfma_f32_16x16x32_bf16 v[28:31], v[176:179], v[192:195], v[28:31]
	v_mfma_f32_16x16x32_bf16 v[16:19], v[168:171], v[208:211], v[16:19]
	v_mfma_f32_16x16x32_bf16 v[12:15], v[176:179], v[208:211], v[12:15]
	v_mfma_f32_16x16x32_bf16 v[8:11], v[168:171], v[216:219], v[8:11]
	v_mfma_f32_16x16x32_bf16 v[4:7], v[176:179], v[216:219], v[4:7]
	v_mfma_f32_16x16x32_bf16 v[48:51], v[172:175], v[188:191], v[48:51]
	v_mfma_f32_16x16x32_bf16 v[44:47], v[180:183], v[188:191], v[44:47]
	v_mfma_f32_16x16x32_bf16 v[32:35], v[172:175], v[204:207], v[32:35]
	v_mfma_f32_16x16x32_bf16 v[28:31], v[180:183], v[204:207], v[28:31]
	v_mfma_f32_16x16x32_bf16 v[16:19], v[172:175], v[212:215], v[16:19]
	v_mfma_f32_16x16x32_bf16 v[12:15], v[180:183], v[212:215], v[12:15]
	v_mfma_f32_16x16x32_bf16 v[8:11], v[172:175], v[220:223], v[8:11]
	v_mfma_f32_16x16x32_bf16 v[4:7], v[180:183], v[220:223], v[4:7]
	s_setprio 0
	s_barrier
	s_add_i32 s68, s68, 2
	s_add_u32 s48, s48, 0x100
	s_addc_u32 s49, s49, 0
	s_cmp_gt_u32 s68, 13
.LBB0_311:
	s_add_u32 s4, s38, s48
	s_addc_u32 s5, s39, s49
	s_add_u32 s98, s4, 0x40080
	s_addc_u32 s99, s5, 0
	s_add_u32 s69, s4, 0x100
	s_addc_u32 s70, s5, 0
	s_add_u32 s50, s64, s48
	s_addc_u32 s51, s65, s49
	s_add_u32 s4, s4, 0x180
	s_addc_u32 s5, s5, 0
	s_add_i32 s71, 0, 0x10000
	s_add_i32 s72, 0, 0x14000
	v_add_u32_e32 v2, s71, v149
	ds_read_b128 v[152:155], v2
	s_waitcnt vmcnt(0)
	ds_read_b128 v[156:159], v2 offset:1024
	ds_read_b128 v[160:163], v2 offset:2048
	ds_read_b128 v[164:167], v2 offset:3072
	v_add_u32_e32 v2, s72, v149
	ds_read_b128 v[168:171], v2
	ds_read_b128 v[172:175], v2 offset:1024
	ds_read_b128 v[176:179], v2 offset:2048
	ds_read_b128 v[180:183], v2 offset:3072
	s_cmpk_eq_i32 s48, 0x700
	s_cselect_b32 s13, s63, s5
	s_cselect_b32 s12, s62, s4
	s_cselect_b32 s51, s37, s51
	s_cselect_b32 s50, s61, s50
	s_cselect_b32 s5, s41, s70
	s_cselect_b32 s4, s60, s69
	s_add_i32 m0, s17, 0xc000
	ds_read_b128 v[184:187], v151
	ds_read_b128 v[188:191], v151 offset:1024
	ds_read_b128 v[192:195], v151 offset:2048
	ds_read_b128 v[204:207], v151 offset:3072
	ds_read_b128 v[208:211], v151 offset:4096
	ds_read_b128 v[212:215], v151 offset:5120
	ds_read_b128 v[216:219], v151 offset:6144
	ds_read_b128 v[220:223], v151 offset:7168
	global_load_lds_dwordx4 v140, s[98:99]
	s_add_i32 m0, s17, 0xe000
	s_nop 0
	global_load_lds_dwordx4 v142, s[98:99]
	s_waitcnt vmcnt(8)
	s_waitcnt lgkmcnt(0)
	s_barrier
	s_setprio 1
	v_mfma_f32_16x16x32_bf16 v[128:131], v[152:155], v[184:187], v[128:131]
	v_mfma_f32_16x16x32_bf16 v[124:127], v[160:163], v[184:187], v[124:127]
	v_mfma_f32_16x16x32_bf16 v[120:123], v[152:155], v[192:195], v[120:123]
	v_mfma_f32_16x16x32_bf16 v[116:119], v[160:163], v[192:195], v[116:119]
	v_mfma_f32_16x16x32_bf16 v[104:107], v[152:155], v[208:211], v[104:107]
	v_mfma_f32_16x16x32_bf16 v[100:103], v[160:163], v[208:211], v[100:103]
	v_mfma_f32_16x16x32_bf16 v[88:91], v[152:155], v[216:219], v[88:91]
	v_mfma_f32_16x16x32_bf16 v[84:87], v[160:163], v[216:219], v[84:87]
	v_mfma_f32_16x16x32_bf16 v[128:131], v[156:159], v[188:191], v[128:131]
	v_mfma_f32_16x16x32_bf16 v[124:127], v[164:167], v[188:191], v[124:127]
	v_mfma_f32_16x16x32_bf16 v[120:123], v[156:159], v[204:207], v[120:123]
	v_mfma_f32_16x16x32_bf16 v[116:119], v[164:167], v[204:207], v[116:119]
	v_mfma_f32_16x16x32_bf16 v[104:107], v[156:159], v[212:215], v[104:107]
	v_mfma_f32_16x16x32_bf16 v[100:103], v[164:167], v[212:215], v[100:103]
	v_mfma_f32_16x16x32_bf16 v[88:91], v[156:159], v[220:223], v[88:91]
	v_mfma_f32_16x16x32_bf16 v[84:87], v[164:167], v[220:223], v[84:87]
	v_mfma_f32_16x16x32_bf16 v[112:115], v[168:171], v[184:187], v[112:115]
	v_mfma_f32_16x16x32_bf16 v[108:111], v[176:179], v[184:187], v[108:111]
	v_mfma_f32_16x16x32_bf16 v[96:99], v[168:171], v[192:195], v[96:99]
	v_mfma_f32_16x16x32_bf16 v[92:95], v[176:179], v[192:195], v[92:95]
	v_mfma_f32_16x16x32_bf16 v[80:83], v[168:171], v[208:211], v[80:83]
	v_mfma_f32_16x16x32_bf16 v[76:79], v[176:179], v[208:211], v[76:79]
	v_mfma_f32_16x16x32_bf16 v[72:75], v[168:171], v[216:219], v[72:75]
	v_mfma_f32_16x16x32_bf16 v[68:71], v[176:179], v[216:219], v[68:71]
	v_mfma_f32_16x16x32_bf16 v[112:115], v[172:175], v[188:191], v[112:115]
	v_mfma_f32_16x16x32_bf16 v[108:111], v[180:183], v[188:191], v[108:111]
	v_mfma_f32_16x16x32_bf16 v[96:99], v[172:175], v[204:207], v[96:99]
	v_mfma_f32_16x16x32_bf16 v[92:95], v[180:183], v[204:207], v[92:95]
	v_mfma_f32_16x16x32_bf16 v[80:83], v[172:175], v[212:215], v[80:83]
	v_mfma_f32_16x16x32_bf16 v[76:79], v[180:183], v[212:215], v[76:79]
	v_mfma_f32_16x16x32_bf16 v[72:75], v[172:175], v[220:223], v[72:75]
	v_mfma_f32_16x16x32_bf16 v[68:71], v[180:183], v[220:223], v[68:71]
	s_setprio 0
	s_barrier
	s_add_i32 s69, s71, s16
	s_mov_b32 m0, s69
	ds_read_b128 v[184:187], v151 offset:16384
	ds_read_b128 v[188:191], v151 offset:17408
	ds_read_b128 v[192:195], v151 offset:18432
	ds_read_b128 v[204:207], v151 offset:19456
	ds_read_b128 v[208:211], v151 offset:20480
	ds_read_b128 v[212:215], v151 offset:21504
	ds_read_b128 v[216:219], v151 offset:22528
	ds_read_b128 v[220:223], v151 offset:23552
	global_load_lds_dwordx4 v134, s[50:51]
	s_add_i32 m0, s69, 0x2000
	s_add_u32 s70, s50, 0x40000
	s_addc_u32 s71, s51, 0
	s_add_i32 s69, s72, s16
	global_load_lds_dwordx4 v138, s[50:51]
	s_mov_b32 m0, s69
	s_nop 0
	global_load_lds_dwordx4 v134, s[70:71]
	s_add_i32 m0, s69, 0x2000
	s_nop 0
	global_load_lds_dwordx4 v138, s[70:71]
	s_mov_b32 m0, s17
	s_nop 0
	global_load_lds_dwordx4 v132, s[4:5]
	s_mov_b32 m0, s21
	s_nop 0
	global_load_lds_dwordx4 v136, s[4:5]
	s_waitcnt vmcnt(8)
	s_waitcnt lgkmcnt(0)
	s_barrier
	s_setprio 1
	v_mfma_f32_16x16x32_bf16 v[64:67], v[152:155], v[184:187], v[64:67]
	v_mfma_f32_16x16x32_bf16 v[60:63], v[160:163], v[184:187], v[60:63]
	v_mfma_f32_16x16x32_bf16 v[56:59], v[152:155], v[192:195], v[56:59]
	v_mfma_f32_16x16x32_bf16 v[52:55], v[160:163], v[192:195], v[52:55]
	v_mfma_f32_16x16x32_bf16 v[40:43], v[152:155], v[208:211], v[40:43]
	v_mfma_f32_16x16x32_bf16 v[36:39], v[160:163], v[208:211], v[36:39]
	v_mfma_f32_16x16x32_bf16 v[24:27], v[152:155], v[216:219], v[24:27]
	v_mfma_f32_16x16x32_bf16 v[20:23], v[160:163], v[216:219], v[20:23]
	v_mfma_f32_16x16x32_bf16 v[64:67], v[156:159], v[188:191], v[64:67]
	v_mfma_f32_16x16x32_bf16 v[60:63], v[164:167], v[188:191], v[60:63]
	v_mfma_f32_16x16x32_bf16 v[56:59], v[156:159], v[204:207], v[56:59]
	v_mfma_f32_16x16x32_bf16 v[52:55], v[164:167], v[204:207], v[52:55]
	v_mfma_f32_16x16x32_bf16 v[40:43], v[156:159], v[212:215], v[40:43]
	v_mfma_f32_16x16x32_bf16 v[36:39], v[164:167], v[212:215], v[36:39]
	v_mfma_f32_16x16x32_bf16 v[24:27], v[156:159], v[220:223], v[24:27]
	v_mfma_f32_16x16x32_bf16 v[20:23], v[164:167], v[220:223], v[20:23]
	v_mfma_f32_16x16x32_bf16 v[48:51], v[168:171], v[184:187], v[48:51]
	v_mfma_f32_16x16x32_bf16 v[44:47], v[176:179], v[184:187], v[44:47]
	v_mfma_f32_16x16x32_bf16 v[32:35], v[168:171], v[192:195], v[32:35]
	v_mfma_f32_16x16x32_bf16 v[28:31], v[176:179], v[192:195], v[28:31]
	v_mfma_f32_16x16x32_bf16 v[16:19], v[168:171], v[208:211], v[16:19]
	v_mfma_f32_16x16x32_bf16 v[12:15], v[176:179], v[208:211], v[12:15]
	v_mfma_f32_16x16x32_bf16 v[8:11], v[168:171], v[216:219], v[8:11]
	v_mfma_f32_16x16x32_bf16 v[4:7], v[176:179], v[216:219], v[4:7]
	v_mfma_f32_16x16x32_bf16 v[48:51], v[172:175], v[188:191], v[48:51]
	v_mfma_f32_16x16x32_bf16 v[44:47], v[180:183], v[188:191], v[44:47]
	v_mfma_f32_16x16x32_bf16 v[32:35], v[172:175], v[204:207], v[32:35]
	v_mfma_f32_16x16x32_bf16 v[28:31], v[180:183], v[204:207], v[28:31]
	v_mfma_f32_16x16x32_bf16 v[16:19], v[172:175], v[212:215], v[16:19]
	v_mfma_f32_16x16x32_bf16 v[12:15], v[180:183], v[212:215], v[12:15]
	v_mfma_f32_16x16x32_bf16 v[8:11], v[172:175], v[220:223], v[8:11]
	v_mfma_f32_16x16x32_bf16 v[4:7], v[180:183], v[220:223], v[4:7]
	s_setprio 0
	s_barrier
	s_add_i32 s69, 0, 0x18000
	v_add_u32_e32 v2, s69, v149
	s_add_i32 s70, 0, 0x1c000
	ds_read_b128 v[152:155], v2
	ds_read_b128 v[156:159], v2 offset:1024
	ds_read_b128 v[160:163], v2 offset:2048
	ds_read_b128 v[164:167], v2 offset:3072
	v_add_u32_e32 v2, s70, v149
	ds_read_b128 v[168:171], v2
	ds_read_b128 v[172:175], v2 offset:1024
	ds_read_b128 v[176:179], v2 offset:2048
	ds_read_b128 v[180:183], v2 offset:3072
	s_add_u32 s4, s4, 0x40000
	s_addc_u32 s5, s5, 0
	s_mov_b32 m0, s46
	ds_read_b128 v[184:187], v151 offset:32768
	ds_read_b128 v[188:191], v151 offset:33792
	ds_read_b128 v[192:195], v151 offset:34816
	ds_read_b128 v[204:207], v151 offset:35840
	ds_read_b128 v[208:211], v151 offset:36864
	ds_read_b128 v[212:215], v151 offset:37888
	ds_read_b128 v[216:219], v151 offset:38912
	ds_read_b128 v[220:223], v151 offset:39936
	global_load_lds_dwordx4 v132, s[4:5]
	s_mov_b32 m0, s47
	s_nop 0
	global_load_lds_dwordx4 v136, s[4:5]
	s_waitcnt vmcnt(8)
	s_waitcnt lgkmcnt(0)
	s_barrier
	s_setprio 1
	v_mfma_f32_16x16x32_bf16 v[128:131], v[152:155], v[184:187], v[128:131]
	v_mfma_f32_16x16x32_bf16 v[124:127], v[160:163], v[184:187], v[124:127]
	v_mfma_f32_16x16x32_bf16 v[120:123], v[152:155], v[192:195], v[120:123]
	v_mfma_f32_16x16x32_bf16 v[116:119], v[160:163], v[192:195], v[116:119]
	v_mfma_f32_16x16x32_bf16 v[104:107], v[152:155], v[208:211], v[104:107]
	v_mfma_f32_16x16x32_bf16 v[100:103], v[160:163], v[208:211], v[100:103]
	v_mfma_f32_16x16x32_bf16 v[88:91], v[152:155], v[216:219], v[88:91]
	v_mfma_f32_16x16x32_bf16 v[84:87], v[160:163], v[216:219], v[84:87]
	v_mfma_f32_16x16x32_bf16 v[128:131], v[156:159], v[188:191], v[128:131]
	v_mfma_f32_16x16x32_bf16 v[124:127], v[164:167], v[188:191], v[124:127]
	v_mfma_f32_16x16x32_bf16 v[120:123], v[156:159], v[204:207], v[120:123]
	v_mfma_f32_16x16x32_bf16 v[116:119], v[164:167], v[204:207], v[116:119]
	v_mfma_f32_16x16x32_bf16 v[104:107], v[156:159], v[212:215], v[104:107]
	v_mfma_f32_16x16x32_bf16 v[100:103], v[164:167], v[212:215], v[100:103]
	v_mfma_f32_16x16x32_bf16 v[88:91], v[156:159], v[220:223], v[88:91]
	v_mfma_f32_16x16x32_bf16 v[84:87], v[164:167], v[220:223], v[84:87]
	v_mfma_f32_16x16x32_bf16 v[112:115], v[168:171], v[184:187], v[112:115]
	v_mfma_f32_16x16x32_bf16 v[108:111], v[176:179], v[184:187], v[108:111]
	v_mfma_f32_16x16x32_bf16 v[96:99], v[168:171], v[192:195], v[96:99]
	v_mfma_f32_16x16x32_bf16 v[92:95], v[176:179], v[192:195], v[92:95]
	v_mfma_f32_16x16x32_bf16 v[80:83], v[168:171], v[208:211], v[80:83]
	v_mfma_f32_16x16x32_bf16 v[76:79], v[176:179], v[208:211], v[76:79]
	v_mfma_f32_16x16x32_bf16 v[72:75], v[168:171], v[216:219], v[72:75]
	v_mfma_f32_16x16x32_bf16 v[68:71], v[176:179], v[216:219], v[68:71]
	v_mfma_f32_16x16x32_bf16 v[112:115], v[172:175], v[188:191], v[112:115]
	v_mfma_f32_16x16x32_bf16 v[108:111], v[180:183], v[188:191], v[108:111]
	v_mfma_f32_16x16x32_bf16 v[96:99], v[172:175], v[204:207], v[96:99]
	v_mfma_f32_16x16x32_bf16 v[92:95], v[180:183], v[204:207], v[92:95]
	v_mfma_f32_16x16x32_bf16 v[80:83], v[172:175], v[212:215], v[80:83]
	v_mfma_f32_16x16x32_bf16 v[76:79], v[180:183], v[212:215], v[76:79]
	v_mfma_f32_16x16x32_bf16 v[72:75], v[172:175], v[220:223], v[72:75]
	v_mfma_f32_16x16x32_bf16 v[68:71], v[180:183], v[220:223], v[68:71]
	s_setprio 0
	s_barrier
	s_add_i32 s4, s69, s16
	s_add_u32 s98, s50, 0x80
	s_addc_u32 s99, s51, 0
	s_mov_b32 m0, s4
	ds_read_b128 v[184:187], v151 offset:49152
	ds_read_b128 v[188:191], v151 offset:50176
	ds_read_b128 v[192:195], v151 offset:51200
	ds_read_b128 v[204:207], v151 offset:52224
	ds_read_b128 v[208:211], v151 offset:53248
	ds_read_b128 v[212:215], v151 offset:54272
	ds_read_b128 v[216:219], v151 offset:55296
	ds_read_b128 v[220:223], v151 offset:56320
	global_load_lds_dwordx4 v134, s[98:99]
	s_add_i32 m0, s4, 0x2000
	s_add_u32 s4, s50, 0x40080
	s_addc_u32 s5, s51, 0
	s_add_i32 s50, s70, s16
	global_load_lds_dwordx4 v138, s[98:99]
	s_mov_b32 m0, s50
	s_nop 0
	global_load_lds_dwordx4 v134, s[4:5]
	s_add_i32 m0, s50, 0x2000
	s_nop 0
	global_load_lds_dwordx4 v138, s[4:5]
	s_mov_b32 m0, s53
	s_nop 0
	global_load_lds_dwordx4 v132, s[12:13]
	s_mov_b32 m0, s56
	s_nop 0
	global_load_lds_dwordx4 v136, s[12:13]
	s_waitcnt vmcnt(8)
	s_waitcnt lgkmcnt(0)
	s_barrier
	s_setprio 1
	v_mfma_f32_16x16x32_bf16 v[64:67], v[152:155], v[184:187], v[64:67]
	v_mfma_f32_16x16x32_bf16 v[60:63], v[160:163], v[184:187], v[60:63]
	v_mfma_f32_16x16x32_bf16 v[56:59], v[152:155], v[192:195], v[56:59]
	v_mfma_f32_16x16x32_bf16 v[52:55], v[160:163], v[192:195], v[52:55]
	v_mfma_f32_16x16x32_bf16 v[40:43], v[152:155], v[208:211], v[40:43]
	v_mfma_f32_16x16x32_bf16 v[36:39], v[160:163], v[208:211], v[36:39]
	v_mfma_f32_16x16x32_bf16 v[24:27], v[152:155], v[216:219], v[24:27]
	v_mfma_f32_16x16x32_bf16 v[20:23], v[160:163], v[216:219], v[20:23]
	v_mfma_f32_16x16x32_bf16 v[64:67], v[156:159], v[188:191], v[64:67]
	v_mfma_f32_16x16x32_bf16 v[60:63], v[164:167], v[188:191], v[60:63]
	v_mfma_f32_16x16x32_bf16 v[56:59], v[156:159], v[204:207], v[56:59]
	v_mfma_f32_16x16x32_bf16 v[52:55], v[164:167], v[204:207], v[52:55]
	v_mfma_f32_16x16x32_bf16 v[40:43], v[156:159], v[212:215], v[40:43]
	v_mfma_f32_16x16x32_bf16 v[36:39], v[164:167], v[212:215], v[36:39]
	v_mfma_f32_16x16x32_bf16 v[24:27], v[156:159], v[220:223], v[24:27]
	v_mfma_f32_16x16x32_bf16 v[20:23], v[164:167], v[220:223], v[20:23]
	v_mfma_f32_16x16x32_bf16 v[48:51], v[168:171], v[184:187], v[48:51]
	v_mfma_f32_16x16x32_bf16 v[44:47], v[176:179], v[184:187], v[44:47]
	v_mfma_f32_16x16x32_bf16 v[32:35], v[168:171], v[192:195], v[32:35]
	v_mfma_f32_16x16x32_bf16 v[28:31], v[176:179], v[192:195], v[28:31]
	v_mfma_f32_16x16x32_bf16 v[16:19], v[168:171], v[208:211], v[16:19]
	v_mfma_f32_16x16x32_bf16 v[12:15], v[176:179], v[208:211], v[12:15]
	v_mfma_f32_16x16x32_bf16 v[8:11], v[168:171], v[216:219], v[8:11]
	v_mfma_f32_16x16x32_bf16 v[4:7], v[176:179], v[216:219], v[4:7]
	v_mfma_f32_16x16x32_bf16 v[48:51], v[172:175], v[188:191], v[48:51]
	v_mfma_f32_16x16x32_bf16 v[44:47], v[180:183], v[188:191], v[44:47]
	v_mfma_f32_16x16x32_bf16 v[32:35], v[172:175], v[204:207], v[32:35]
	v_mfma_f32_16x16x32_bf16 v[28:31], v[180:183], v[204:207], v[28:31]
	v_mfma_f32_16x16x32_bf16 v[16:19], v[172:175], v[212:215], v[16:19]
	v_mfma_f32_16x16x32_bf16 v[12:15], v[180:183], v[212:215], v[12:15]
	v_mfma_f32_16x16x32_bf16 v[8:11], v[172:175], v[220:223], v[8:11]
	v_mfma_f32_16x16x32_bf16 v[4:7], v[180:183], v[220:223], v[4:7]
	s_setprio 0
	s_barrier
	s_add_i32 s68, s68, 2
	s_add_u32 s48, s48, 0x100
	s_addc_u32 s49, s49, 0
	s_cmp_gt_u32 s68, 13
	s_cbranch_scc0 .LBB0_311
	s_and_b64 vcc, exec, s[18:19]
	s_mov_b32 s62, 0x18000
	s_mov_b32 s63, 0x1a000
	s_cbranch_vccz .LBB0_314
	s_barrier

.LBB0_382:
	s_ashr_i32 s51, s50, 31
	s_lshl_b64 s[4:5], s[50:51], 19
	s_add_u32 s64, s8, s4
	s_addc_u32 s65, s9, s5
	s_and_b64 s[4:5], s[38:39], exec
	s_cselect_b32 s51, s65, s41
	s_cselect_b32 s71, s64, s40
	s_ashr_i32 s11, s10, 31
	s_lshl_b64 s[4:5], s[10:11], 18
	s_add_u32 s36, s16, s4
	s_addc_u32 s37, s17, s5
	s_and_b64 s[4:5], s[38:39], exec
	s_cselect_b32 s11, s37, s43
	s_cselect_b32 s74, s36, s42
	s_add_u32 s75, s71, 0x80
	s_addc_u32 s76, s51, 0
	s_add_u32 s4, s40, 0x40080
	s_addc_u32 s5, s41, 0
	s_add_u32 s77, s42, 0x100
	v_lshl_add_u64 v[100:101], s[4:5], 0, v[176:177]
	v_lshl_add_u64 v[102:103], s[4:5], 0, v[178:179]
	s_addc_u32 s78, s43, 0
	s_mov_b32 s79, -2
	s_mov_b64 s[42:43], 0
	s_add_u32 s4, s40, s42
	s_addc_u32 s5, s41, s43
	s_add_u32 s98, s4, 0x40080
	s_addc_u32 s99, s5, 0
	s_add_u32 s80, s4, 0x100
	s_addc_u32 s81, s5, 0
	s_add_u32 s48, s77, s42
	s_addc_u32 s49, s78, s43
	s_add_u32 s4, s4, 0x180
	s_addc_u32 s5, s5, 0
	s_add_i32 s82, 0, 0x10000
	s_add_i32 s83, 0, 0x14000
	v_add_u32_e32 v2, s82, v203
	ds_read_b128 v[104:107], v2
	ds_read_b128 v[124:127], v2 offset:1024
	ds_read_b128 v[128:131], v2 offset:2048
	ds_read_b128 v[148:151], v2 offset:3072
	v_add_u32_e32 v2, s83, v203
	ds_read_b128 v[152:155], v2
	ds_read_b128 v[156:159], v2 offset:1024
	ds_read_b128 v[160:163], v2 offset:2048
	ds_read_b128 v[164:167], v2 offset:3072
	s_cmpk_eq_i32 s42, 0x300
	s_cselect_b32 s45, s76, s5
	s_cselect_b32 s44, s75, s4
	s_cselect_b32 s49, s11, s49
	s_cselect_b32 s48, s74, s48
	s_cselect_b32 s5, s51, s81
	s_cselect_b32 s4, s71, s80
	s_add_i32 m0, s47, 0xc000
	ds_read_b128 v[180:183], v210
	ds_read_b128 v[184:187], v210 offset:1024
	ds_read_b128 v[188:191], v210 offset:2048
	ds_read_b128 v[192:195], v210 offset:3072
	ds_read_b128 v[204:207], v210 offset:4096
	ds_read_b128 v[212:215], v210 offset:5120
	ds_read_b128 v[216:219], v210 offset:6144
	ds_read_b128 v[220:223], v210 offset:7168
	global_load_lds_dwordx4 v176, s[98:99]
	s_add_i32 m0, s47, 0xe000
	s_nop 0
	global_load_lds_dwordx4 v178, s[98:99]
	s_waitcnt vmcnt(8)
	s_waitcnt lgkmcnt(0)
	s_barrier
	s_setprio 1
	v_mfma_f32_16x16x32_bf16 v[144:147], v[104:107], v[180:183], 0
	v_mfma_f32_16x16x32_bf16 v[140:143], v[128:131], v[180:183], 0
	v_mfma_f32_16x16x32_bf16 v[120:123], v[104:107], v[188:191], 0
	v_mfma_f32_16x16x32_bf16 v[116:119], v[128:131], v[188:191], 0
	v_mfma_f32_16x16x32_bf16 v[96:99], v[104:107], v[204:207], 0
	v_mfma_f32_16x16x32_bf16 v[92:95], v[128:131], v[204:207], 0
	v_mfma_f32_16x16x32_bf16 v[80:83], v[104:107], v[216:219], 0
	v_mfma_f32_16x16x32_bf16 v[76:79], v[128:131], v[216:219], 0
	v_mfma_f32_16x16x32_bf16 v[144:147], v[124:127], v[184:187], v[144:147]
	v_mfma_f32_16x16x32_bf16 v[140:143], v[148:151], v[184:187], v[140:143]
	v_mfma_f32_16x16x32_bf16 v[120:123], v[124:127], v[192:195], v[120:123]
	v_mfma_f32_16x16x32_bf16 v[116:119], v[148:151], v[192:195], v[116:119]
	v_mfma_f32_16x16x32_bf16 v[96:99], v[124:127], v[212:215], v[96:99]
	v_mfma_f32_16x16x32_bf16 v[92:95], v[148:151], v[212:215], v[92:95]
	v_mfma_f32_16x16x32_bf16 v[80:83], v[124:127], v[220:223], v[80:83]
	v_mfma_f32_16x16x32_bf16 v[76:79], v[148:151], v[220:223], v[76:79]
	v_mfma_f32_16x16x32_bf16 v[136:139], v[152:155], v[180:183], 0
	v_mfma_f32_16x16x32_bf16 v[132:135], v[160:163], v[180:183], 0
	v_mfma_f32_16x16x32_bf16 v[112:115], v[152:155], v[188:191], 0
	v_mfma_f32_16x16x32_bf16 v[108:111], v[160:163], v[188:191], 0
	v_mfma_f32_16x16x32_bf16 v[88:91], v[152:155], v[204:207], 0
	v_mfma_f32_16x16x32_bf16 v[84:87], v[160:163], v[204:207], 0
	v_mfma_f32_16x16x32_bf16 v[72:75], v[152:155], v[216:219], 0
	v_mfma_f32_16x16x32_bf16 v[68:71], v[160:163], v[216:219], 0
	v_mfma_f32_16x16x32_bf16 v[136:139], v[156:159], v[184:187], v[136:139]
	v_mfma_f32_16x16x32_bf16 v[132:135], v[164:167], v[184:187], v[132:135]
	v_mfma_f32_16x16x32_bf16 v[112:115], v[156:159], v[192:195], v[112:115]
	v_mfma_f32_16x16x32_bf16 v[108:111], v[164:167], v[192:195], v[108:111]
	v_mfma_f32_16x16x32_bf16 v[88:91], v[156:159], v[212:215], v[88:91]
	v_mfma_f32_16x16x32_bf16 v[84:87], v[164:167], v[212:215], v[84:87]
	v_mfma_f32_16x16x32_bf16 v[72:75], v[156:159], v[220:223], v[72:75]
	v_mfma_f32_16x16x32_bf16 v[68:71], v[164:167], v[220:223], v[68:71]
	s_setprio 0
	s_barrier
	s_add_i32 s80, s82, s46
	s_mov_b32 m0, s80
	ds_read_b128 v[180:183], v210 offset:16384
	ds_read_b128 v[184:187], v210 offset:17408
	ds_read_b128 v[188:191], v210 offset:18432
	ds_read_b128 v[192:195], v210 offset:19456
	ds_read_b128 v[204:207], v210 offset:20480
	ds_read_b128 v[212:215], v210 offset:21504
	ds_read_b128 v[216:219], v210 offset:22528
	ds_read_b128 v[220:223], v210 offset:23552
	global_load_lds_dwordx4 v172, s[48:49]
	s_add_i32 m0, s80, 0x2000
	s_add_u32 s80, s48, 0x20000
	s_addc_u32 s81, s49, 0
	s_add_i32 s82, s83, s46
	global_load_lds_dwordx4 v168, s[48:49]
	s_mov_b32 m0, s82
	s_nop 0
	global_load_lds_dwordx4 v172, s[80:81]
	s_add_i32 m0, s82, 0x2000
	s_nop 0
	global_load_lds_dwordx4 v168, s[80:81]
	s_mov_b32 m0, s47
	s_nop 0
	global_load_lds_dwordx4 v174, s[4:5]
	s_mov_b32 m0, s56
	s_nop 0
	global_load_lds_dwordx4 v170, s[4:5]
	s_waitcnt vmcnt(8)
	s_waitcnt lgkmcnt(0)
	s_barrier
	s_setprio 1
	v_mfma_f32_16x16x32_bf16 v[64:67], v[104:107], v[180:183], 0
	v_mfma_f32_16x16x32_bf16 v[60:63], v[128:131], v[180:183], 0
	v_mfma_f32_16x16x32_bf16 v[48:51], v[104:107], v[188:191], 0
	v_mfma_f32_16x16x32_bf16 v[44:47], v[128:131], v[188:191], 0
	v_mfma_f32_16x16x32_bf16 v[32:35], v[104:107], v[204:207], 0
	v_mfma_f32_16x16x32_bf16 v[28:31], v[128:131], v[204:207], 0
	v_mfma_f32_16x16x32_bf16 v[16:19], v[104:107], v[216:219], 0
	v_mfma_f32_16x16x32_bf16 v[12:15], v[128:131], v[216:219], 0
	v_mfma_f32_16x16x32_bf16 v[64:67], v[124:127], v[184:187], v[64:67]
	v_mfma_f32_16x16x32_bf16 v[60:63], v[148:151], v[184:187], v[60:63]
	v_mfma_f32_16x16x32_bf16 v[48:51], v[124:127], v[192:195], v[48:51]
	v_mfma_f32_16x16x32_bf16 v[44:47], v[148:151], v[192:195], v[44:47]
	v_mfma_f32_16x16x32_bf16 v[32:35], v[124:127], v[212:215], v[32:35]
	v_mfma_f32_16x16x32_bf16 v[28:31], v[148:151], v[212:215], v[28:31]
	v_mfma_f32_16x16x32_bf16 v[16:19], v[124:127], v[220:223], v[16:19]
	v_mfma_f32_16x16x32_bf16 v[12:15], v[148:151], v[220:223], v[12:15]
	v_mfma_f32_16x16x32_bf16 v[56:59], v[152:155], v[180:183], 0
	v_mfma_f32_16x16x32_bf16 v[52:55], v[160:163], v[180:183], 0
	v_mfma_f32_16x16x32_bf16 v[40:43], v[152:155], v[188:191], 0
	v_mfma_f32_16x16x32_bf16 v[36:39], v[160:163], v[188:191], 0
	v_mfma_f32_16x16x32_bf16 v[24:27], v[152:155], v[204:207], 0
	v_mfma_f32_16x16x32_bf16 v[20:23], v[160:163], v[204:207], 0
	v_mfma_f32_16x16x32_bf16 v[8:11], v[152:155], v[216:219], 0
	v_mfma_f32_16x16x32_bf16 v[4:7], v[160:163], v[216:219], 0
	v_mfma_f32_16x16x32_bf16 v[56:59], v[156:159], v[184:187], v[56:59]
	v_mfma_f32_16x16x32_bf16 v[52:55], v[164:167], v[184:187], v[52:55]
	v_mfma_f32_16x16x32_bf16 v[40:43], v[156:159], v[192:195], v[40:43]
	v_mfma_f32_16x16x32_bf16 v[36:39], v[164:167], v[192:195], v[36:39]
	v_mfma_f32_16x16x32_bf16 v[24:27], v[156:159], v[212:215], v[24:27]
	v_mfma_f32_16x16x32_bf16 v[20:23], v[164:167], v[212:215], v[20:23]
	v_mfma_f32_16x16x32_bf16 v[8:11], v[156:159], v[220:223], v[8:11]
	v_mfma_f32_16x16x32_bf16 v[4:7], v[164:167], v[220:223], v[4:7]
	s_setprio 0
	s_barrier
	s_add_i32 s80, 0, 0x18000
	v_add_u32_e32 v2, s80, v203
	s_add_i32 s81, 0, 0x1c000
	ds_read_b128 v[104:107], v2
	ds_read_b128 v[124:127], v2 offset:1024
	ds_read_b128 v[128:131], v2 offset:2048
	ds_read_b128 v[148:151], v2 offset:3072
	v_add_u32_e32 v2, s81, v203
	ds_read_b128 v[152:155], v2
	ds_read_b128 v[156:159], v2 offset:1024
	ds_read_b128 v[160:163], v2 offset:2048
	ds_read_b128 v[164:167], v2 offset:3072
	s_add_u32 s4, s4, 0x40000
	s_addc_u32 s5, s5, 0
	s_mov_b32 m0, s58
	ds_read_b128 v[180:183], v210 offset:32768
	ds_read_b128 v[184:187], v210 offset:33792
	ds_read_b128 v[188:191], v210 offset:34816
	ds_read_b128 v[192:195], v210 offset:35840
	ds_read_b128 v[204:207], v210 offset:36864
	ds_read_b128 v[212:215], v210 offset:37888
	ds_read_b128 v[216:219], v210 offset:38912
	ds_read_b128 v[220:223], v210 offset:39936
	global_load_lds_dwordx4 v174, s[4:5]
	s_mov_b32 m0, s59
	s_nop 0
	global_load_lds_dwordx4 v170, s[4:5]
	s_waitcnt vmcnt(8)
	s_waitcnt lgkmcnt(0)
	s_barrier
	s_setprio 1
	v_mfma_f32_16x16x32_bf16 v[144:147], v[104:107], v[180:183], v[144:147]
	v_mfma_f32_16x16x32_bf16 v[140:143], v[128:131], v[180:183], v[140:143]
	v_mfma_f32_16x16x32_bf16 v[120:123], v[104:107], v[188:191], v[120:123]
	v_mfma_f32_16x16x32_bf16 v[116:119], v[128:131], v[188:191], v[116:119]
	v_mfma_f32_16x16x32_bf16 v[96:99], v[104:107], v[204:207], v[96:99]
	v_mfma_f32_16x16x32_bf16 v[92:95], v[128:131], v[204:207], v[92:95]
	v_mfma_f32_16x16x32_bf16 v[80:83], v[104:107], v[216:219], v[80:83]
	v_mfma_f32_16x16x32_bf16 v[76:79], v[128:131], v[216:219], v[76:79]
	v_mfma_f32_16x16x32_bf16 v[144:147], v[124:127], v[184:187], v[144:147]
	v_mfma_f32_16x16x32_bf16 v[140:143], v[148:151], v[184:187], v[140:143]
	v_mfma_f32_16x16x32_bf16 v[120:123], v[124:127], v[192:195], v[120:123]
	v_mfma_f32_16x16x32_bf16 v[116:119], v[148:151], v[192:195], v[116:119]
	v_mfma_f32_16x16x32_bf16 v[96:99], v[124:127], v[212:215], v[96:99]
	v_mfma_f32_16x16x32_bf16 v[92:95], v[148:151], v[212:215], v[92:95]
	v_mfma_f32_16x16x32_bf16 v[80:83], v[124:127], v[220:223], v[80:83]
	v_mfma_f32_16x16x32_bf16 v[76:79], v[148:151], v[220:223], v[76:79]
	v_mfma_f32_16x16x32_bf16 v[136:139], v[152:155], v[180:183], v[136:139]
	v_mfma_f32_16x16x32_bf16 v[132:135], v[160:163], v[180:183], v[132:135]
	v_mfma_f32_16x16x32_bf16 v[112:115], v[152:155], v[188:191], v[112:115]
	v_mfma_f32_16x16x32_bf16 v[108:111], v[160:163], v[188:191], v[108:111]
	v_mfma_f32_16x16x32_bf16 v[88:91], v[152:155], v[204:207], v[88:91]
	v_mfma_f32_16x16x32_bf16 v[84:87], v[160:163], v[204:207], v[84:87]
	v_mfma_f32_16x16x32_bf16 v[72:75], v[152:155], v[216:219], v[72:75]
	v_mfma_f32_16x16x32_bf16 v[68:71], v[160:163], v[216:219], v[68:71]
	v_mfma_f32_16x16x32_bf16 v[136:139], v[156:159], v[184:187], v[136:139]
	v_mfma_f32_16x16x32_bf16 v[132:135], v[164:167], v[184:187], v[132:135]
	v_mfma_f32_16x16x32_bf16 v[112:115], v[156:159], v[192:195], v[112:115]
	v_mfma_f32_16x16x32_bf16 v[108:111], v[164:167], v[192:195], v[108:111]
	v_mfma_f32_16x16x32_bf16 v[88:91], v[156:159], v[212:215], v[88:91]
	v_mfma_f32_16x16x32_bf16 v[84:87], v[164:167], v[212:215], v[84:87]
	v_mfma_f32_16x16x32_bf16 v[72:75], v[156:159], v[220:223], v[72:75]
	v_mfma_f32_16x16x32_bf16 v[68:71], v[164:167], v[220:223], v[68:71]
	s_setprio 0
	s_barrier
	s_add_i32 s4, s80, s46
	s_add_u32 s98, s48, 0x80
	s_addc_u32 s99, s49, 0
	s_mov_b32 m0, s4
	ds_read_b128 v[180:183], v210 offset:49152
	ds_read_b128 v[184:187], v210 offset:50176
	ds_read_b128 v[188:191], v210 offset:51200
	ds_read_b128 v[192:195], v210 offset:52224
	ds_read_b128 v[204:207], v210 offset:53248
	ds_read_b128 v[212:215], v210 offset:54272
	ds_read_b128 v[216:219], v210 offset:55296
	ds_read_b128 v[220:223], v210 offset:56320
	global_load_lds_dwordx4 v172, s[98:99]
	s_add_i32 m0, s4, 0x2000
	s_add_u32 s4, s48, 0x20080
	s_addc_u32 s5, s49, 0
	s_add_i32 s48, s81, s46
	global_load_lds_dwordx4 v168, s[98:99]
	s_mov_b32 m0, s48
	s_nop 0
	global_load_lds_dwordx4 v172, s[4:5]
	s_add_i32 m0, s48, 0x2000
	s_nop 0
	global_load_lds_dwordx4 v168, s[4:5]
	s_mov_b32 m0, s68
	s_nop 0
	global_load_lds_dwordx4 v174, s[44:45]
	s_mov_b32 m0, s69
	s_nop 0
	global_load_lds_dwordx4 v170, s[44:45]
	s_waitcnt vmcnt(8)
	s_waitcnt lgkmcnt(0)
	s_barrier
	s_setprio 1
	v_mfma_f32_16x16x32_bf16 v[64:67], v[104:107], v[180:183], v[64:67]
	v_mfma_f32_16x16x32_bf16 v[60:63], v[128:131], v[180:183], v[60:63]
	v_mfma_f32_16x16x32_bf16 v[48:51], v[104:107], v[188:191], v[48:51]
	v_mfma_f32_16x16x32_bf16 v[44:47], v[128:131], v[188:191], v[44:47]
	v_mfma_f32_16x16x32_bf16 v[32:35], v[104:107], v[204:207], v[32:35]
	v_mfma_f32_16x16x32_bf16 v[28:31], v[128:131], v[204:207], v[28:31]
	v_mfma_f32_16x16x32_bf16 v[16:19], v[104:107], v[216:219], v[16:19]
	v_mfma_f32_16x16x32_bf16 v[12:15], v[128:131], v[216:219], v[12:15]
	v_mfma_f32_16x16x32_bf16 v[64:67], v[124:127], v[184:187], v[64:67]
	v_mfma_f32_16x16x32_bf16 v[60:63], v[148:151], v[184:187], v[60:63]
	v_mfma_f32_16x16x32_bf16 v[48:51], v[124:127], v[192:195], v[48:51]
	v_mfma_f32_16x16x32_bf16 v[44:47], v[148:151], v[192:195], v[44:47]
	v_mfma_f32_16x16x32_bf16 v[32:35], v[124:127], v[212:215], v[32:35]
	v_mfma_f32_16x16x32_bf16 v[28:31], v[148:151], v[212:215], v[28:31]
	v_mfma_f32_16x16x32_bf16 v[16:19], v[124:127], v[220:223], v[16:19]
	v_mfma_f32_16x16x32_bf16 v[12:15], v[148:151], v[220:223], v[12:15]
	v_mfma_f32_16x16x32_bf16 v[56:59], v[152:155], v[180:183], v[56:59]
	v_mfma_f32_16x16x32_bf16 v[52:55], v[160:163], v[180:183], v[52:55]
	v_mfma_f32_16x16x32_bf16 v[40:43], v[152:155], v[188:191], v[40:43]
	v_mfma_f32_16x16x32_bf16 v[36:39], v[160:163], v[188:191], v[36:39]
	v_mfma_f32_16x16x32_bf16 v[24:27], v[152:155], v[204:207], v[24:27]
	v_mfma_f32_16x16x32_bf16 v[20:23], v[160:163], v[204:207], v[20:23]
	v_mfma_f32_16x16x32_bf16 v[8:11], v[152:155], v[216:219], v[8:11]
	v_mfma_f32_16x16x32_bf16 v[4:7], v[160:163], v[216:219], v[4:7]
	v_mfma_f32_16x16x32_bf16 v[56:59], v[156:159], v[184:187], v[56:59]
	v_mfma_f32_16x16x32_bf16 v[52:55], v[164:167], v[184:187], v[52:55]
	v_mfma_f32_16x16x32_bf16 v[40:43], v[156:159], v[192:195], v[40:43]
	v_mfma_f32_16x16x32_bf16 v[36:39], v[164:167], v[192:195], v[36:39]
	v_mfma_f32_16x16x32_bf16 v[24:27], v[156:159], v[212:215], v[24:27]
	v_mfma_f32_16x16x32_bf16 v[20:23], v[164:167], v[212:215], v[20:23]
	v_mfma_f32_16x16x32_bf16 v[8:11], v[156:159], v[220:223], v[8:11]
	v_mfma_f32_16x16x32_bf16 v[4:7], v[164:167], v[220:223], v[4:7]
	s_setprio 0
	s_barrier
	s_add_i32 s79, s79, 2
	s_add_u32 s42, s42, 0x100
	s_addc_u32 s43, s43, 0
	s_cmp_gt_u32 s79, 5
.LBB0_383:
	s_add_u32 s4, s40, s42
	s_addc_u32 s5, s41, s43
	s_add_u32 s98, s4, 0x40080
	s_addc_u32 s99, s5, 0
	s_add_u32 s80, s4, 0x100
	s_addc_u32 s81, s5, 0
	s_add_u32 s48, s77, s42
	s_addc_u32 s49, s78, s43
	s_add_u32 s4, s4, 0x180
	s_addc_u32 s5, s5, 0
	s_add_i32 s82, 0, 0x10000
	s_add_i32 s83, 0, 0x14000
	v_add_u32_e32 v2, s82, v203
	ds_read_b128 v[104:107], v2
	ds_read_b128 v[124:127], v2 offset:1024
	ds_read_b128 v[128:131], v2 offset:2048
	ds_read_b128 v[148:151], v2 offset:3072
	v_add_u32_e32 v2, s83, v203
	ds_read_b128 v[152:155], v2
	ds_read_b128 v[156:159], v2 offset:1024
	ds_read_b128 v[160:163], v2 offset:2048
	ds_read_b128 v[164:167], v2 offset:3072
	s_cmpk_eq_i32 s42, 0x300
	s_cselect_b32 s45, s76, s5
	s_cselect_b32 s44, s75, s4
	s_cselect_b32 s49, s11, s49
	s_cselect_b32 s48, s74, s48
	s_cselect_b32 s5, s51, s81
	s_cselect_b32 s4, s71, s80
	s_add_i32 m0, s47, 0xc000
	ds_read_b128 v[180:183], v210
	ds_read_b128 v[184:187], v210 offset:1024
	ds_read_b128 v[188:191], v210 offset:2048
	ds_read_b128 v[192:195], v210 offset:3072
	ds_read_b128 v[204:207], v210 offset:4096
	ds_read_b128 v[212:215], v210 offset:5120
	ds_read_b128 v[216:219], v210 offset:6144
	ds_read_b128 v[220:223], v210 offset:7168
	global_load_lds_dwordx4 v176, s[98:99]
	s_add_i32 m0, s47, 0xe000
	s_nop 0
	global_load_lds_dwordx4 v178, s[98:99]
	s_waitcnt vmcnt(8)
	s_waitcnt lgkmcnt(0)
	s_barrier
	s_setprio 1
	v_mfma_f32_16x16x32_bf16 v[144:147], v[104:107], v[180:183], v[144:147]
	v_mfma_f32_16x16x32_bf16 v[140:143], v[128:131], v[180:183], v[140:143]
	v_mfma_f32_16x16x32_bf16 v[120:123], v[104:107], v[188:191], v[120:123]
	v_mfma_f32_16x16x32_bf16 v[116:119], v[128:131], v[188:191], v[116:119]
	v_mfma_f32_16x16x32_bf16 v[96:99], v[104:107], v[204:207], v[96:99]
	v_mfma_f32_16x16x32_bf16 v[92:95], v[128:131], v[204:207], v[92:95]
	v_mfma_f32_16x16x32_bf16 v[80:83], v[104:107], v[216:219], v[80:83]
	v_mfma_f32_16x16x32_bf16 v[76:79], v[128:131], v[216:219], v[76:79]
	v_mfma_f32_16x16x32_bf16 v[144:147], v[124:127], v[184:187], v[144:147]
	v_mfma_f32_16x16x32_bf16 v[140:143], v[148:151], v[184:187], v[140:143]
	v_mfma_f32_16x16x32_bf16 v[120:123], v[124:127], v[192:195], v[120:123]
	v_mfma_f32_16x16x32_bf16 v[116:119], v[148:151], v[192:195], v[116:119]
	v_mfma_f32_16x16x32_bf16 v[96:99], v[124:127], v[212:215], v[96:99]
	v_mfma_f32_16x16x32_bf16 v[92:95], v[148:151], v[212:215], v[92:95]
	v_mfma_f32_16x16x32_bf16 v[80:83], v[124:127], v[220:223], v[80:83]
	v_mfma_f32_16x16x32_bf16 v[76:79], v[148:151], v[220:223], v[76:79]
	v_mfma_f32_16x16x32_bf16 v[136:139], v[152:155], v[180:183], v[136:139]
	v_mfma_f32_16x16x32_bf16 v[132:135], v[160:163], v[180:183], v[132:135]
	v_mfma_f32_16x16x32_bf16 v[112:115], v[152:155], v[188:191], v[112:115]
	v_mfma_f32_16x16x32_bf16 v[108:111], v[160:163], v[188:191], v[108:111]
	v_mfma_f32_16x16x32_bf16 v[88:91], v[152:155], v[204:207], v[88:91]
	v_mfma_f32_16x16x32_bf16 v[84:87], v[160:163], v[204:207], v[84:87]
	v_mfma_f32_16x16x32_bf16 v[72:75], v[152:155], v[216:219], v[72:75]
	v_mfma_f32_16x16x32_bf16 v[68:71], v[160:163], v[216:219], v[68:71]
	v_mfma_f32_16x16x32_bf16 v[136:139], v[156:159], v[184:187], v[136:139]
	v_mfma_f32_16x16x32_bf16 v[132:135], v[164:167], v[184:187], v[132:135]
	v_mfma_f32_16x16x32_bf16 v[112:115], v[156:159], v[192:195], v[112:115]
	v_mfma_f32_16x16x32_bf16 v[108:111], v[164:167], v[192:195], v[108:111]
	v_mfma_f32_16x16x32_bf16 v[88:91], v[156:159], v[212:215], v[88:91]
	v_mfma_f32_16x16x32_bf16 v[84:87], v[164:167], v[212:215], v[84:87]
	v_mfma_f32_16x16x32_bf16 v[72:75], v[156:159], v[220:223], v[72:75]
	v_mfma_f32_16x16x32_bf16 v[68:71], v[164:167], v[220:223], v[68:71]
	s_setprio 0
	s_barrier
	s_add_i32 s80, s82, s46
	s_mov_b32 m0, s80
	ds_read_b128 v[180:183], v210 offset:16384
	ds_read_b128 v[184:187], v210 offset:17408
	ds_read_b128 v[188:191], v210 offset:18432
	ds_read_b128 v[192:195], v210 offset:19456
	ds_read_b128 v[204:207], v210 offset:20480
	ds_read_b128 v[212:215], v210 offset:21504
	ds_read_b128 v[216:219], v210 offset:22528
	ds_read_b128 v[220:223], v210 offset:23552
	global_load_lds_dwordx4 v172, s[48:49]
	s_add_i32 m0, s80, 0x2000
	s_add_u32 s80, s48, 0x20000
	s_addc_u32 s81, s49, 0
	s_add_i32 s82, s83, s46
	global_load_lds_dwordx4 v168, s[48:49]
	s_mov_b32 m0, s82
	s_nop 0
	global_load_lds_dwordx4 v172, s[80:81]
	s_add_i32 m0, s82, 0x2000
	s_nop 0
	global_load_lds_dwordx4 v168, s[80:81]
	s_mov_b32 m0, s47
	s_nop 0
	global_load_lds_dwordx4 v174, s[4:5]
	s_mov_b32 m0, s56
	s_nop 0
	global_load_lds_dwordx4 v170, s[4:5]
	s_waitcnt vmcnt(8)
	s_waitcnt lgkmcnt(0)
	s_barrier
	s_setprio 1
	v_mfma_f32_16x16x32_bf16 v[64:67], v[104:107], v[180:183], v[64:67]
	v_mfma_f32_16x16x32_bf16 v[60:63], v[128:131], v[180:183], v[60:63]
	v_mfma_f32_16x16x32_bf16 v[48:51], v[104:107], v[188:191], v[48:51]
	v_mfma_f32_16x16x32_bf16 v[44:47], v[128:131], v[188:191], v[44:47]
	v_mfma_f32_16x16x32_bf16 v[32:35], v[104:107], v[204:207], v[32:35]
	v_mfma_f32_16x16x32_bf16 v[28:31], v[128:131], v[204:207], v[28:31]
	v_mfma_f32_16x16x32_bf16 v[16:19], v[104:107], v[216:219], v[16:19]
	v_mfma_f32_16x16x32_bf16 v[12:15], v[128:131], v[216:219], v[12:15]
	v_mfma_f32_16x16x32_bf16 v[64:67], v[124:127], v[184:187], v[64:67]
	v_mfma_f32_16x16x32_bf16 v[60:63], v[148:151], v[184:187], v[60:63]
	v_mfma_f32_16x16x32_bf16 v[48:51], v[124:127], v[192:195], v[48:51]
	v_mfma_f32_16x16x32_bf16 v[44:47], v[148:151], v[192:195], v[44:47]
	v_mfma_f32_16x16x32_bf16 v[32:35], v[124:127], v[212:215], v[32:35]
	v_mfma_f32_16x16x32_bf16 v[28:31], v[148:151], v[212:215], v[28:31]
	v_mfma_f32_16x16x32_bf16 v[16:19], v[124:127], v[220:223], v[16:19]
	v_mfma_f32_16x16x32_bf16 v[12:15], v[148:151], v[220:223], v[12:15]
	v_mfma_f32_16x16x32_bf16 v[56:59], v[152:155], v[180:183], v[56:59]
	v_mfma_f32_16x16x32_bf16 v[52:55], v[160:163], v[180:183], v[52:55]
	v_mfma_f32_16x16x32_bf16 v[40:43], v[152:155], v[188:191], v[40:43]
	v_mfma_f32_16x16x32_bf16 v[36:39], v[160:163], v[188:191], v[36:39]
	v_mfma_f32_16x16x32_bf16 v[24:27], v[152:155], v[204:207], v[24:27]
	v_mfma_f32_16x16x32_bf16 v[20:23], v[160:163], v[204:207], v[20:23]
	v_mfma_f32_16x16x32_bf16 v[8:11], v[152:155], v[216:219], v[8:11]
	v_mfma_f32_16x16x32_bf16 v[4:7], v[160:163], v[216:219], v[4:7]
	v_mfma_f32_16x16x32_bf16 v[56:59], v[156:159], v[184:187], v[56:59]
	v_mfma_f32_16x16x32_bf16 v[52:55], v[164:167], v[184:187], v[52:55]
	v_mfma_f32_16x16x32_bf16 v[40:43], v[156:159], v[192:195], v[40:43]
	v_mfma_f32_16x16x32_bf16 v[36:39], v[164:167], v[192:195], v[36:39]
	v_mfma_f32_16x16x32_bf16 v[24:27], v[156:159], v[212:215], v[24:27]
	v_mfma_f32_16x16x32_bf16 v[20:23], v[164:167], v[212:215], v[20:23]
	v_mfma_f32_16x16x32_bf16 v[8:11], v[156:159], v[220:223], v[8:11]
	v_mfma_f32_16x16x32_bf16 v[4:7], v[164:167], v[220:223], v[4:7]
	s_setprio 0
	s_barrier
	s_add_i32 s80, 0, 0x18000
	v_add_u32_e32 v2, s80, v203
	s_add_i32 s81, 0, 0x1c000
	ds_read_b128 v[104:107], v2
	ds_read_b128 v[124:127], v2 offset:1024
	ds_read_b128 v[128:131], v2 offset:2048
	ds_read_b128 v[148:151], v2 offset:3072
	v_add_u32_e32 v2, s81, v203
	ds_read_b128 v[152:155], v2
	ds_read_b128 v[156:159], v2 offset:1024
	ds_read_b128 v[160:163], v2 offset:2048
	ds_read_b128 v[164:167], v2 offset:3072
	s_add_u32 s4, s4, 0x40000
	s_addc_u32 s5, s5, 0
	s_mov_b32 m0, s58
	ds_read_b128 v[180:183], v210 offset:32768
	ds_read_b128 v[184:187], v210 offset:33792
	ds_read_b128 v[188:191], v210 offset:34816
	ds_read_b128 v[192:195], v210 offset:35840
	ds_read_b128 v[204:207], v210 offset:36864
	ds_read_b128 v[212:215], v210 offset:37888
	ds_read_b128 v[216:219], v210 offset:38912
	ds_read_b128 v[220:223], v210 offset:39936
	global_load_lds_dwordx4 v174, s[4:5]
	s_mov_b32 m0, s59
	s_nop 0
	global_load_lds_dwordx4 v170, s[4:5]
	s_waitcnt vmcnt(8)
	s_waitcnt lgkmcnt(0)
	s_barrier
	s_setprio 1
	v_mfma_f32_16x16x32_bf16 v[144:147], v[104:107], v[180:183], v[144:147]
	v_mfma_f32_16x16x32_bf16 v[140:143], v[128:131], v[180:183], v[140:143]
	v_mfma_f32_16x16x32_bf16 v[120:123], v[104:107], v[188:191], v[120:123]
	v_mfma_f32_16x16x32_bf16 v[116:119], v[128:131], v[188:191], v[116:119]
	v_mfma_f32_16x16x32_bf16 v[96:99], v[104:107], v[204:207], v[96:99]
	v_mfma_f32_16x16x32_bf16 v[92:95], v[128:131], v[204:207], v[92:95]
	v_mfma_f32_16x16x32_bf16 v[80:83], v[104:107], v[216:219], v[80:83]
	v_mfma_f32_16x16x32_bf16 v[76:79], v[128:131], v[216:219], v[76:79]
	v_mfma_f32_16x16x32_bf16 v[144:147], v[124:127], v[184:187], v[144:147]
	v_mfma_f32_16x16x32_bf16 v[140:143], v[148:151], v[184:187], v[140:143]
	v_mfma_f32_16x16x32_bf16 v[120:123], v[124:127], v[192:195], v[120:123]
	v_mfma_f32_16x16x32_bf16 v[116:119], v[148:151], v[192:195], v[116:119]
	v_mfma_f32_16x16x32_bf16 v[96:99], v[124:127], v[212:215], v[96:99]
	v_mfma_f32_16x16x32_bf16 v[92:95], v[148:151], v[212:215], v[92:95]
	v_mfma_f32_16x16x32_bf16 v[80:83], v[124:127], v[220:223], v[80:83]
	v_mfma_f32_16x16x32_bf16 v[76:79], v[148:151], v[220:223], v[76:79]
	v_mfma_f32_16x16x32_bf16 v[136:139], v[152:155], v[180:183], v[136:139]
	v_mfma_f32_16x16x32_bf16 v[132:135], v[160:163], v[180:183], v[132:135]
	v_mfma_f32_16x16x32_bf16 v[112:115], v[152:155], v[188:191], v[112:115]
	v_mfma_f32_16x16x32_bf16 v[108:111], v[160:163], v[188:191], v[108:111]
	v_mfma_f32_16x16x32_bf16 v[88:91], v[152:155], v[204:207], v[88:91]
	v_mfma_f32_16x16x32_bf16 v[84:87], v[160:163], v[204:207], v[84:87]
	v_mfma_f32_16x16x32_bf16 v[72:75], v[152:155], v[216:219], v[72:75]
	v_mfma_f32_16x16x32_bf16 v[68:71], v[160:163], v[216:219], v[68:71]
	v_mfma_f32_16x16x32_bf16 v[136:139], v[156:159], v[184:187], v[136:139]
	v_mfma_f32_16x16x32_bf16 v[132:135], v[164:167], v[184:187], v[132:135]
	v_mfma_f32_16x16x32_bf16 v[112:115], v[156:159], v[192:195], v[112:115]
	v_mfma_f32_16x16x32_bf16 v[108:111], v[164:167], v[192:195], v[108:111]
	v_mfma_f32_16x16x32_bf16 v[88:91], v[156:159], v[212:215], v[88:91]
	v_mfma_f32_16x16x32_bf16 v[84:87], v[164:167], v[212:215], v[84:87]
	v_mfma_f32_16x16x32_bf16 v[72:75], v[156:159], v[220:223], v[72:75]
	v_mfma_f32_16x16x32_bf16 v[68:71], v[164:167], v[220:223], v[68:71]
	s_setprio 0
	s_barrier
	s_add_i32 s4, s80, s46
	s_add_u32 s98, s48, 0x80
	s_addc_u32 s99, s49, 0
	s_mov_b32 m0, s4
	ds_read_b128 v[180:183], v210 offset:49152
	ds_read_b128 v[184:187], v210 offset:50176
	ds_read_b128 v[188:191], v210 offset:51200
	ds_read_b128 v[192:195], v210 offset:52224
	ds_read_b128 v[204:207], v210 offset:53248
	ds_read_b128 v[212:215], v210 offset:54272
	ds_read_b128 v[216:219], v210 offset:55296
	ds_read_b128 v[220:223], v210 offset:56320
	global_load_lds_dwordx4 v172, s[98:99]
	s_add_i32 m0, s4, 0x2000
	s_add_u32 s4, s48, 0x20080
	s_addc_u32 s5, s49, 0
	s_add_i32 s48, s81, s46
	global_load_lds_dwordx4 v168, s[98:99]
	s_mov_b32 m0, s48
	s_nop 0
	global_load_lds_dwordx4 v172, s[4:5]
	s_add_i32 m0, s48, 0x2000
	s_nop 0
	global_load_lds_dwordx4 v168, s[4:5]
	s_mov_b32 m0, s68
	s_nop 0
	global_load_lds_dwordx4 v174, s[44:45]
	s_mov_b32 m0, s69
	s_nop 0
	global_load_lds_dwordx4 v170, s[44:45]
	s_waitcnt vmcnt(8)
	s_waitcnt lgkmcnt(0)
	s_barrier
	s_setprio 1
	v_mfma_f32_16x16x32_bf16 v[64:67], v[104:107], v[180:183], v[64:67]
	v_mfma_f32_16x16x32_bf16 v[60:63], v[128:131], v[180:183], v[60:63]
	v_mfma_f32_16x16x32_bf16 v[48:51], v[104:107], v[188:191], v[48:51]
	v_mfma_f32_16x16x32_bf16 v[44:47], v[128:131], v[188:191], v[44:47]
	v_mfma_f32_16x16x32_bf16 v[32:35], v[104:107], v[204:207], v[32:35]
	v_mfma_f32_16x16x32_bf16 v[28:31], v[128:131], v[204:207], v[28:31]
	v_mfma_f32_16x16x32_bf16 v[16:19], v[104:107], v[216:219], v[16:19]
	v_mfma_f32_16x16x32_bf16 v[12:15], v[128:131], v[216:219], v[12:15]
	v_mfma_f32_16x16x32_bf16 v[64:67], v[124:127], v[184:187], v[64:67]
	v_mfma_f32_16x16x32_bf16 v[60:63], v[148:151], v[184:187], v[60:63]
	v_mfma_f32_16x16x32_bf16 v[48:51], v[124:127], v[192:195], v[48:51]
	v_mfma_f32_16x16x32_bf16 v[44:47], v[148:151], v[192:195], v[44:47]
	v_mfma_f32_16x16x32_bf16 v[32:35], v[124:127], v[212:215], v[32:35]
	v_mfma_f32_16x16x32_bf16 v[28:31], v[148:151], v[212:215], v[28:31]
	v_mfma_f32_16x16x32_bf16 v[16:19], v[124:127], v[220:223], v[16:19]
	v_mfma_f32_16x16x32_bf16 v[12:15], v[148:151], v[220:223], v[12:15]
	v_mfma_f32_16x16x32_bf16 v[56:59], v[152:155], v[180:183], v[56:59]
	v_mfma_f32_16x16x32_bf16 v[52:55], v[160:163], v[180:183], v[52:55]
	v_mfma_f32_16x16x32_bf16 v[40:43], v[152:155], v[188:191], v[40:43]
	v_mfma_f32_16x16x32_bf16 v[36:39], v[160:163], v[188:191], v[36:39]
	v_mfma_f32_16x16x32_bf16 v[24:27], v[152:155], v[204:207], v[24:27]
	v_mfma_f32_16x16x32_bf16 v[20:23], v[160:163], v[204:207], v[20:23]
	v_mfma_f32_16x16x32_bf16 v[8:11], v[152:155], v[216:219], v[8:11]
	v_mfma_f32_16x16x32_bf16 v[4:7], v[160:163], v[216:219], v[4:7]
	v_mfma_f32_16x16x32_bf16 v[56:59], v[156:159], v[184:187], v[56:59]
	v_mfma_f32_16x16x32_bf16 v[52:55], v[164:167], v[184:187], v[52:55]
	v_mfma_f32_16x16x32_bf16 v[40:43], v[156:159], v[192:195], v[40:43]
	v_mfma_f32_16x16x32_bf16 v[36:39], v[164:167], v[192:195], v[36:39]
	v_mfma_f32_16x16x32_bf16 v[24:27], v[156:159], v[212:215], v[24:27]
	v_mfma_f32_16x16x32_bf16 v[20:23], v[164:167], v[212:215], v[20:23]
	v_mfma_f32_16x16x32_bf16 v[8:11], v[156:159], v[220:223], v[8:11]
	v_mfma_f32_16x16x32_bf16 v[4:7], v[164:167], v[220:223], v[4:7]
	s_setprio 0
	s_barrier
	s_add_i32 s79, s79, 2
	s_add_u32 s42, s42, 0x100
	s_addc_u32 s43, s43, 0
	s_cmp_gt_u32 s79, 5
	s_cbranch_scc0 .LBB0_383
	s_and_b64 vcc, exec, s[72:73]
	s_cbranch_vccz .LBB0_386
	s_barrier

.LBB0_1043:
	s_ashr_i32 s41, s40, 31
	s_lshl_b64 s[4:5], s[40:41], 19
	s_add_u32 s42, s6, s4
	s_addc_u32 s43, s7, s5
	s_and_b64 s[4:5], s[38:39], exec
	s_cselect_b32 s41, s43, s49
	s_cselect_b32 s65, s42, s48
	s_ashr_i32 s37, s36, 31
	s_lshl_b64 s[4:5], s[36:37], 19
	s_add_u32 s44, s8, s4
	s_addc_u32 s45, s9, s5
	s_and_b64 s[4:5], s[38:39], exec
	s_cselect_b32 s37, s45, s51
	s_cselect_b32 s68, s44, s50
	s_add_u32 s69, s65, 0x80
	s_addc_u32 s70, s41, 0
	s_add_u32 s4, s48, 0x40080
	s_addc_u32 s5, s49, 0
	s_add_u32 s71, s50, 0x100
	v_lshl_add_u64 v[140:141], s[4:5], 0, v[136:137]
	v_lshl_add_u64 v[142:143], s[4:5], 0, v[138:139]
	s_addc_u32 s72, s51, 0
	s_mov_b32 s73, -2
	s_mov_b64 s[50:51], 0
	s_waitcnt vmcnt(0)
	s_add_u32 s4, s48, s50
	s_addc_u32 s5, s49, s51
	s_add_u32 s98, s4, 0x40080
	s_addc_u32 s99, s5, 0
	s_add_u32 s74, s4, 0x100
	s_addc_u32 s75, s5, 0
	s_add_u32 s52, s71, s50
	s_addc_u32 s53, s72, s51
	s_add_u32 s4, s4, 0x180
	s_addc_u32 s5, s5, 0
	s_add_i32 s76, 0, 0x10000
	s_add_i32 s77, 0, 0x14000
	v_add_u32_e32 v2, s76, v203
	ds_read_b128 v[144:147], v2
	ds_read_b128 v[148:151], v2 offset:1024
	ds_read_b128 v[152:155], v2 offset:2048
	ds_read_b128 v[156:159], v2 offset:3072
	v_add_u32_e32 v2, s77, v203
	ds_read_b128 v[160:163], v2
	ds_read_b128 v[164:167], v2 offset:1024
	ds_read_b128 v[168:171], v2 offset:2048
	ds_read_b128 v[172:175], v2 offset:3072
	s_cmpk_eq_i32 s50, 0x700
	s_cselect_b32 s13, s70, s5
	s_cselect_b32 s12, s69, s4
	s_cselect_b32 s53, s37, s53
	s_cselect_b32 s52, s68, s52
	s_cselect_b32 s5, s41, s75
	s_cselect_b32 s4, s65, s74
	s_add_i32 m0, s17, 0xc000
	ds_read_b128 v[176:179], v224
	ds_read_b128 v[180:183], v224 offset:1024
	ds_read_b128 v[184:187], v224 offset:2048
	ds_read_b128 v[188:191], v224 offset:3072
	ds_read_b128 v[192:195], v224 offset:4096
	ds_read_b128 v[196:199], v224 offset:5120
	ds_read_b128 v[204:207], v224 offset:6144
	ds_read_b128 v[208:211], v224 offset:7168
	global_load_lds_dwordx4 v136, s[98:99]
	s_add_i32 m0, s17, 0xe000
	s_nop 0
	global_load_lds_dwordx4 v138, s[98:99]
	s_waitcnt vmcnt(8)
	s_waitcnt lgkmcnt(0)
	s_barrier
	s_setprio 1
	v_mfma_f32_16x16x32_bf16 v[128:131], v[144:147], v[176:179], 0
	v_mfma_f32_16x16x32_bf16 v[124:127], v[152:155], v[176:179], 0
	v_mfma_f32_16x16x32_bf16 v[112:115], v[144:147], v[184:187], 0
	v_mfma_f32_16x16x32_bf16 v[108:111], v[152:155], v[184:187], 0
	v_mfma_f32_16x16x32_bf16 v[96:99], v[144:147], v[192:195], 0
	v_mfma_f32_16x16x32_bf16 v[92:95], v[152:155], v[192:195], 0
	v_mfma_f32_16x16x32_bf16 v[80:83], v[144:147], v[204:207], 0
	v_mfma_f32_16x16x32_bf16 v[76:79], v[152:155], v[204:207], 0
	v_mfma_f32_16x16x32_bf16 v[128:131], v[148:151], v[180:183], v[128:131]
	v_mfma_f32_16x16x32_bf16 v[124:127], v[156:159], v[180:183], v[124:127]
	v_mfma_f32_16x16x32_bf16 v[112:115], v[148:151], v[188:191], v[112:115]
	v_mfma_f32_16x16x32_bf16 v[108:111], v[156:159], v[188:191], v[108:111]
	v_mfma_f32_16x16x32_bf16 v[96:99], v[148:151], v[196:199], v[96:99]
	v_mfma_f32_16x16x32_bf16 v[92:95], v[156:159], v[196:199], v[92:95]
	v_mfma_f32_16x16x32_bf16 v[80:83], v[148:151], v[208:211], v[80:83]
	v_mfma_f32_16x16x32_bf16 v[76:79], v[156:159], v[208:211], v[76:79]
	v_mfma_f32_16x16x32_bf16 v[120:123], v[160:163], v[176:179], 0
	v_mfma_f32_16x16x32_bf16 v[116:119], v[168:171], v[176:179], 0
	v_mfma_f32_16x16x32_bf16 v[104:107], v[160:163], v[184:187], 0
	v_mfma_f32_16x16x32_bf16 v[100:103], v[168:171], v[184:187], 0
	v_mfma_f32_16x16x32_bf16 v[88:91], v[160:163], v[192:195], 0
	v_mfma_f32_16x16x32_bf16 v[84:87], v[168:171], v[192:195], 0
	v_mfma_f32_16x16x32_bf16 v[72:75], v[160:163], v[204:207], 0
	v_mfma_f32_16x16x32_bf16 v[68:71], v[168:171], v[204:207], 0
	v_mfma_f32_16x16x32_bf16 v[120:123], v[164:167], v[180:183], v[120:123]
	v_mfma_f32_16x16x32_bf16 v[116:119], v[172:175], v[180:183], v[116:119]
	v_mfma_f32_16x16x32_bf16 v[104:107], v[164:167], v[188:191], v[104:107]
	v_mfma_f32_16x16x32_bf16 v[100:103], v[172:175], v[188:191], v[100:103]
	v_mfma_f32_16x16x32_bf16 v[88:91], v[164:167], v[196:199], v[88:91]
	v_mfma_f32_16x16x32_bf16 v[84:87], v[172:175], v[196:199], v[84:87]
	v_mfma_f32_16x16x32_bf16 v[72:75], v[164:167], v[208:211], v[72:75]
	v_mfma_f32_16x16x32_bf16 v[68:71], v[172:175], v[208:211], v[68:71]
	s_setprio 0
	s_barrier
	s_add_i32 s74, s76, s16
	s_mov_b32 m0, s74
	ds_read_b128 v[176:179], v224 offset:16384
	ds_read_b128 v[180:183], v224 offset:17408
	ds_read_b128 v[184:187], v224 offset:18432
	ds_read_b128 v[188:191], v224 offset:19456
	ds_read_b128 v[192:195], v224 offset:20480
	ds_read_b128 v[196:199], v224 offset:21504
	ds_read_b128 v[204:207], v224 offset:22528
	ds_read_b128 v[208:211], v224 offset:23552
	global_load_lds_dwordx4 v134, s[52:53]
	s_add_i32 m0, s74, 0x2000
	s_add_u32 s74, s52, 0x40000
	s_addc_u32 s75, s53, 0
	s_add_i32 s76, s77, s16
	global_load_lds_dwordx4 v132, s[52:53]
	s_mov_b32 m0, s76
	s_nop 0
	global_load_lds_dwordx4 v134, s[74:75]
	s_add_i32 m0, s76, 0x2000
	s_nop 0
	global_load_lds_dwordx4 v132, s[74:75]
	s_mov_b32 m0, s17
	s_nop 0
	global_load_lds_dwordx4 v134, s[4:5]
	s_mov_b32 m0, s46
	s_nop 0
	global_load_lds_dwordx4 v132, s[4:5]
	s_waitcnt vmcnt(8)
	s_waitcnt lgkmcnt(0)
	s_barrier
	s_setprio 1
	v_mfma_f32_16x16x32_bf16 v[64:67], v[144:147], v[176:179], 0
	v_mfma_f32_16x16x32_bf16 v[60:63], v[152:155], v[176:179], 0
	v_mfma_f32_16x16x32_bf16 v[48:51], v[144:147], v[184:187], 0
	v_mfma_f32_16x16x32_bf16 v[44:47], v[152:155], v[184:187], 0
	v_mfma_f32_16x16x32_bf16 v[32:35], v[144:147], v[192:195], 0
	v_mfma_f32_16x16x32_bf16 v[28:31], v[152:155], v[192:195], 0
	v_mfma_f32_16x16x32_bf16 v[16:19], v[144:147], v[204:207], 0
	v_mfma_f32_16x16x32_bf16 v[12:15], v[152:155], v[204:207], 0
	v_mfma_f32_16x16x32_bf16 v[64:67], v[148:151], v[180:183], v[64:67]
	v_mfma_f32_16x16x32_bf16 v[60:63], v[156:159], v[180:183], v[60:63]
	v_mfma_f32_16x16x32_bf16 v[48:51], v[148:151], v[188:191], v[48:51]
	v_mfma_f32_16x16x32_bf16 v[44:47], v[156:159], v[188:191], v[44:47]
	v_mfma_f32_16x16x32_bf16 v[32:35], v[148:151], v[196:199], v[32:35]
	v_mfma_f32_16x16x32_bf16 v[28:31], v[156:159], v[196:199], v[28:31]
	v_mfma_f32_16x16x32_bf16 v[16:19], v[148:151], v[208:211], v[16:19]
	v_mfma_f32_16x16x32_bf16 v[12:15], v[156:159], v[208:211], v[12:15]
	v_mfma_f32_16x16x32_bf16 v[56:59], v[160:163], v[176:179], 0
	v_mfma_f32_16x16x32_bf16 v[52:55], v[168:171], v[176:179], 0
	v_mfma_f32_16x16x32_bf16 v[40:43], v[160:163], v[184:187], 0
	v_mfma_f32_16x16x32_bf16 v[36:39], v[168:171], v[184:187], 0
	v_mfma_f32_16x16x32_bf16 v[24:27], v[160:163], v[192:195], 0
	v_mfma_f32_16x16x32_bf16 v[20:23], v[168:171], v[192:195], 0
	v_mfma_f32_16x16x32_bf16 v[8:11], v[160:163], v[204:207], 0
	v_mfma_f32_16x16x32_bf16 v[4:7], v[168:171], v[204:207], 0
	v_mfma_f32_16x16x32_bf16 v[56:59], v[164:167], v[180:183], v[56:59]
	v_mfma_f32_16x16x32_bf16 v[52:55], v[172:175], v[180:183], v[52:55]
	v_mfma_f32_16x16x32_bf16 v[40:43], v[164:167], v[188:191], v[40:43]
	v_mfma_f32_16x16x32_bf16 v[36:39], v[172:175], v[188:191], v[36:39]
	v_mfma_f32_16x16x32_bf16 v[24:27], v[164:167], v[196:199], v[24:27]
	v_mfma_f32_16x16x32_bf16 v[20:23], v[172:175], v[196:199], v[20:23]
	v_mfma_f32_16x16x32_bf16 v[8:11], v[164:167], v[208:211], v[8:11]
	v_mfma_f32_16x16x32_bf16 v[4:7], v[172:175], v[208:211], v[4:7]
	s_setprio 0
	s_barrier
	s_add_i32 s74, 0, 0x18000
	v_add_u32_e32 v2, s74, v203
	s_add_i32 s75, 0, 0x1c000
	ds_read_b128 v[144:147], v2
	ds_read_b128 v[148:151], v2 offset:1024
	ds_read_b128 v[152:155], v2 offset:2048
	ds_read_b128 v[156:159], v2 offset:3072
	v_add_u32_e32 v2, s75, v203
	ds_read_b128 v[160:163], v2
	ds_read_b128 v[164:167], v2 offset:1024
	ds_read_b128 v[168:171], v2 offset:2048
	ds_read_b128 v[172:175], v2 offset:3072
	s_add_u32 s4, s4, 0x40000
	s_addc_u32 s5, s5, 0
	s_mov_b32 m0, s47
	ds_read_b128 v[176:179], v224 offset:32768
	ds_read_b128 v[180:183], v224 offset:33792
	ds_read_b128 v[184:187], v224 offset:34816
	ds_read_b128 v[188:191], v224 offset:35840
	ds_read_b128 v[192:195], v224 offset:36864
	ds_read_b128 v[196:199], v224 offset:37888
	ds_read_b128 v[204:207], v224 offset:38912
	ds_read_b128 v[208:211], v224 offset:39936
	global_load_lds_dwordx4 v134, s[4:5]
	s_mov_b32 m0, s56
	s_nop 0
	global_load_lds_dwordx4 v132, s[4:5]
	s_waitcnt vmcnt(8)
	s_waitcnt lgkmcnt(0)
	s_barrier
	s_setprio 1
	v_mfma_f32_16x16x32_bf16 v[128:131], v[144:147], v[176:179], v[128:131]
	v_mfma_f32_16x16x32_bf16 v[124:127], v[152:155], v[176:179], v[124:127]
	v_mfma_f32_16x16x32_bf16 v[112:115], v[144:147], v[184:187], v[112:115]
	v_mfma_f32_16x16x32_bf16 v[108:111], v[152:155], v[184:187], v[108:111]
	v_mfma_f32_16x16x32_bf16 v[96:99], v[144:147], v[192:195], v[96:99]
	v_mfma_f32_16x16x32_bf16 v[92:95], v[152:155], v[192:195], v[92:95]
	v_mfma_f32_16x16x32_bf16 v[80:83], v[144:147], v[204:207], v[80:83]
	v_mfma_f32_16x16x32_bf16 v[76:79], v[152:155], v[204:207], v[76:79]
	v_mfma_f32_16x16x32_bf16 v[128:131], v[148:151], v[180:183], v[128:131]
	v_mfma_f32_16x16x32_bf16 v[124:127], v[156:159], v[180:183], v[124:127]
	v_mfma_f32_16x16x32_bf16 v[112:115], v[148:151], v[188:191], v[112:115]
	v_mfma_f32_16x16x32_bf16 v[108:111], v[156:159], v[188:191], v[108:111]
	v_mfma_f32_16x16x32_bf16 v[96:99], v[148:151], v[196:199], v[96:99]
	v_mfma_f32_16x16x32_bf16 v[92:95], v[156:159], v[196:199], v[92:95]
	v_mfma_f32_16x16x32_bf16 v[80:83], v[148:151], v[208:211], v[80:83]
	v_mfma_f32_16x16x32_bf16 v[76:79], v[156:159], v[208:211], v[76:79]
	v_mfma_f32_16x16x32_bf16 v[120:123], v[160:163], v[176:179], v[120:123]
	v_mfma_f32_16x16x32_bf16 v[116:119], v[168:171], v[176:179], v[116:119]
	v_mfma_f32_16x16x32_bf16 v[104:107], v[160:163], v[184:187], v[104:107]
	v_mfma_f32_16x16x32_bf16 v[100:103], v[168:171], v[184:187], v[100:103]
	v_mfma_f32_16x16x32_bf16 v[88:91], v[160:163], v[192:195], v[88:91]
	v_mfma_f32_16x16x32_bf16 v[84:87], v[168:171], v[192:195], v[84:87]
	v_mfma_f32_16x16x32_bf16 v[72:75], v[160:163], v[204:207], v[72:75]
	v_mfma_f32_16x16x32_bf16 v[68:71], v[168:171], v[204:207], v[68:71]
	v_mfma_f32_16x16x32_bf16 v[120:123], v[164:167], v[180:183], v[120:123]
	v_mfma_f32_16x16x32_bf16 v[116:119], v[172:175], v[180:183], v[116:119]
	v_mfma_f32_16x16x32_bf16 v[104:107], v[164:167], v[188:191], v[104:107]
	v_mfma_f32_16x16x32_bf16 v[100:103], v[172:175], v[188:191], v[100:103]
	v_mfma_f32_16x16x32_bf16 v[88:91], v[164:167], v[196:199], v[88:91]
	v_mfma_f32_16x16x32_bf16 v[84:87], v[172:175], v[196:199], v[84:87]
	v_mfma_f32_16x16x32_bf16 v[72:75], v[164:167], v[208:211], v[72:75]
	v_mfma_f32_16x16x32_bf16 v[68:71], v[172:175], v[208:211], v[68:71]
	s_setprio 0
	s_barrier
	s_add_i32 s4, s74, s16
	s_add_u32 s98, s52, 0x80
	s_addc_u32 s99, s53, 0
	s_mov_b32 m0, s4
	ds_read_b128 v[176:179], v224 offset:49152
	ds_read_b128 v[180:183], v224 offset:50176
	ds_read_b128 v[184:187], v224 offset:51200
	ds_read_b128 v[188:191], v224 offset:52224
	ds_read_b128 v[192:195], v224 offset:53248
	ds_read_b128 v[196:199], v224 offset:54272
	ds_read_b128 v[204:207], v224 offset:55296
	ds_read_b128 v[208:211], v224 offset:56320
	global_load_lds_dwordx4 v134, s[98:99]
	s_add_i32 m0, s4, 0x2000
	s_add_u32 s4, s52, 0x40080
	s_addc_u32 s5, s53, 0
	s_add_i32 s52, s75, s16
	global_load_lds_dwordx4 v132, s[98:99]
	s_mov_b32 m0, s52
	s_nop 0
	global_load_lds_dwordx4 v134, s[4:5]
	s_add_i32 m0, s52, 0x2000
	s_nop 0
	global_load_lds_dwordx4 v132, s[4:5]
	s_mov_b32 m0, s59
	s_nop 0
	global_load_lds_dwordx4 v134, s[12:13]
	s_mov_b32 m0, s60
	s_nop 0
	global_load_lds_dwordx4 v132, s[12:13]
	s_waitcnt vmcnt(8)
	s_waitcnt lgkmcnt(0)
	s_barrier
	s_setprio 1
	v_mfma_f32_16x16x32_bf16 v[64:67], v[144:147], v[176:179], v[64:67]
	v_mfma_f32_16x16x32_bf16 v[60:63], v[152:155], v[176:179], v[60:63]
	v_mfma_f32_16x16x32_bf16 v[48:51], v[144:147], v[184:187], v[48:51]
	v_mfma_f32_16x16x32_bf16 v[44:47], v[152:155], v[184:187], v[44:47]
	v_mfma_f32_16x16x32_bf16 v[32:35], v[144:147], v[192:195], v[32:35]
	v_mfma_f32_16x16x32_bf16 v[28:31], v[152:155], v[192:195], v[28:31]
	v_mfma_f32_16x16x32_bf16 v[16:19], v[144:147], v[204:207], v[16:19]
	v_mfma_f32_16x16x32_bf16 v[12:15], v[152:155], v[204:207], v[12:15]
	v_mfma_f32_16x16x32_bf16 v[64:67], v[148:151], v[180:183], v[64:67]
	v_mfma_f32_16x16x32_bf16 v[60:63], v[156:159], v[180:183], v[60:63]
	v_mfma_f32_16x16x32_bf16 v[48:51], v[148:151], v[188:191], v[48:51]
	v_mfma_f32_16x16x32_bf16 v[44:47], v[156:159], v[188:191], v[44:47]
	v_mfma_f32_16x16x32_bf16 v[32:35], v[148:151], v[196:199], v[32:35]
	v_mfma_f32_16x16x32_bf16 v[28:31], v[156:159], v[196:199], v[28:31]
	v_mfma_f32_16x16x32_bf16 v[16:19], v[148:151], v[208:211], v[16:19]
	v_mfma_f32_16x16x32_bf16 v[12:15], v[156:159], v[208:211], v[12:15]
	v_mfma_f32_16x16x32_bf16 v[56:59], v[160:163], v[176:179], v[56:59]
	v_mfma_f32_16x16x32_bf16 v[52:55], v[168:171], v[176:179], v[52:55]
	v_mfma_f32_16x16x32_bf16 v[40:43], v[160:163], v[184:187], v[40:43]
	v_mfma_f32_16x16x32_bf16 v[36:39], v[168:171], v[184:187], v[36:39]
	v_mfma_f32_16x16x32_bf16 v[24:27], v[160:163], v[192:195], v[24:27]
	v_mfma_f32_16x16x32_bf16 v[20:23], v[168:171], v[192:195], v[20:23]
	v_mfma_f32_16x16x32_bf16 v[8:11], v[160:163], v[204:207], v[8:11]
	v_mfma_f32_16x16x32_bf16 v[4:7], v[168:171], v[204:207], v[4:7]
	v_mfma_f32_16x16x32_bf16 v[56:59], v[164:167], v[180:183], v[56:59]
	v_mfma_f32_16x16x32_bf16 v[52:55], v[172:175], v[180:183], v[52:55]
	v_mfma_f32_16x16x32_bf16 v[40:43], v[164:167], v[188:191], v[40:43]
	v_mfma_f32_16x16x32_bf16 v[36:39], v[172:175], v[188:191], v[36:39]
	v_mfma_f32_16x16x32_bf16 v[24:27], v[164:167], v[196:199], v[24:27]
	v_mfma_f32_16x16x32_bf16 v[20:23], v[172:175], v[196:199], v[20:23]
	v_mfma_f32_16x16x32_bf16 v[8:11], v[164:167], v[208:211], v[8:11]
	v_mfma_f32_16x16x32_bf16 v[4:7], v[172:175], v[208:211], v[4:7]
	s_setprio 0
	s_barrier
	s_add_i32 s73, s73, 2
	s_add_u32 s50, s50, 0x100
	s_addc_u32 s51, s51, 0
	s_cmp_gt_u32 s73, 13
.LBB0_1044:
	s_add_u32 s4, s48, s50
	s_addc_u32 s5, s49, s51
	s_add_u32 s98, s4, 0x40080
	s_addc_u32 s99, s5, 0
	s_add_u32 s74, s4, 0x100
	s_addc_u32 s75, s5, 0
	s_add_u32 s52, s71, s50
	s_addc_u32 s53, s72, s51
	s_add_u32 s4, s4, 0x180
	s_addc_u32 s5, s5, 0
	s_add_i32 s76, 0, 0x10000
	s_add_i32 s77, 0, 0x14000
	v_add_u32_e32 v2, s76, v203
	ds_read_b128 v[144:147], v2
	ds_read_b128 v[148:151], v2 offset:1024
	ds_read_b128 v[152:155], v2 offset:2048
	ds_read_b128 v[156:159], v2 offset:3072
	v_add_u32_e32 v2, s77, v203
	ds_read_b128 v[160:163], v2
	ds_read_b128 v[164:167], v2 offset:1024
	ds_read_b128 v[168:171], v2 offset:2048
	ds_read_b128 v[172:175], v2 offset:3072
	s_cmpk_eq_i32 s50, 0x700
	s_cselect_b32 s13, s70, s5
	s_cselect_b32 s12, s69, s4
	s_cselect_b32 s53, s37, s53
	s_cselect_b32 s52, s68, s52
	s_cselect_b32 s5, s41, s75
	s_cselect_b32 s4, s65, s74
	s_add_i32 m0, s17, 0xc000
	ds_read_b128 v[176:179], v224
	ds_read_b128 v[180:183], v224 offset:1024
	ds_read_b128 v[184:187], v224 offset:2048
	ds_read_b128 v[188:191], v224 offset:3072
	ds_read_b128 v[192:195], v224 offset:4096
	ds_read_b128 v[196:199], v224 offset:5120
	ds_read_b128 v[204:207], v224 offset:6144
	ds_read_b128 v[208:211], v224 offset:7168
	global_load_lds_dwordx4 v136, s[98:99]
	s_add_i32 m0, s17, 0xe000
	s_nop 0
	global_load_lds_dwordx4 v138, s[98:99]
	s_waitcnt vmcnt(8)
	s_waitcnt lgkmcnt(0)
	s_barrier
	s_setprio 1
	v_mfma_f32_16x16x32_bf16 v[128:131], v[144:147], v[176:179], v[128:131]
	v_mfma_f32_16x16x32_bf16 v[124:127], v[152:155], v[176:179], v[124:127]
	v_mfma_f32_16x16x32_bf16 v[112:115], v[144:147], v[184:187], v[112:115]
	v_mfma_f32_16x16x32_bf16 v[108:111], v[152:155], v[184:187], v[108:111]
	v_mfma_f32_16x16x32_bf16 v[96:99], v[144:147], v[192:195], v[96:99]
	v_mfma_f32_16x16x32_bf16 v[92:95], v[152:155], v[192:195], v[92:95]
	v_mfma_f32_16x16x32_bf16 v[80:83], v[144:147], v[204:207], v[80:83]
	v_mfma_f32_16x16x32_bf16 v[76:79], v[152:155], v[204:207], v[76:79]
	v_mfma_f32_16x16x32_bf16 v[128:131], v[148:151], v[180:183], v[128:131]
	v_mfma_f32_16x16x32_bf16 v[124:127], v[156:159], v[180:183], v[124:127]
	v_mfma_f32_16x16x32_bf16 v[112:115], v[148:151], v[188:191], v[112:115]
	v_mfma_f32_16x16x32_bf16 v[108:111], v[156:159], v[188:191], v[108:111]
	v_mfma_f32_16x16x32_bf16 v[96:99], v[148:151], v[196:199], v[96:99]
	v_mfma_f32_16x16x32_bf16 v[92:95], v[156:159], v[196:199], v[92:95]
	v_mfma_f32_16x16x32_bf16 v[80:83], v[148:151], v[208:211], v[80:83]
	v_mfma_f32_16x16x32_bf16 v[76:79], v[156:159], v[208:211], v[76:79]
	v_mfma_f32_16x16x32_bf16 v[120:123], v[160:163], v[176:179], v[120:123]
	v_mfma_f32_16x16x32_bf16 v[116:119], v[168:171], v[176:179], v[116:119]
	v_mfma_f32_16x16x32_bf16 v[104:107], v[160:163], v[184:187], v[104:107]
	v_mfma_f32_16x16x32_bf16 v[100:103], v[168:171], v[184:187], v[100:103]
	v_mfma_f32_16x16x32_bf16 v[88:91], v[160:163], v[192:195], v[88:91]
	v_mfma_f32_16x16x32_bf16 v[84:87], v[168:171], v[192:195], v[84:87]
	v_mfma_f32_16x16x32_bf16 v[72:75], v[160:163], v[204:207], v[72:75]
	v_mfma_f32_16x16x32_bf16 v[68:71], v[168:171], v[204:207], v[68:71]
	v_mfma_f32_16x16x32_bf16 v[120:123], v[164:167], v[180:183], v[120:123]
	v_mfma_f32_16x16x32_bf16 v[116:119], v[172:175], v[180:183], v[116:119]
	v_mfma_f32_16x16x32_bf16 v[104:107], v[164:167], v[188:191], v[104:107]
	v_mfma_f32_16x16x32_bf16 v[100:103], v[172:175], v[188:191], v[100:103]
	v_mfma_f32_16x16x32_bf16 v[88:91], v[164:167], v[196:199], v[88:91]
	v_mfma_f32_16x16x32_bf16 v[84:87], v[172:175], v[196:199], v[84:87]
	v_mfma_f32_16x16x32_bf16 v[72:75], v[164:167], v[208:211], v[72:75]
	v_mfma_f32_16x16x32_bf16 v[68:71], v[172:175], v[208:211], v[68:71]
	s_setprio 0
	s_barrier
	s_add_i32 s74, s76, s16
	s_mov_b32 m0, s74
	ds_read_b128 v[176:179], v224 offset:16384
	ds_read_b128 v[180:183], v224 offset:17408
	ds_read_b128 v[184:187], v224 offset:18432
	ds_read_b128 v[188:191], v224 offset:19456
	ds_read_b128 v[192:195], v224 offset:20480
	ds_read_b128 v[196:199], v224 offset:21504
	ds_read_b128 v[204:207], v224 offset:22528
	ds_read_b128 v[208:211], v224 offset:23552
	global_load_lds_dwordx4 v134, s[52:53]
	s_add_i32 m0, s74, 0x2000
	s_add_u32 s74, s52, 0x40000
	s_addc_u32 s75, s53, 0
	s_add_i32 s76, s77, s16
	global_load_lds_dwordx4 v132, s[52:53]
	s_mov_b32 m0, s76
	s_nop 0
	global_load_lds_dwordx4 v134, s[74:75]
	s_add_i32 m0, s76, 0x2000
	s_nop 0
	global_load_lds_dwordx4 v132, s[74:75]
	s_mov_b32 m0, s17
	s_nop 0
	global_load_lds_dwordx4 v134, s[4:5]
	s_mov_b32 m0, s46
	s_nop 0
	global_load_lds_dwordx4 v132, s[4:5]
	s_waitcnt vmcnt(8)
	s_waitcnt lgkmcnt(0)
	s_barrier
	s_setprio 1
	v_mfma_f32_16x16x32_bf16 v[64:67], v[144:147], v[176:179], v[64:67]
	v_mfma_f32_16x16x32_bf16 v[60:63], v[152:155], v[176:179], v[60:63]
	v_mfma_f32_16x16x32_bf16 v[48:51], v[144:147], v[184:187], v[48:51]
	v_mfma_f32_16x16x32_bf16 v[44:47], v[152:155], v[184:187], v[44:47]
	v_mfma_f32_16x16x32_bf16 v[32:35], v[144:147], v[192:195], v[32:35]
	v_mfma_f32_16x16x32_bf16 v[28:31], v[152:155], v[192:195], v[28:31]
	v_mfma_f32_16x16x32_bf16 v[16:19], v[144:147], v[204:207], v[16:19]
	v_mfma_f32_16x16x32_bf16 v[12:15], v[152:155], v[204:207], v[12:15]
	v_mfma_f32_16x16x32_bf16 v[64:67], v[148:151], v[180:183], v[64:67]
	v_mfma_f32_16x16x32_bf16 v[60:63], v[156:159], v[180:183], v[60:63]
	v_mfma_f32_16x16x32_bf16 v[48:51], v[148:151], v[188:191], v[48:51]
	v_mfma_f32_16x16x32_bf16 v[44:47], v[156:159], v[188:191], v[44:47]
	v_mfma_f32_16x16x32_bf16 v[32:35], v[148:151], v[196:199], v[32:35]
	v_mfma_f32_16x16x32_bf16 v[28:31], v[156:159], v[196:199], v[28:31]
	v_mfma_f32_16x16x32_bf16 v[16:19], v[148:151], v[208:211], v[16:19]
	v_mfma_f32_16x16x32_bf16 v[12:15], v[156:159], v[208:211], v[12:15]
	v_mfma_f32_16x16x32_bf16 v[56:59], v[160:163], v[176:179], v[56:59]
	v_mfma_f32_16x16x32_bf16 v[52:55], v[168:171], v[176:179], v[52:55]
	v_mfma_f32_16x16x32_bf16 v[40:43], v[160:163], v[184:187], v[40:43]
	v_mfma_f32_16x16x32_bf16 v[36:39], v[168:171], v[184:187], v[36:39]
	v_mfma_f32_16x16x32_bf16 v[24:27], v[160:163], v[192:195], v[24:27]
	v_mfma_f32_16x16x32_bf16 v[20:23], v[168:171], v[192:195], v[20:23]
	v_mfma_f32_16x16x32_bf16 v[8:11], v[160:163], v[204:207], v[8:11]
	v_mfma_f32_16x16x32_bf16 v[4:7], v[168:171], v[204:207], v[4:7]
	v_mfma_f32_16x16x32_bf16 v[56:59], v[164:167], v[180:183], v[56:59]
	v_mfma_f32_16x16x32_bf16 v[52:55], v[172:175], v[180:183], v[52:55]
	v_mfma_f32_16x16x32_bf16 v[40:43], v[164:167], v[188:191], v[40:43]
	v_mfma_f32_16x16x32_bf16 v[36:39], v[172:175], v[188:191], v[36:39]
	v_mfma_f32_16x16x32_bf16 v[24:27], v[164:167], v[196:199], v[24:27]
	v_mfma_f32_16x16x32_bf16 v[20:23], v[172:175], v[196:199], v[20:23]
	v_mfma_f32_16x16x32_bf16 v[8:11], v[164:167], v[208:211], v[8:11]
	v_mfma_f32_16x16x32_bf16 v[4:7], v[172:175], v[208:211], v[4:7]
	s_setprio 0
	s_barrier
	s_add_i32 s74, 0, 0x18000
	v_add_u32_e32 v2, s74, v203
	s_add_i32 s75, 0, 0x1c000
	ds_read_b128 v[144:147], v2
	ds_read_b128 v[148:151], v2 offset:1024
	ds_read_b128 v[152:155], v2 offset:2048
	ds_read_b128 v[156:159], v2 offset:3072
	v_add_u32_e32 v2, s75, v203
	ds_read_b128 v[160:163], v2
	ds_read_b128 v[164:167], v2 offset:1024
	ds_read_b128 v[168:171], v2 offset:2048
	ds_read_b128 v[172:175], v2 offset:3072
	s_add_u32 s4, s4, 0x40000
	s_addc_u32 s5, s5, 0
	s_mov_b32 m0, s47
	ds_read_b128 v[176:179], v224 offset:32768
	ds_read_b128 v[180:183], v224 offset:33792
	ds_read_b128 v[184:187], v224 offset:34816
	ds_read_b128 v[188:191], v224 offset:35840
	ds_read_b128 v[192:195], v224 offset:36864
	ds_read_b128 v[196:199], v224 offset:37888
	ds_read_b128 v[204:207], v224 offset:38912
	ds_read_b128 v[208:211], v224 offset:39936
	global_load_lds_dwordx4 v134, s[4:5]
	s_mov_b32 m0, s56
	s_nop 0
	global_load_lds_dwordx4 v132, s[4:5]
	s_waitcnt vmcnt(8)
	s_waitcnt lgkmcnt(0)
	s_barrier
	s_setprio 1
	v_mfma_f32_16x16x32_bf16 v[128:131], v[144:147], v[176:179], v[128:131]
	v_mfma_f32_16x16x32_bf16 v[124:127], v[152:155], v[176:179], v[124:127]
	v_mfma_f32_16x16x32_bf16 v[112:115], v[144:147], v[184:187], v[112:115]
	v_mfma_f32_16x16x32_bf16 v[108:111], v[152:155], v[184:187], v[108:111]
	v_mfma_f32_16x16x32_bf16 v[96:99], v[144:147], v[192:195], v[96:99]
	v_mfma_f32_16x16x32_bf16 v[92:95], v[152:155], v[192:195], v[92:95]
	v_mfma_f32_16x16x32_bf16 v[80:83], v[144:147], v[204:207], v[80:83]
	v_mfma_f32_16x16x32_bf16 v[76:79], v[152:155], v[204:207], v[76:79]
	v_mfma_f32_16x16x32_bf16 v[128:131], v[148:151], v[180:183], v[128:131]
	v_mfma_f32_16x16x32_bf16 v[124:127], v[156:159], v[180:183], v[124:127]
	v_mfma_f32_16x16x32_bf16 v[112:115], v[148:151], v[188:191], v[112:115]
	v_mfma_f32_16x16x32_bf16 v[108:111], v[156:159], v[188:191], v[108:111]
	v_mfma_f32_16x16x32_bf16 v[96:99], v[148:151], v[196:199], v[96:99]
	v_mfma_f32_16x16x32_bf16 v[92:95], v[156:159], v[196:199], v[92:95]
	v_mfma_f32_16x16x32_bf16 v[80:83], v[148:151], v[208:211], v[80:83]
	v_mfma_f32_16x16x32_bf16 v[76:79], v[156:159], v[208:211], v[76:79]
	v_mfma_f32_16x16x32_bf16 v[120:123], v[160:163], v[176:179], v[120:123]
	v_mfma_f32_16x16x32_bf16 v[116:119], v[168:171], v[176:179], v[116:119]
	v_mfma_f32_16x16x32_bf16 v[104:107], v[160:163], v[184:187], v[104:107]
	v_mfma_f32_16x16x32_bf16 v[100:103], v[168:171], v[184:187], v[100:103]
	v_mfma_f32_16x16x32_bf16 v[88:91], v[160:163], v[192:195], v[88:91]
	v_mfma_f32_16x16x32_bf16 v[84:87], v[168:171], v[192:195], v[84:87]
	v_mfma_f32_16x16x32_bf16 v[72:75], v[160:163], v[204:207], v[72:75]
	v_mfma_f32_16x16x32_bf16 v[68:71], v[168:171], v[204:207], v[68:71]
	v_mfma_f32_16x16x32_bf16 v[120:123], v[164:167], v[180:183], v[120:123]
	v_mfma_f32_16x16x32_bf16 v[116:119], v[172:175], v[180:183], v[116:119]
	v_mfma_f32_16x16x32_bf16 v[104:107], v[164:167], v[188:191], v[104:107]
	v_mfma_f32_16x16x32_bf16 v[100:103], v[172:175], v[188:191], v[100:103]
	v_mfma_f32_16x16x32_bf16 v[88:91], v[164:167], v[196:199], v[88:91]
	v_mfma_f32_16x16x32_bf16 v[84:87], v[172:175], v[196:199], v[84:87]
	v_mfma_f32_16x16x32_bf16 v[72:75], v[164:167], v[208:211], v[72:75]
	v_mfma_f32_16x16x32_bf16 v[68:71], v[172:175], v[208:211], v[68:71]
	s_setprio 0
	s_barrier
	s_add_i32 s4, s74, s16
	s_add_u32 s98, s52, 0x80
	s_addc_u32 s99, s53, 0
	s_mov_b32 m0, s4
	ds_read_b128 v[176:179], v224 offset:49152
	ds_read_b128 v[180:183], v224 offset:50176
	ds_read_b128 v[184:187], v224 offset:51200
	ds_read_b128 v[188:191], v224 offset:52224
	ds_read_b128 v[192:195], v224 offset:53248
	ds_read_b128 v[196:199], v224 offset:54272
	ds_read_b128 v[204:207], v224 offset:55296
	ds_read_b128 v[208:211], v224 offset:56320
	global_load_lds_dwordx4 v134, s[98:99]
	s_add_i32 m0, s4, 0x2000
	s_add_u32 s4, s52, 0x40080
	s_addc_u32 s5, s53, 0
	s_add_i32 s52, s75, s16
	global_load_lds_dwordx4 v132, s[98:99]
	s_mov_b32 m0, s52
	s_nop 0
	global_load_lds_dwordx4 v134, s[4:5]
	s_add_i32 m0, s52, 0x2000
	s_nop 0
	global_load_lds_dwordx4 v132, s[4:5]
	s_mov_b32 m0, s59
	s_nop 0
	global_load_lds_dwordx4 v134, s[12:13]
	s_mov_b32 m0, s60
	s_nop 0
	global_load_lds_dwordx4 v132, s[12:13]
	s_waitcnt vmcnt(8)
	s_waitcnt lgkmcnt(0)
	s_barrier
	s_setprio 1
	v_mfma_f32_16x16x32_bf16 v[64:67], v[144:147], v[176:179], v[64:67]
	v_mfma_f32_16x16x32_bf16 v[60:63], v[152:155], v[176:179], v[60:63]
	v_mfma_f32_16x16x32_bf16 v[48:51], v[144:147], v[184:187], v[48:51]
	v_mfma_f32_16x16x32_bf16 v[44:47], v[152:155], v[184:187], v[44:47]
	v_mfma_f32_16x16x32_bf16 v[32:35], v[144:147], v[192:195], v[32:35]
	v_mfma_f32_16x16x32_bf16 v[28:31], v[152:155], v[192:195], v[28:31]
	v_mfma_f32_16x16x32_bf16 v[16:19], v[144:147], v[204:207], v[16:19]
	v_mfma_f32_16x16x32_bf16 v[12:15], v[152:155], v[204:207], v[12:15]
	v_mfma_f32_16x16x32_bf16 v[64:67], v[148:151], v[180:183], v[64:67]
	v_mfma_f32_16x16x32_bf16 v[60:63], v[156:159], v[180:183], v[60:63]
	v_mfma_f32_16x16x32_bf16 v[48:51], v[148:151], v[188:191], v[48:51]
	v_mfma_f32_16x16x32_bf16 v[44:47], v[156:159], v[188:191], v[44:47]
	v_mfma_f32_16x16x32_bf16 v[32:35], v[148:151], v[196:199], v[32:35]
	v_mfma_f32_16x16x32_bf16 v[28:31], v[156:159], v[196:199], v[28:31]
	v_mfma_f32_16x16x32_bf16 v[16:19], v[148:151], v[208:211], v[16:19]
	v_mfma_f32_16x16x32_bf16 v[12:15], v[156:159], v[208:211], v[12:15]
	v_mfma_f32_16x16x32_bf16 v[56:59], v[160:163], v[176:179], v[56:59]
	v_mfma_f32_16x16x32_bf16 v[52:55], v[168:171], v[176:179], v[52:55]
	v_mfma_f32_16x16x32_bf16 v[40:43], v[160:163], v[184:187], v[40:43]
	v_mfma_f32_16x16x32_bf16 v[36:39], v[168:171], v[184:187], v[36:39]
	v_mfma_f32_16x16x32_bf16 v[24:27], v[160:163], v[192:195], v[24:27]
	v_mfma_f32_16x16x32_bf16 v[20:23], v[168:171], v[192:195], v[20:23]
	v_mfma_f32_16x16x32_bf16 v[8:11], v[160:163], v[204:207], v[8:11]
	v_mfma_f32_16x16x32_bf16 v[4:7], v[168:171], v[204:207], v[4:7]
	v_mfma_f32_16x16x32_bf16 v[56:59], v[164:167], v[180:183], v[56:59]
	v_mfma_f32_16x16x32_bf16 v[52:55], v[172:175], v[180:183], v[52:55]
	v_mfma_f32_16x16x32_bf16 v[40:43], v[164:167], v[188:191], v[40:43]
	v_mfma_f32_16x16x32_bf16 v[36:39], v[172:175], v[188:191], v[36:39]
	v_mfma_f32_16x16x32_bf16 v[24:27], v[164:167], v[196:199], v[24:27]
	v_mfma_f32_16x16x32_bf16 v[20:23], v[172:175], v[196:199], v[20:23]
	v_mfma_f32_16x16x32_bf16 v[8:11], v[164:167], v[208:211], v[8:11]
	v_mfma_f32_16x16x32_bf16 v[4:7], v[172:175], v[208:211], v[4:7]
	s_setprio 0
	s_barrier
	s_add_i32 s73, s73, 2
	s_add_u32 s50, s50, 0x100
	s_addc_u32 s51, s51, 0
	s_cmp_gt_u32 s73, 13
	s_cbranch_scc0 .LBB0_1044
	s_and_b64 vcc, exec, s[22:23]
	s_cbranch_vccz .LBB0_1047
	s_barrier

.LBB0_1117:
	s_ashr_i32 s37, s36, 31
	s_lshl_b64 s[4:5], s[36:37], 19
	s_add_u32 s40, s6, s4
	s_addc_u32 s41, s7, s5
	s_and_b64 s[4:5], s[38:39], exec
	s_cselect_b32 s37, s41, s45
	s_cselect_b32 s64, s40, s44
	s_ashr_i32 s23, s22, 31
	s_lshl_b64 s[4:5], s[22:23], 19
	s_add_u32 s42, s8, s4
	s_addc_u32 s43, s9, s5
	s_and_b64 s[4:5], s[38:39], exec
	s_cselect_b32 s23, s43, s49
	s_cselect_b32 s65, s42, s48
	s_add_u32 s68, s64, 0x80
	s_addc_u32 s69, s37, 0
	s_add_u32 s70, s48, 0x100
	s_addc_u32 s71, s49, 0
	s_add_u32 s4, s44, 0x40080
	s_addc_u32 s5, s45, 0
	v_lshl_add_u64 v[108:109], s[4:5], 0, v[210:211]
	v_lshl_add_u64 v[110:111], s[4:5], 0, v[212:213]
	s_mov_b32 s72, -2
	s_mov_b64 s[48:49], 0
	s_waitcnt lgkmcnt(0)
	s_waitcnt vmcnt(0)
	s_add_u32 s4, s44, s48
	s_addc_u32 s5, s45, s49
	s_add_u32 s98, s4, 0x40080
	s_addc_u32 s99, s5, 0
	s_add_u32 s73, s4, 0x100
	s_addc_u32 s74, s5, 0
	s_add_u32 s50, s70, s48
	s_addc_u32 s51, s71, s49
	s_add_u32 s4, s4, 0x180
	s_addc_u32 s5, s5, 0
	s_add_i32 s75, 0, 0x10000
	s_add_i32 s76, 0, 0x14000
	v_add_u32_e32 v148, s75, v203
	v_add_u32_e32 v164, s76, v203
	ds_read_b128 v[116:119], v148
	ds_read_b128 v[128:131], v148 offset:1024
	ds_read_b128 v[136:139], v148 offset:2048
	ds_read_b128 v[148:151], v148 offset:3072
	ds_read_b128 v[152:155], v164
	ds_read_b128 v[156:159], v164 offset:1024
	ds_read_b128 v[160:163], v164 offset:2048
	ds_read_b128 v[164:167], v164 offset:3072
	s_cmpk_eq_i32 s48, 0x700
	s_cselect_b32 s13, s69, s5
	s_cselect_b32 s12, s68, s4
	s_cselect_b32 s51, s23, s51
	s_cselect_b32 s50, s65, s50
	s_cselect_b32 s5, s37, s74
	s_cselect_b32 s4, s64, s73
	s_add_i32 m0, s17, 0xc000
	ds_read_b128 v[168:171], v236
	ds_read_b128 v[172:175], v236 offset:1024
	ds_read_b128 v[176:179], v236 offset:2048
	ds_read_b128 v[180:183], v236 offset:3072
	ds_read_b128 v[184:187], v236 offset:4096
	ds_read_b128 v[188:191], v236 offset:5120
	ds_read_b128 v[192:195], v236 offset:6144
	ds_read_b128 v[196:199], v236 offset:7168
	global_load_lds_dwordx4 v210, s[98:99]
	s_add_i32 m0, s17, 0xe000
	s_nop 0
	global_load_lds_dwordx4 v212, s[98:99]
	s_waitcnt vmcnt(8)
	s_waitcnt lgkmcnt(0)
	s_barrier
	s_setprio 1
	v_mfma_f32_16x16x32_bf16 v[144:147], v[116:119], v[168:171], 0
	v_mfma_f32_16x16x32_bf16 v[140:143], v[136:139], v[168:171], 0
	v_mfma_f32_16x16x32_bf16 v[120:123], v[116:119], v[176:179], 0
	v_mfma_f32_16x16x32_bf16 v[112:115], v[136:139], v[176:179], 0
	v_mfma_f32_16x16x32_bf16 v[96:99], v[116:119], v[184:187], 0
	v_mfma_f32_16x16x32_bf16 v[92:95], v[136:139], v[184:187], 0
	v_mfma_f32_16x16x32_bf16 v[80:83], v[116:119], v[192:195], 0
	v_mfma_f32_16x16x32_bf16 v[76:79], v[136:139], v[192:195], 0
	v_mfma_f32_16x16x32_bf16 v[144:147], v[128:131], v[172:175], v[144:147]
	v_mfma_f32_16x16x32_bf16 v[140:143], v[148:151], v[172:175], v[140:143]
	v_mfma_f32_16x16x32_bf16 v[120:123], v[128:131], v[180:183], v[120:123]
	v_mfma_f32_16x16x32_bf16 v[112:115], v[148:151], v[180:183], v[112:115]
	v_mfma_f32_16x16x32_bf16 v[96:99], v[128:131], v[188:191], v[96:99]
	v_mfma_f32_16x16x32_bf16 v[92:95], v[148:151], v[188:191], v[92:95]
	v_mfma_f32_16x16x32_bf16 v[80:83], v[128:131], v[196:199], v[80:83]
	v_mfma_f32_16x16x32_bf16 v[76:79], v[148:151], v[196:199], v[76:79]
	v_mfma_f32_16x16x32_bf16 v[132:135], v[152:155], v[168:171], 0
	v_mfma_f32_16x16x32_bf16 v[124:127], v[160:163], v[168:171], 0
	v_mfma_f32_16x16x32_bf16 v[104:107], v[152:155], v[176:179], 0
	v_mfma_f32_16x16x32_bf16 v[100:103], v[160:163], v[176:179], 0
	v_mfma_f32_16x16x32_bf16 v[88:91], v[152:155], v[184:187], 0
	v_mfma_f32_16x16x32_bf16 v[84:87], v[160:163], v[184:187], 0
	v_mfma_f32_16x16x32_bf16 v[72:75], v[152:155], v[192:195], 0
	v_mfma_f32_16x16x32_bf16 v[68:71], v[160:163], v[192:195], 0
	v_mfma_f32_16x16x32_bf16 v[132:135], v[156:159], v[172:175], v[132:135]
	v_mfma_f32_16x16x32_bf16 v[124:127], v[164:167], v[172:175], v[124:127]
	v_mfma_f32_16x16x32_bf16 v[104:107], v[156:159], v[180:183], v[104:107]
	v_mfma_f32_16x16x32_bf16 v[100:103], v[164:167], v[180:183], v[100:103]
	v_mfma_f32_16x16x32_bf16 v[88:91], v[156:159], v[188:191], v[88:91]
	v_mfma_f32_16x16x32_bf16 v[84:87], v[164:167], v[188:191], v[84:87]
	v_mfma_f32_16x16x32_bf16 v[72:75], v[156:159], v[196:199], v[72:75]
	v_mfma_f32_16x16x32_bf16 v[68:71], v[164:167], v[196:199], v[68:71]
	s_setprio 0
	s_barrier
	s_add_i32 s73, s75, s16
	s_mov_b32 m0, s73
	ds_read_b128 v[168:171], v236 offset:16384
	ds_read_b128 v[172:175], v236 offset:17408
	ds_read_b128 v[176:179], v236 offset:18432
	ds_read_b128 v[180:183], v236 offset:19456
	ds_read_b128 v[184:187], v236 offset:20480
	ds_read_b128 v[188:191], v236 offset:21504
	ds_read_b128 v[192:195], v236 offset:22528
	ds_read_b128 v[196:199], v236 offset:23552
	global_load_lds_dwordx4 v2, s[50:51]
	s_add_i32 m0, s73, 0x2000
	s_add_u32 s74, s50, 0x40000
	s_addc_u32 s75, s51, 0
	s_add_i32 s73, s76, s16
	global_load_lds_dwordx4 v204, s[50:51]
	s_mov_b32 m0, s73
	s_nop 0
	global_load_lds_dwordx4 v2, s[74:75]
	s_add_i32 m0, s73, 0x2000
	s_nop 0
	global_load_lds_dwordx4 v204, s[74:75]
	s_mov_b32 m0, s17
	s_nop 0
	global_load_lds_dwordx4 v208, s[4:5]
	s_mov_b32 m0, s46
	s_nop 0
	global_load_lds_dwordx4 v206, s[4:5]
	s_waitcnt vmcnt(8)
	s_waitcnt lgkmcnt(0)
	s_barrier
	s_setprio 1
	v_mfma_f32_16x16x32_bf16 v[64:67], v[116:119], v[168:171], 0
	v_mfma_f32_16x16x32_bf16 v[60:63], v[136:139], v[168:171], 0
	v_mfma_f32_16x16x32_bf16 v[48:51], v[116:119], v[176:179], 0
	v_mfma_f32_16x16x32_bf16 v[44:47], v[136:139], v[176:179], 0
	v_mfma_f32_16x16x32_bf16 v[32:35], v[116:119], v[184:187], 0
	v_mfma_f32_16x16x32_bf16 v[28:31], v[136:139], v[184:187], 0
	v_mfma_f32_16x16x32_bf16 v[16:19], v[116:119], v[192:195], 0
	v_mfma_f32_16x16x32_bf16 v[12:15], v[136:139], v[192:195], 0
	v_mfma_f32_16x16x32_bf16 v[64:67], v[128:131], v[172:175], v[64:67]
	v_mfma_f32_16x16x32_bf16 v[60:63], v[148:151], v[172:175], v[60:63]
	v_mfma_f32_16x16x32_bf16 v[48:51], v[128:131], v[180:183], v[48:51]
	v_mfma_f32_16x16x32_bf16 v[44:47], v[148:151], v[180:183], v[44:47]
	v_mfma_f32_16x16x32_bf16 v[32:35], v[128:131], v[188:191], v[32:35]
	v_mfma_f32_16x16x32_bf16 v[28:31], v[148:151], v[188:191], v[28:31]
	v_mfma_f32_16x16x32_bf16 v[16:19], v[128:131], v[196:199], v[16:19]
	v_mfma_f32_16x16x32_bf16 v[12:15], v[148:151], v[196:199], v[12:15]
	v_mfma_f32_16x16x32_bf16 v[56:59], v[152:155], v[168:171], 0
	v_mfma_f32_16x16x32_bf16 v[52:55], v[160:163], v[168:171], 0
	v_mfma_f32_16x16x32_bf16 v[40:43], v[152:155], v[176:179], 0
	v_mfma_f32_16x16x32_bf16 v[36:39], v[160:163], v[176:179], 0
	v_mfma_f32_16x16x32_bf16 v[24:27], v[152:155], v[184:187], 0
	v_mfma_f32_16x16x32_bf16 v[20:23], v[160:163], v[184:187], 0
	v_mfma_f32_16x16x32_bf16 v[8:11], v[152:155], v[192:195], 0
	v_mfma_f32_16x16x32_bf16 v[4:7], v[160:163], v[192:195], 0
	v_mfma_f32_16x16x32_bf16 v[56:59], v[156:159], v[172:175], v[56:59]
	v_mfma_f32_16x16x32_bf16 v[52:55], v[164:167], v[172:175], v[52:55]
	v_mfma_f32_16x16x32_bf16 v[40:43], v[156:159], v[180:183], v[40:43]
	v_mfma_f32_16x16x32_bf16 v[36:39], v[164:167], v[180:183], v[36:39]
	v_mfma_f32_16x16x32_bf16 v[24:27], v[156:159], v[188:191], v[24:27]
	v_mfma_f32_16x16x32_bf16 v[20:23], v[164:167], v[188:191], v[20:23]
	v_mfma_f32_16x16x32_bf16 v[8:11], v[156:159], v[196:199], v[8:11]
	v_mfma_f32_16x16x32_bf16 v[4:7], v[164:167], v[196:199], v[4:7]
	s_setprio 0
	s_barrier
	s_add_i32 s73, 0, 0x18000
	s_add_i32 s74, 0, 0x1c000
	v_add_u32_e32 v148, s73, v203
	v_add_u32_e32 v164, s74, v203
	ds_read_b128 v[116:119], v148
	ds_read_b128 v[128:131], v148 offset:1024
	ds_read_b128 v[136:139], v148 offset:2048
	ds_read_b128 v[148:151], v148 offset:3072
	ds_read_b128 v[152:155], v164
	ds_read_b128 v[156:159], v164 offset:1024
	ds_read_b128 v[160:163], v164 offset:2048
	ds_read_b128 v[164:167], v164 offset:3072
	s_add_u32 s4, s4, 0x40000
	s_addc_u32 s5, s5, 0
	s_mov_b32 m0, s47
	ds_read_b128 v[168:171], v236 offset:32768
	ds_read_b128 v[172:175], v236 offset:33792
	ds_read_b128 v[176:179], v236 offset:34816
	ds_read_b128 v[180:183], v236 offset:35840
	ds_read_b128 v[184:187], v236 offset:36864
	ds_read_b128 v[188:191], v236 offset:37888
	ds_read_b128 v[192:195], v236 offset:38912
	ds_read_b128 v[196:199], v236 offset:39936
	global_load_lds_dwordx4 v208, s[4:5]
	s_mov_b32 m0, s52
	s_nop 0
	global_load_lds_dwordx4 v206, s[4:5]
	s_waitcnt vmcnt(8)
	s_waitcnt lgkmcnt(0)
	s_barrier
	s_setprio 1
	v_mfma_f32_16x16x32_bf16 v[144:147], v[116:119], v[168:171], v[144:147]
	v_mfma_f32_16x16x32_bf16 v[140:143], v[136:139], v[168:171], v[140:143]
	v_mfma_f32_16x16x32_bf16 v[120:123], v[116:119], v[176:179], v[120:123]
	v_mfma_f32_16x16x32_bf16 v[112:115], v[136:139], v[176:179], v[112:115]
	v_mfma_f32_16x16x32_bf16 v[96:99], v[116:119], v[184:187], v[96:99]
	v_mfma_f32_16x16x32_bf16 v[92:95], v[136:139], v[184:187], v[92:95]
	v_mfma_f32_16x16x32_bf16 v[80:83], v[116:119], v[192:195], v[80:83]
	v_mfma_f32_16x16x32_bf16 v[76:79], v[136:139], v[192:195], v[76:79]
	v_mfma_f32_16x16x32_bf16 v[144:147], v[128:131], v[172:175], v[144:147]
	v_mfma_f32_16x16x32_bf16 v[140:143], v[148:151], v[172:175], v[140:143]
	v_mfma_f32_16x16x32_bf16 v[120:123], v[128:131], v[180:183], v[120:123]
	v_mfma_f32_16x16x32_bf16 v[112:115], v[148:151], v[180:183], v[112:115]
	v_mfma_f32_16x16x32_bf16 v[96:99], v[128:131], v[188:191], v[96:99]
	v_mfma_f32_16x16x32_bf16 v[92:95], v[148:151], v[188:191], v[92:95]
	v_mfma_f32_16x16x32_bf16 v[80:83], v[128:131], v[196:199], v[80:83]
	v_mfma_f32_16x16x32_bf16 v[76:79], v[148:151], v[196:199], v[76:79]
	v_mfma_f32_16x16x32_bf16 v[132:135], v[152:155], v[168:171], v[132:135]
	v_mfma_f32_16x16x32_bf16 v[124:127], v[160:163], v[168:171], v[124:127]
	v_mfma_f32_16x16x32_bf16 v[104:107], v[152:155], v[176:179], v[104:107]
	v_mfma_f32_16x16x32_bf16 v[100:103], v[160:163], v[176:179], v[100:103]
	v_mfma_f32_16x16x32_bf16 v[88:91], v[152:155], v[184:187], v[88:91]
	v_mfma_f32_16x16x32_bf16 v[84:87], v[160:163], v[184:187], v[84:87]
	v_mfma_f32_16x16x32_bf16 v[72:75], v[152:155], v[192:195], v[72:75]
	v_mfma_f32_16x16x32_bf16 v[68:71], v[160:163], v[192:195], v[68:71]
	v_mfma_f32_16x16x32_bf16 v[132:135], v[156:159], v[172:175], v[132:135]
	v_mfma_f32_16x16x32_bf16 v[124:127], v[164:167], v[172:175], v[124:127]
	v_mfma_f32_16x16x32_bf16 v[104:107], v[156:159], v[180:183], v[104:107]
	v_mfma_f32_16x16x32_bf16 v[100:103], v[164:167], v[180:183], v[100:103]
	v_mfma_f32_16x16x32_bf16 v[88:91], v[156:159], v[188:191], v[88:91]
	v_mfma_f32_16x16x32_bf16 v[84:87], v[164:167], v[188:191], v[84:87]
	v_mfma_f32_16x16x32_bf16 v[72:75], v[156:159], v[196:199], v[72:75]
	v_mfma_f32_16x16x32_bf16 v[68:71], v[164:167], v[196:199], v[68:71]
	s_setprio 0
	s_barrier
	s_add_i32 s4, s73, s16
	s_add_u32 s98, s50, 0x80
	s_addc_u32 s99, s51, 0
	s_mov_b32 m0, s4
	ds_read_b128 v[168:171], v236 offset:49152
	ds_read_b128 v[172:175], v236 offset:50176
	ds_read_b128 v[176:179], v236 offset:51200
	ds_read_b128 v[180:183], v236 offset:52224
	ds_read_b128 v[184:187], v236 offset:53248
	ds_read_b128 v[188:191], v236 offset:54272
	ds_read_b128 v[192:195], v236 offset:55296
	ds_read_b128 v[196:199], v236 offset:56320
	global_load_lds_dwordx4 v2, s[98:99]
	s_add_i32 m0, s4, 0x2000
	s_add_u32 s4, s50, 0x40080
	s_addc_u32 s5, s51, 0
	s_add_i32 s50, s74, s16
	global_load_lds_dwordx4 v204, s[98:99]
	s_mov_b32 m0, s50
	s_nop 0
	global_load_lds_dwordx4 v2, s[4:5]
	s_add_i32 m0, s50, 0x2000
	s_nop 0
	global_load_lds_dwordx4 v204, s[4:5]
	s_mov_b32 m0, s60
	s_nop 0
	global_load_lds_dwordx4 v208, s[12:13]
	s_mov_b32 m0, s61
	s_nop 0
	global_load_lds_dwordx4 v206, s[12:13]
	s_waitcnt vmcnt(8)
	s_waitcnt lgkmcnt(0)
	s_barrier
	s_setprio 1
	v_mfma_f32_16x16x32_bf16 v[64:67], v[116:119], v[168:171], v[64:67]
	v_mfma_f32_16x16x32_bf16 v[60:63], v[136:139], v[168:171], v[60:63]
	v_mfma_f32_16x16x32_bf16 v[48:51], v[116:119], v[176:179], v[48:51]
	v_mfma_f32_16x16x32_bf16 v[44:47], v[136:139], v[176:179], v[44:47]
	v_mfma_f32_16x16x32_bf16 v[32:35], v[116:119], v[184:187], v[32:35]
	v_mfma_f32_16x16x32_bf16 v[28:31], v[136:139], v[184:187], v[28:31]
	v_mfma_f32_16x16x32_bf16 v[16:19], v[116:119], v[192:195], v[16:19]
	v_mfma_f32_16x16x32_bf16 v[12:15], v[136:139], v[192:195], v[12:15]
	v_mfma_f32_16x16x32_bf16 v[64:67], v[128:131], v[172:175], v[64:67]
	v_mfma_f32_16x16x32_bf16 v[60:63], v[148:151], v[172:175], v[60:63]
	v_mfma_f32_16x16x32_bf16 v[48:51], v[128:131], v[180:183], v[48:51]
	v_mfma_f32_16x16x32_bf16 v[44:47], v[148:151], v[180:183], v[44:47]
	v_mfma_f32_16x16x32_bf16 v[32:35], v[128:131], v[188:191], v[32:35]
	v_mfma_f32_16x16x32_bf16 v[28:31], v[148:151], v[188:191], v[28:31]
	v_mfma_f32_16x16x32_bf16 v[16:19], v[128:131], v[196:199], v[16:19]
	v_mfma_f32_16x16x32_bf16 v[12:15], v[148:151], v[196:199], v[12:15]
	v_mfma_f32_16x16x32_bf16 v[56:59], v[152:155], v[168:171], v[56:59]
	v_mfma_f32_16x16x32_bf16 v[52:55], v[160:163], v[168:171], v[52:55]
	v_mfma_f32_16x16x32_bf16 v[40:43], v[152:155], v[176:179], v[40:43]
	v_mfma_f32_16x16x32_bf16 v[36:39], v[160:163], v[176:179], v[36:39]
	v_mfma_f32_16x16x32_bf16 v[24:27], v[152:155], v[184:187], v[24:27]
	v_mfma_f32_16x16x32_bf16 v[20:23], v[160:163], v[184:187], v[20:23]
	v_mfma_f32_16x16x32_bf16 v[8:11], v[152:155], v[192:195], v[8:11]
	v_mfma_f32_16x16x32_bf16 v[4:7], v[160:163], v[192:195], v[4:7]
	v_mfma_f32_16x16x32_bf16 v[56:59], v[156:159], v[172:175], v[56:59]
	v_mfma_f32_16x16x32_bf16 v[52:55], v[164:167], v[172:175], v[52:55]
	v_mfma_f32_16x16x32_bf16 v[40:43], v[156:159], v[180:183], v[40:43]
	v_mfma_f32_16x16x32_bf16 v[36:39], v[164:167], v[180:183], v[36:39]
	v_mfma_f32_16x16x32_bf16 v[24:27], v[156:159], v[188:191], v[24:27]
	v_mfma_f32_16x16x32_bf16 v[20:23], v[164:167], v[188:191], v[20:23]
	v_mfma_f32_16x16x32_bf16 v[8:11], v[156:159], v[196:199], v[8:11]
	v_mfma_f32_16x16x32_bf16 v[4:7], v[164:167], v[196:199], v[4:7]
	s_setprio 0
	s_barrier
	s_add_i32 s72, s72, 2
	s_add_u32 s48, s48, 0x100
	s_addc_u32 s49, s49, 0
	s_cmp_gt_u32 s72, 13
.LBB0_1118:
	s_add_u32 s4, s44, s48
	s_addc_u32 s5, s45, s49
	s_add_u32 s98, s4, 0x40080
	s_addc_u32 s99, s5, 0
	s_add_u32 s73, s4, 0x100
	s_addc_u32 s74, s5, 0
	s_add_u32 s50, s70, s48
	s_addc_u32 s51, s71, s49
	s_add_u32 s4, s4, 0x180
	s_addc_u32 s5, s5, 0
	s_add_i32 s75, 0, 0x10000
	s_add_i32 s76, 0, 0x14000
	v_add_u32_e32 v148, s75, v203
	v_add_u32_e32 v164, s76, v203
	ds_read_b128 v[116:119], v148
	ds_read_b128 v[128:131], v148 offset:1024
	ds_read_b128 v[136:139], v148 offset:2048
	ds_read_b128 v[148:151], v148 offset:3072
	ds_read_b128 v[152:155], v164
	ds_read_b128 v[156:159], v164 offset:1024
	ds_read_b128 v[160:163], v164 offset:2048
	ds_read_b128 v[164:167], v164 offset:3072
	s_cmpk_eq_i32 s48, 0x700
	s_cselect_b32 s13, s69, s5
	s_cselect_b32 s12, s68, s4
	s_cselect_b32 s51, s23, s51
	s_cselect_b32 s50, s65, s50
	s_cselect_b32 s5, s37, s74
	s_cselect_b32 s4, s64, s73
	s_add_i32 m0, s17, 0xc000
	ds_read_b128 v[168:171], v236
	ds_read_b128 v[172:175], v236 offset:1024
	ds_read_b128 v[176:179], v236 offset:2048
	ds_read_b128 v[180:183], v236 offset:3072
	ds_read_b128 v[184:187], v236 offset:4096
	ds_read_b128 v[188:191], v236 offset:5120
	ds_read_b128 v[192:195], v236 offset:6144
	ds_read_b128 v[196:199], v236 offset:7168
	global_load_lds_dwordx4 v210, s[98:99]
	s_add_i32 m0, s17, 0xe000
	s_nop 0
	global_load_lds_dwordx4 v212, s[98:99]
	s_waitcnt vmcnt(8)
	s_waitcnt lgkmcnt(0)
	s_barrier
	s_setprio 1
	v_mfma_f32_16x16x32_bf16 v[144:147], v[116:119], v[168:171], v[144:147]
	v_mfma_f32_16x16x32_bf16 v[140:143], v[136:139], v[168:171], v[140:143]
	v_mfma_f32_16x16x32_bf16 v[120:123], v[116:119], v[176:179], v[120:123]
	v_mfma_f32_16x16x32_bf16 v[112:115], v[136:139], v[176:179], v[112:115]
	v_mfma_f32_16x16x32_bf16 v[96:99], v[116:119], v[184:187], v[96:99]
	v_mfma_f32_16x16x32_bf16 v[92:95], v[136:139], v[184:187], v[92:95]
	v_mfma_f32_16x16x32_bf16 v[80:83], v[116:119], v[192:195], v[80:83]
	v_mfma_f32_16x16x32_bf16 v[76:79], v[136:139], v[192:195], v[76:79]
	v_mfma_f32_16x16x32_bf16 v[144:147], v[128:131], v[172:175], v[144:147]
	v_mfma_f32_16x16x32_bf16 v[140:143], v[148:151], v[172:175], v[140:143]
	v_mfma_f32_16x16x32_bf16 v[120:123], v[128:131], v[180:183], v[120:123]
	v_mfma_f32_16x16x32_bf16 v[112:115], v[148:151], v[180:183], v[112:115]
	v_mfma_f32_16x16x32_bf16 v[96:99], v[128:131], v[188:191], v[96:99]
	v_mfma_f32_16x16x32_bf16 v[92:95], v[148:151], v[188:191], v[92:95]
	v_mfma_f32_16x16x32_bf16 v[80:83], v[128:131], v[196:199], v[80:83]
	v_mfma_f32_16x16x32_bf16 v[76:79], v[148:151], v[196:199], v[76:79]
	v_mfma_f32_16x16x32_bf16 v[132:135], v[152:155], v[168:171], v[132:135]
	v_mfma_f32_16x16x32_bf16 v[124:127], v[160:163], v[168:171], v[124:127]
	v_mfma_f32_16x16x32_bf16 v[104:107], v[152:155], v[176:179], v[104:107]
	v_mfma_f32_16x16x32_bf16 v[100:103], v[160:163], v[176:179], v[100:103]
	v_mfma_f32_16x16x32_bf16 v[88:91], v[152:155], v[184:187], v[88:91]
	v_mfma_f32_16x16x32_bf16 v[84:87], v[160:163], v[184:187], v[84:87]
	v_mfma_f32_16x16x32_bf16 v[72:75], v[152:155], v[192:195], v[72:75]
	v_mfma_f32_16x16x32_bf16 v[68:71], v[160:163], v[192:195], v[68:71]
	v_mfma_f32_16x16x32_bf16 v[132:135], v[156:159], v[172:175], v[132:135]
	v_mfma_f32_16x16x32_bf16 v[124:127], v[164:167], v[172:175], v[124:127]
	v_mfma_f32_16x16x32_bf16 v[104:107], v[156:159], v[180:183], v[104:107]
	v_mfma_f32_16x16x32_bf16 v[100:103], v[164:167], v[180:183], v[100:103]
	v_mfma_f32_16x16x32_bf16 v[88:91], v[156:159], v[188:191], v[88:91]
	v_mfma_f32_16x16x32_bf16 v[84:87], v[164:167], v[188:191], v[84:87]
	v_mfma_f32_16x16x32_bf16 v[72:75], v[156:159], v[196:199], v[72:75]
	v_mfma_f32_16x16x32_bf16 v[68:71], v[164:167], v[196:199], v[68:71]
	s_setprio 0
	s_barrier
	s_add_i32 s73, s75, s16
	s_mov_b32 m0, s73
	ds_read_b128 v[168:171], v236 offset:16384
	ds_read_b128 v[172:175], v236 offset:17408
	ds_read_b128 v[176:179], v236 offset:18432
	ds_read_b128 v[180:183], v236 offset:19456
	ds_read_b128 v[184:187], v236 offset:20480
	ds_read_b128 v[188:191], v236 offset:21504
	ds_read_b128 v[192:195], v236 offset:22528
	ds_read_b128 v[196:199], v236 offset:23552
	global_load_lds_dwordx4 v2, s[50:51]
	s_add_i32 m0, s73, 0x2000
	s_add_u32 s74, s50, 0x40000
	s_addc_u32 s75, s51, 0
	s_add_i32 s73, s76, s16
	global_load_lds_dwordx4 v204, s[50:51]
	s_mov_b32 m0, s73
	s_nop 0
	global_load_lds_dwordx4 v2, s[74:75]
	s_add_i32 m0, s73, 0x2000
	s_nop 0
	global_load_lds_dwordx4 v204, s[74:75]
	s_mov_b32 m0, s17
	s_nop 0
	global_load_lds_dwordx4 v208, s[4:5]
	s_mov_b32 m0, s46
	s_nop 0
	global_load_lds_dwordx4 v206, s[4:5]
	s_waitcnt vmcnt(8)
	s_waitcnt lgkmcnt(0)
	s_barrier
	s_setprio 1
	v_mfma_f32_16x16x32_bf16 v[64:67], v[116:119], v[168:171], v[64:67]
	v_mfma_f32_16x16x32_bf16 v[60:63], v[136:139], v[168:171], v[60:63]
	v_mfma_f32_16x16x32_bf16 v[48:51], v[116:119], v[176:179], v[48:51]
	v_mfma_f32_16x16x32_bf16 v[44:47], v[136:139], v[176:179], v[44:47]
	v_mfma_f32_16x16x32_bf16 v[32:35], v[116:119], v[184:187], v[32:35]
	v_mfma_f32_16x16x32_bf16 v[28:31], v[136:139], v[184:187], v[28:31]
	v_mfma_f32_16x16x32_bf16 v[16:19], v[116:119], v[192:195], v[16:19]
	v_mfma_f32_16x16x32_bf16 v[12:15], v[136:139], v[192:195], v[12:15]
	v_mfma_f32_16x16x32_bf16 v[64:67], v[128:131], v[172:175], v[64:67]
	v_mfma_f32_16x16x32_bf16 v[60:63], v[148:151], v[172:175], v[60:63]
	v_mfma_f32_16x16x32_bf16 v[48:51], v[128:131], v[180:183], v[48:51]
	v_mfma_f32_16x16x32_bf16 v[44:47], v[148:151], v[180:183], v[44:47]
	v_mfma_f32_16x16x32_bf16 v[32:35], v[128:131], v[188:191], v[32:35]
	v_mfma_f32_16x16x32_bf16 v[28:31], v[148:151], v[188:191], v[28:31]
	v_mfma_f32_16x16x32_bf16 v[16:19], v[128:131], v[196:199], v[16:19]
	v_mfma_f32_16x16x32_bf16 v[12:15], v[148:151], v[196:199], v[12:15]
	v_mfma_f32_16x16x32_bf16 v[56:59], v[152:155], v[168:171], v[56:59]
	v_mfma_f32_16x16x32_bf16 v[52:55], v[160:163], v[168:171], v[52:55]
	v_mfma_f32_16x16x32_bf16 v[40:43], v[152:155], v[176:179], v[40:43]
	v_mfma_f32_16x16x32_bf16 v[36:39], v[160:163], v[176:179], v[36:39]
	v_mfma_f32_16x16x32_bf16 v[24:27], v[152:155], v[184:187], v[24:27]
	v_mfma_f32_16x16x32_bf16 v[20:23], v[160:163], v[184:187], v[20:23]
	v_mfma_f32_16x16x32_bf16 v[8:11], v[152:155], v[192:195], v[8:11]
	v_mfma_f32_16x16x32_bf16 v[4:7], v[160:163], v[192:195], v[4:7]
	v_mfma_f32_16x16x32_bf16 v[56:59], v[156:159], v[172:175], v[56:59]
	v_mfma_f32_16x16x32_bf16 v[52:55], v[164:167], v[172:175], v[52:55]
	v_mfma_f32_16x16x32_bf16 v[40:43], v[156:159], v[180:183], v[40:43]
	v_mfma_f32_16x16x32_bf16 v[36:39], v[164:167], v[180:183], v[36:39]
	v_mfma_f32_16x16x32_bf16 v[24:27], v[156:159], v[188:191], v[24:27]
	v_mfma_f32_16x16x32_bf16 v[20:23], v[164:167], v[188:191], v[20:23]
	v_mfma_f32_16x16x32_bf16 v[8:11], v[156:159], v[196:199], v[8:11]
	v_mfma_f32_16x16x32_bf16 v[4:7], v[164:167], v[196:199], v[4:7]
	s_setprio 0
	s_barrier
	s_add_i32 s73, 0, 0x18000
	s_add_i32 s74, 0, 0x1c000
	v_add_u32_e32 v148, s73, v203
	v_add_u32_e32 v164, s74, v203
	ds_read_b128 v[116:119], v148
	ds_read_b128 v[128:131], v148 offset:1024
	ds_read_b128 v[136:139], v148 offset:2048
	ds_read_b128 v[148:151], v148 offset:3072
	ds_read_b128 v[152:155], v164
	ds_read_b128 v[156:159], v164 offset:1024
	ds_read_b128 v[160:163], v164 offset:2048
	ds_read_b128 v[164:167], v164 offset:3072
	s_add_u32 s4, s4, 0x40000
	s_addc_u32 s5, s5, 0
	s_mov_b32 m0, s47
	ds_read_b128 v[168:171], v236 offset:32768
	ds_read_b128 v[172:175], v236 offset:33792
	ds_read_b128 v[176:179], v236 offset:34816
	ds_read_b128 v[180:183], v236 offset:35840
	ds_read_b128 v[184:187], v236 offset:36864
	ds_read_b128 v[188:191], v236 offset:37888
	ds_read_b128 v[192:195], v236 offset:38912
	ds_read_b128 v[196:199], v236 offset:39936
	global_load_lds_dwordx4 v208, s[4:5]
	s_mov_b32 m0, s52
	s_nop 0
	global_load_lds_dwordx4 v206, s[4:5]
	s_waitcnt vmcnt(8)
	s_waitcnt lgkmcnt(0)
	s_barrier
	s_setprio 1
	v_mfma_f32_16x16x32_bf16 v[144:147], v[116:119], v[168:171], v[144:147]
	v_mfma_f32_16x16x32_bf16 v[140:143], v[136:139], v[168:171], v[140:143]
	v_mfma_f32_16x16x32_bf16 v[120:123], v[116:119], v[176:179], v[120:123]
	v_mfma_f32_16x16x32_bf16 v[112:115], v[136:139], v[176:179], v[112:115]
	v_mfma_f32_16x16x32_bf16 v[96:99], v[116:119], v[184:187], v[96:99]
	v_mfma_f32_16x16x32_bf16 v[92:95], v[136:139], v[184:187], v[92:95]
	v_mfma_f32_16x16x32_bf16 v[80:83], v[116:119], v[192:195], v[80:83]
	v_mfma_f32_16x16x32_bf16 v[76:79], v[136:139], v[192:195], v[76:79]
	v_mfma_f32_16x16x32_bf16 v[144:147], v[128:131], v[172:175], v[144:147]
	v_mfma_f32_16x16x32_bf16 v[140:143], v[148:151], v[172:175], v[140:143]
	v_mfma_f32_16x16x32_bf16 v[120:123], v[128:131], v[180:183], v[120:123]
	v_mfma_f32_16x16x32_bf16 v[112:115], v[148:151], v[180:183], v[112:115]
	v_mfma_f32_16x16x32_bf16 v[96:99], v[128:131], v[188:191], v[96:99]
	v_mfma_f32_16x16x32_bf16 v[92:95], v[148:151], v[188:191], v[92:95]
	v_mfma_f32_16x16x32_bf16 v[80:83], v[128:131], v[196:199], v[80:83]
	v_mfma_f32_16x16x32_bf16 v[76:79], v[148:151], v[196:199], v[76:79]
	v_mfma_f32_16x16x32_bf16 v[132:135], v[152:155], v[168:171], v[132:135]
	v_mfma_f32_16x16x32_bf16 v[124:127], v[160:163], v[168:171], v[124:127]
	v_mfma_f32_16x16x32_bf16 v[104:107], v[152:155], v[176:179], v[104:107]
	v_mfma_f32_16x16x32_bf16 v[100:103], v[160:163], v[176:179], v[100:103]
	v_mfma_f32_16x16x32_bf16 v[88:91], v[152:155], v[184:187], v[88:91]
	v_mfma_f32_16x16x32_bf16 v[84:87], v[160:163], v[184:187], v[84:87]
	v_mfma_f32_16x16x32_bf16 v[72:75], v[152:155], v[192:195], v[72:75]
	v_mfma_f32_16x16x32_bf16 v[68:71], v[160:163], v[192:195], v[68:71]
	v_mfma_f32_16x16x32_bf16 v[132:135], v[156:159], v[172:175], v[132:135]
	v_mfma_f32_16x16x32_bf16 v[124:127], v[164:167], v[172:175], v[124:127]
	v_mfma_f32_16x16x32_bf16 v[104:107], v[156:159], v[180:183], v[104:107]
	v_mfma_f32_16x16x32_bf16 v[100:103], v[164:167], v[180:183], v[100:103]
	v_mfma_f32_16x16x32_bf16 v[88:91], v[156:159], v[188:191], v[88:91]
	v_mfma_f32_16x16x32_bf16 v[84:87], v[164:167], v[188:191], v[84:87]
	v_mfma_f32_16x16x32_bf16 v[72:75], v[156:159], v[196:199], v[72:75]
	v_mfma_f32_16x16x32_bf16 v[68:71], v[164:167], v[196:199], v[68:71]
	s_setprio 0
	s_barrier
	s_add_i32 s4, s73, s16
	s_add_u32 s98, s50, 0x80
	s_addc_u32 s99, s51, 0
	s_mov_b32 m0, s4
	ds_read_b128 v[168:171], v236 offset:49152
	ds_read_b128 v[172:175], v236 offset:50176
	ds_read_b128 v[176:179], v236 offset:51200
	ds_read_b128 v[180:183], v236 offset:52224
	ds_read_b128 v[184:187], v236 offset:53248
	ds_read_b128 v[188:191], v236 offset:54272
	ds_read_b128 v[192:195], v236 offset:55296
	ds_read_b128 v[196:199], v236 offset:56320
	global_load_lds_dwordx4 v2, s[98:99]
	s_add_i32 m0, s4, 0x2000
	s_add_u32 s4, s50, 0x40080
	s_addc_u32 s5, s51, 0
	s_add_i32 s50, s74, s16
	global_load_lds_dwordx4 v204, s[98:99]
	s_mov_b32 m0, s50
	s_nop 0
	global_load_lds_dwordx4 v2, s[4:5]
	s_add_i32 m0, s50, 0x2000
	s_nop 0
	global_load_lds_dwordx4 v204, s[4:5]
	s_mov_b32 m0, s60
	s_nop 0
	global_load_lds_dwordx4 v208, s[12:13]
	s_mov_b32 m0, s61
	s_nop 0
	global_load_lds_dwordx4 v206, s[12:13]
	s_waitcnt vmcnt(8)
	s_waitcnt lgkmcnt(0)
	s_barrier
	s_setprio 1
	v_mfma_f32_16x16x32_bf16 v[64:67], v[116:119], v[168:171], v[64:67]
	v_mfma_f32_16x16x32_bf16 v[60:63], v[136:139], v[168:171], v[60:63]
	v_mfma_f32_16x16x32_bf16 v[48:51], v[116:119], v[176:179], v[48:51]
	v_mfma_f32_16x16x32_bf16 v[44:47], v[136:139], v[176:179], v[44:47]
	v_mfma_f32_16x16x32_bf16 v[32:35], v[116:119], v[184:187], v[32:35]
	v_mfma_f32_16x16x32_bf16 v[28:31], v[136:139], v[184:187], v[28:31]
	v_mfma_f32_16x16x32_bf16 v[16:19], v[116:119], v[192:195], v[16:19]
	v_mfma_f32_16x16x32_bf16 v[12:15], v[136:139], v[192:195], v[12:15]
	v_mfma_f32_16x16x32_bf16 v[64:67], v[128:131], v[172:175], v[64:67]
	v_mfma_f32_16x16x32_bf16 v[60:63], v[148:151], v[172:175], v[60:63]
	v_mfma_f32_16x16x32_bf16 v[48:51], v[128:131], v[180:183], v[48:51]
	v_mfma_f32_16x16x32_bf16 v[44:47], v[148:151], v[180:183], v[44:47]
	v_mfma_f32_16x16x32_bf16 v[32:35], v[128:131], v[188:191], v[32:35]
	v_mfma_f32_16x16x32_bf16 v[28:31], v[148:151], v[188:191], v[28:31]
	v_mfma_f32_16x16x32_bf16 v[16:19], v[128:131], v[196:199], v[16:19]
	v_mfma_f32_16x16x32_bf16 v[12:15], v[148:151], v[196:199], v[12:15]
	v_mfma_f32_16x16x32_bf16 v[56:59], v[152:155], v[168:171], v[56:59]
	v_mfma_f32_16x16x32_bf16 v[52:55], v[160:163], v[168:171], v[52:55]
	v_mfma_f32_16x16x32_bf16 v[40:43], v[152:155], v[176:179], v[40:43]
	v_mfma_f32_16x16x32_bf16 v[36:39], v[160:163], v[176:179], v[36:39]
	v_mfma_f32_16x16x32_bf16 v[24:27], v[152:155], v[184:187], v[24:27]
	v_mfma_f32_16x16x32_bf16 v[20:23], v[160:163], v[184:187], v[20:23]
	v_mfma_f32_16x16x32_bf16 v[8:11], v[152:155], v[192:195], v[8:11]
	v_mfma_f32_16x16x32_bf16 v[4:7], v[160:163], v[192:195], v[4:7]
	v_mfma_f32_16x16x32_bf16 v[56:59], v[156:159], v[172:175], v[56:59]
	v_mfma_f32_16x16x32_bf16 v[52:55], v[164:167], v[172:175], v[52:55]
	v_mfma_f32_16x16x32_bf16 v[40:43], v[156:159], v[180:183], v[40:43]
	v_mfma_f32_16x16x32_bf16 v[36:39], v[164:167], v[180:183], v[36:39]
	v_mfma_f32_16x16x32_bf16 v[24:27], v[156:159], v[188:191], v[24:27]
	v_mfma_f32_16x16x32_bf16 v[20:23], v[164:167], v[188:191], v[20:23]
	v_mfma_f32_16x16x32_bf16 v[8:11], v[156:159], v[196:199], v[8:11]
	v_mfma_f32_16x16x32_bf16 v[4:7], v[164:167], v[196:199], v[4:7]
	s_setprio 0
	s_barrier
	s_add_i32 s72, s72, 2
	s_add_u32 s48, s48, 0x100
	s_addc_u32 s49, s49, 0
	s_cmp_gt_u32 s72, 13
	s_cbranch_scc0 .LBB0_1118
	s_and_b64 vcc, exec, s[20:21]
	s_cbranch_vccz .LBB0_1121
	s_barrier

.LBB0_1205:
	s_ashr_i32 s37, s36, 31
	s_lshl_b64 s[4:5], s[36:37], 19
	s_add_u32 s40, s6, s4
	s_addc_u32 s41, s7, s5
	s_and_b64 s[4:5], s[38:39], exec
	s_cselect_b32 s37, s41, s23
	s_cselect_b32 s61, s40, s22
	s_ashr_i32 s21, s20, 31
	s_lshl_b64 s[4:5], s[20:21], 19
	s_add_u32 s42, s8, s4
	s_addc_u32 s43, s9, s5
	s_and_b64 s[4:5], s[38:39], exec
	s_cselect_b32 s21, s43, s45
	s_cselect_b32 s62, s42, s44
	s_add_u32 s63, s61, 0x80
	s_addc_u32 s64, s37, 0
	s_add_u32 s4, s22, 0x40080
	s_addc_u32 s5, s23, 0
	s_add_u32 s65, s44, 0x100
	v_lshl_add_u64 v[142:143], s[4:5], 0, v[138:139]
	v_lshl_add_u64 v[144:145], s[4:5], 0, v[140:141]
	s_addc_u32 s68, s45, 0
	s_mov_b32 s69, -2
	s_mov_b64 s[44:45], 0
	s_add_u32 s4, s22, s44
	s_addc_u32 s5, s23, s45
	s_add_u32 s98, s4, 0x40080
	s_addc_u32 s99, s5, 0
	s_add_u32 s70, s4, 0x100
	s_addc_u32 s71, s5, 0
	s_add_u32 s48, s65, s44
	s_addc_u32 s49, s68, s45
	s_add_u32 s4, s4, 0x180
	s_addc_u32 s5, s5, 0
	s_add_i32 s72, 0, 0x10000
	s_add_i32 s73, 0, 0x14000
	v_add_u32_e32 v160, s72, v146
	v_add_u32_e32 v176, s73, v146
	ds_read_b128 v[148:151], v160
	ds_read_b128 v[152:155], v160 offset:1024
	ds_read_b128 v[156:159], v160 offset:2048
	ds_read_b128 v[160:163], v160 offset:3072
	ds_read_b128 v[164:167], v176
	ds_read_b128 v[168:171], v176 offset:1024
	ds_read_b128 v[172:175], v176 offset:2048
	ds_read_b128 v[176:179], v176 offset:3072
	s_cmpk_eq_i32 s44, 0x700
	s_cselect_b32 s13, s64, s5
	s_cselect_b32 s12, s63, s4
	s_cselect_b32 s49, s21, s49
	s_cselect_b32 s48, s62, s48
	s_cselect_b32 s5, s37, s71
	s_cselect_b32 s4, s61, s70
	s_add_i32 m0, s17, 0xc000
	ds_read_b128 v[180:183], v147
	ds_read_b128 v[184:187], v147 offset:1024
	ds_read_b128 v[188:191], v147 offset:2048
	ds_read_b128 v[192:195], v147 offset:3072
	ds_read_b128 v[196:199], v147 offset:4096
	ds_read_b128 v[204:207], v147 offset:5120
	ds_read_b128 v[208:211], v147 offset:6144
	ds_read_b128 v[212:215], v147 offset:7168
	global_load_lds_dwordx4 v138, s[98:99]
	s_add_i32 m0, s17, 0xe000
	s_nop 0
	global_load_lds_dwordx4 v140, s[98:99]
	s_waitcnt vmcnt(8)
	s_waitcnt lgkmcnt(0)
	s_barrier
	s_setprio 1
	v_mfma_f32_16x16x32_bf16 v[128:131], v[148:151], v[180:183], 0
	v_mfma_f32_16x16x32_bf16 v[124:127], v[156:159], v[180:183], 0
	v_mfma_f32_16x16x32_bf16 v[120:123], v[148:151], v[188:191], 0
	v_mfma_f32_16x16x32_bf16 v[116:119], v[156:159], v[188:191], 0
	v_mfma_f32_16x16x32_bf16 v[104:107], v[148:151], v[196:199], 0
	v_mfma_f32_16x16x32_bf16 v[100:103], v[156:159], v[196:199], 0
	v_mfma_f32_16x16x32_bf16 v[88:91], v[148:151], v[208:211], 0
	v_mfma_f32_16x16x32_bf16 v[84:87], v[156:159], v[208:211], 0
	v_mfma_f32_16x16x32_bf16 v[128:131], v[152:155], v[184:187], v[128:131]
	v_mfma_f32_16x16x32_bf16 v[124:127], v[160:163], v[184:187], v[124:127]
	v_mfma_f32_16x16x32_bf16 v[120:123], v[152:155], v[192:195], v[120:123]
	v_mfma_f32_16x16x32_bf16 v[116:119], v[160:163], v[192:195], v[116:119]
	v_mfma_f32_16x16x32_bf16 v[104:107], v[152:155], v[204:207], v[104:107]
	v_mfma_f32_16x16x32_bf16 v[100:103], v[160:163], v[204:207], v[100:103]
	v_mfma_f32_16x16x32_bf16 v[88:91], v[152:155], v[212:215], v[88:91]
	v_mfma_f32_16x16x32_bf16 v[84:87], v[160:163], v[212:215], v[84:87]
	v_mfma_f32_16x16x32_bf16 v[112:115], v[164:167], v[180:183], 0
	v_mfma_f32_16x16x32_bf16 v[108:111], v[172:175], v[180:183], 0
	v_mfma_f32_16x16x32_bf16 v[96:99], v[164:167], v[188:191], 0
	v_mfma_f32_16x16x32_bf16 v[92:95], v[172:175], v[188:191], 0
	v_mfma_f32_16x16x32_bf16 v[80:83], v[164:167], v[196:199], 0
	v_mfma_f32_16x16x32_bf16 v[76:79], v[172:175], v[196:199], 0
	v_mfma_f32_16x16x32_bf16 v[72:75], v[164:167], v[208:211], 0
	v_mfma_f32_16x16x32_bf16 v[68:71], v[172:175], v[208:211], 0
	v_mfma_f32_16x16x32_bf16 v[112:115], v[168:171], v[184:187], v[112:115]
	v_mfma_f32_16x16x32_bf16 v[108:111], v[176:179], v[184:187], v[108:111]
	v_mfma_f32_16x16x32_bf16 v[96:99], v[168:171], v[192:195], v[96:99]
	v_mfma_f32_16x16x32_bf16 v[92:95], v[176:179], v[192:195], v[92:95]
	v_mfma_f32_16x16x32_bf16 v[80:83], v[168:171], v[204:207], v[80:83]
	v_mfma_f32_16x16x32_bf16 v[76:79], v[176:179], v[204:207], v[76:79]
	v_mfma_f32_16x16x32_bf16 v[72:75], v[168:171], v[212:215], v[72:75]
	v_mfma_f32_16x16x32_bf16 v[68:71], v[176:179], v[212:215], v[68:71]
	s_setprio 0
	s_barrier
	s_add_i32 s70, s72, s16
	s_mov_b32 m0, s70
	ds_read_b128 v[180:183], v147 offset:16384
	ds_read_b128 v[184:187], v147 offset:17408
	ds_read_b128 v[188:191], v147 offset:18432
	ds_read_b128 v[192:195], v147 offset:19456
	ds_read_b128 v[196:199], v147 offset:20480
	ds_read_b128 v[204:207], v147 offset:21504
	ds_read_b128 v[208:211], v147 offset:22528
	ds_read_b128 v[212:215], v147 offset:23552
	global_load_lds_dwordx4 v2, s[48:49]
	s_add_i32 m0, s70, 0x2000
	s_add_u32 s70, s48, 0x40000
	s_addc_u32 s71, s49, 0
	s_add_i32 s72, s73, s16
	global_load_lds_dwordx4 v132, s[48:49]
	s_mov_b32 m0, s72
	s_nop 0
	global_load_lds_dwordx4 v2, s[70:71]
	s_add_i32 m0, s72, 0x2000
	s_nop 0
	global_load_lds_dwordx4 v132, s[70:71]
	s_mov_b32 m0, s17
	s_nop 0
	global_load_lds_dwordx4 v136, s[4:5]
	s_mov_b32 m0, s46
	s_nop 0
	global_load_lds_dwordx4 v134, s[4:5]
	s_waitcnt vmcnt(8)
	s_waitcnt lgkmcnt(0)
	s_barrier
	s_setprio 1
	v_mfma_f32_16x16x32_bf16 v[64:67], v[148:151], v[180:183], 0
	v_mfma_f32_16x16x32_bf16 v[60:63], v[156:159], v[180:183], 0
	v_mfma_f32_16x16x32_bf16 v[56:59], v[148:151], v[188:191], 0
	v_mfma_f32_16x16x32_bf16 v[52:55], v[156:159], v[188:191], 0
	v_mfma_f32_16x16x32_bf16 v[40:43], v[148:151], v[196:199], 0
	v_mfma_f32_16x16x32_bf16 v[36:39], v[156:159], v[196:199], 0
	v_mfma_f32_16x16x32_bf16 v[24:27], v[148:151], v[208:211], 0
	v_mfma_f32_16x16x32_bf16 v[20:23], v[156:159], v[208:211], 0
	v_mfma_f32_16x16x32_bf16 v[64:67], v[152:155], v[184:187], v[64:67]
	v_mfma_f32_16x16x32_bf16 v[60:63], v[160:163], v[184:187], v[60:63]
	v_mfma_f32_16x16x32_bf16 v[56:59], v[152:155], v[192:195], v[56:59]
	v_mfma_f32_16x16x32_bf16 v[52:55], v[160:163], v[192:195], v[52:55]
	v_mfma_f32_16x16x32_bf16 v[40:43], v[152:155], v[204:207], v[40:43]
	v_mfma_f32_16x16x32_bf16 v[36:39], v[160:163], v[204:207], v[36:39]
	v_mfma_f32_16x16x32_bf16 v[24:27], v[152:155], v[212:215], v[24:27]
	v_mfma_f32_16x16x32_bf16 v[20:23], v[160:163], v[212:215], v[20:23]
	v_mfma_f32_16x16x32_bf16 v[48:51], v[164:167], v[180:183], 0
	v_mfma_f32_16x16x32_bf16 v[44:47], v[172:175], v[180:183], 0
	v_mfma_f32_16x16x32_bf16 v[32:35], v[164:167], v[188:191], 0
	v_mfma_f32_16x16x32_bf16 v[28:31], v[172:175], v[188:191], 0
	v_mfma_f32_16x16x32_bf16 v[16:19], v[164:167], v[196:199], 0
	v_mfma_f32_16x16x32_bf16 v[12:15], v[172:175], v[196:199], 0
	v_mfma_f32_16x16x32_bf16 v[8:11], v[164:167], v[208:211], 0
	v_mfma_f32_16x16x32_bf16 v[4:7], v[172:175], v[208:211], 0
	v_mfma_f32_16x16x32_bf16 v[48:51], v[168:171], v[184:187], v[48:51]
	v_mfma_f32_16x16x32_bf16 v[44:47], v[176:179], v[184:187], v[44:47]
	v_mfma_f32_16x16x32_bf16 v[32:35], v[168:171], v[192:195], v[32:35]
	v_mfma_f32_16x16x32_bf16 v[28:31], v[176:179], v[192:195], v[28:31]
	v_mfma_f32_16x16x32_bf16 v[16:19], v[168:171], v[204:207], v[16:19]
	v_mfma_f32_16x16x32_bf16 v[12:15], v[176:179], v[204:207], v[12:15]
	v_mfma_f32_16x16x32_bf16 v[8:11], v[168:171], v[212:215], v[8:11]
	v_mfma_f32_16x16x32_bf16 v[4:7], v[176:179], v[212:215], v[4:7]
	s_setprio 0
	s_barrier
	s_add_i32 s70, 0, 0x18000
	s_add_i32 s71, 0, 0x1c000
	v_add_u32_e32 v160, s70, v146
	v_add_u32_e32 v176, s71, v146
	ds_read_b128 v[148:151], v160
	ds_read_b128 v[152:155], v160 offset:1024
	ds_read_b128 v[156:159], v160 offset:2048
	ds_read_b128 v[160:163], v160 offset:3072
	ds_read_b128 v[164:167], v176
	ds_read_b128 v[168:171], v176 offset:1024
	ds_read_b128 v[172:175], v176 offset:2048
	ds_read_b128 v[176:179], v176 offset:3072
	s_add_u32 s4, s4, 0x40000
	s_addc_u32 s5, s5, 0
	s_mov_b32 m0, s47
	ds_read_b128 v[180:183], v147 offset:32768
	ds_read_b128 v[184:187], v147 offset:33792
	ds_read_b128 v[188:191], v147 offset:34816
	ds_read_b128 v[192:195], v147 offset:35840
	ds_read_b128 v[196:199], v147 offset:36864
	ds_read_b128 v[204:207], v147 offset:37888
	ds_read_b128 v[208:211], v147 offset:38912
	ds_read_b128 v[212:215], v147 offset:39936
	global_load_lds_dwordx4 v136, s[4:5]
	s_mov_b32 m0, s50
	s_nop 0
	global_load_lds_dwordx4 v134, s[4:5]
	s_waitcnt vmcnt(8)
	s_waitcnt lgkmcnt(0)
	s_barrier
	s_setprio 1
	v_mfma_f32_16x16x32_bf16 v[128:131], v[148:151], v[180:183], v[128:131]
	v_mfma_f32_16x16x32_bf16 v[124:127], v[156:159], v[180:183], v[124:127]
	v_mfma_f32_16x16x32_bf16 v[120:123], v[148:151], v[188:191], v[120:123]
	v_mfma_f32_16x16x32_bf16 v[116:119], v[156:159], v[188:191], v[116:119]
	v_mfma_f32_16x16x32_bf16 v[104:107], v[148:151], v[196:199], v[104:107]
	v_mfma_f32_16x16x32_bf16 v[100:103], v[156:159], v[196:199], v[100:103]
	v_mfma_f32_16x16x32_bf16 v[88:91], v[148:151], v[208:211], v[88:91]
	v_mfma_f32_16x16x32_bf16 v[84:87], v[156:159], v[208:211], v[84:87]
	v_mfma_f32_16x16x32_bf16 v[128:131], v[152:155], v[184:187], v[128:131]
	v_mfma_f32_16x16x32_bf16 v[124:127], v[160:163], v[184:187], v[124:127]
	v_mfma_f32_16x16x32_bf16 v[120:123], v[152:155], v[192:195], v[120:123]
	v_mfma_f32_16x16x32_bf16 v[116:119], v[160:163], v[192:195], v[116:119]
	v_mfma_f32_16x16x32_bf16 v[104:107], v[152:155], v[204:207], v[104:107]
	v_mfma_f32_16x16x32_bf16 v[100:103], v[160:163], v[204:207], v[100:103]
	v_mfma_f32_16x16x32_bf16 v[88:91], v[152:155], v[212:215], v[88:91]
	v_mfma_f32_16x16x32_bf16 v[84:87], v[160:163], v[212:215], v[84:87]
	v_mfma_f32_16x16x32_bf16 v[112:115], v[164:167], v[180:183], v[112:115]
	v_mfma_f32_16x16x32_bf16 v[108:111], v[172:175], v[180:183], v[108:111]
	v_mfma_f32_16x16x32_bf16 v[96:99], v[164:167], v[188:191], v[96:99]
	v_mfma_f32_16x16x32_bf16 v[92:95], v[172:175], v[188:191], v[92:95]
	v_mfma_f32_16x16x32_bf16 v[80:83], v[164:167], v[196:199], v[80:83]
	v_mfma_f32_16x16x32_bf16 v[76:79], v[172:175], v[196:199], v[76:79]
	v_mfma_f32_16x16x32_bf16 v[72:75], v[164:167], v[208:211], v[72:75]
	v_mfma_f32_16x16x32_bf16 v[68:71], v[172:175], v[208:211], v[68:71]
	v_mfma_f32_16x16x32_bf16 v[112:115], v[168:171], v[184:187], v[112:115]
	v_mfma_f32_16x16x32_bf16 v[108:111], v[176:179], v[184:187], v[108:111]
	v_mfma_f32_16x16x32_bf16 v[96:99], v[168:171], v[192:195], v[96:99]
	v_mfma_f32_16x16x32_bf16 v[92:95], v[176:179], v[192:195], v[92:95]
	v_mfma_f32_16x16x32_bf16 v[80:83], v[168:171], v[204:207], v[80:83]
	v_mfma_f32_16x16x32_bf16 v[76:79], v[176:179], v[204:207], v[76:79]
	v_mfma_f32_16x16x32_bf16 v[72:75], v[168:171], v[212:215], v[72:75]
	v_mfma_f32_16x16x32_bf16 v[68:71], v[176:179], v[212:215], v[68:71]
	s_setprio 0
	s_barrier
	s_add_i32 s4, s70, s16
	s_add_u32 s98, s48, 0x80
	s_addc_u32 s99, s49, 0
	s_mov_b32 m0, s4
	ds_read_b128 v[180:183], v147 offset:49152
	ds_read_b128 v[184:187], v147 offset:50176
	ds_read_b128 v[188:191], v147 offset:51200
	ds_read_b128 v[192:195], v147 offset:52224
	ds_read_b128 v[196:199], v147 offset:53248
	ds_read_b128 v[204:207], v147 offset:54272
	ds_read_b128 v[208:211], v147 offset:55296
	ds_read_b128 v[212:215], v147 offset:56320
	global_load_lds_dwordx4 v2, s[98:99]
	s_add_i32 m0, s4, 0x2000
	s_add_u32 s4, s48, 0x40080
	s_addc_u32 s5, s49, 0
	s_add_i32 s48, s71, s16
	global_load_lds_dwordx4 v132, s[98:99]
	s_mov_b32 m0, s48
	s_nop 0
	global_load_lds_dwordx4 v2, s[4:5]
	s_add_i32 m0, s48, 0x2000
	s_nop 0
	global_load_lds_dwordx4 v132, s[4:5]
	s_mov_b32 m0, s53
	s_nop 0
	global_load_lds_dwordx4 v136, s[12:13]
	s_mov_b32 m0, s56
	s_nop 0
	global_load_lds_dwordx4 v134, s[12:13]
	s_waitcnt vmcnt(8)
	s_waitcnt lgkmcnt(0)
	s_barrier
	s_setprio 1
	v_mfma_f32_16x16x32_bf16 v[64:67], v[148:151], v[180:183], v[64:67]
	v_mfma_f32_16x16x32_bf16 v[60:63], v[156:159], v[180:183], v[60:63]
	v_mfma_f32_16x16x32_bf16 v[56:59], v[148:151], v[188:191], v[56:59]
	v_mfma_f32_16x16x32_bf16 v[52:55], v[156:159], v[188:191], v[52:55]
	v_mfma_f32_16x16x32_bf16 v[40:43], v[148:151], v[196:199], v[40:43]
	v_mfma_f32_16x16x32_bf16 v[36:39], v[156:159], v[196:199], v[36:39]
	v_mfma_f32_16x16x32_bf16 v[24:27], v[148:151], v[208:211], v[24:27]
	v_mfma_f32_16x16x32_bf16 v[20:23], v[156:159], v[208:211], v[20:23]
	v_mfma_f32_16x16x32_bf16 v[64:67], v[152:155], v[184:187], v[64:67]
	v_mfma_f32_16x16x32_bf16 v[60:63], v[160:163], v[184:187], v[60:63]
	v_mfma_f32_16x16x32_bf16 v[56:59], v[152:155], v[192:195], v[56:59]
	v_mfma_f32_16x16x32_bf16 v[52:55], v[160:163], v[192:195], v[52:55]
	v_mfma_f32_16x16x32_bf16 v[40:43], v[152:155], v[204:207], v[40:43]
	v_mfma_f32_16x16x32_bf16 v[36:39], v[160:163], v[204:207], v[36:39]
	v_mfma_f32_16x16x32_bf16 v[24:27], v[152:155], v[212:215], v[24:27]
	v_mfma_f32_16x16x32_bf16 v[20:23], v[160:163], v[212:215], v[20:23]
	v_mfma_f32_16x16x32_bf16 v[48:51], v[164:167], v[180:183], v[48:51]
	v_mfma_f32_16x16x32_bf16 v[44:47], v[172:175], v[180:183], v[44:47]
	v_mfma_f32_16x16x32_bf16 v[32:35], v[164:167], v[188:191], v[32:35]
	v_mfma_f32_16x16x32_bf16 v[28:31], v[172:175], v[188:191], v[28:31]
	v_mfma_f32_16x16x32_bf16 v[16:19], v[164:167], v[196:199], v[16:19]
	v_mfma_f32_16x16x32_bf16 v[12:15], v[172:175], v[196:199], v[12:15]
	v_mfma_f32_16x16x32_bf16 v[8:11], v[164:167], v[208:211], v[8:11]
	v_mfma_f32_16x16x32_bf16 v[4:7], v[172:175], v[208:211], v[4:7]
	v_mfma_f32_16x16x32_bf16 v[48:51], v[168:171], v[184:187], v[48:51]
	v_mfma_f32_16x16x32_bf16 v[44:47], v[176:179], v[184:187], v[44:47]
	v_mfma_f32_16x16x32_bf16 v[32:35], v[168:171], v[192:195], v[32:35]
	v_mfma_f32_16x16x32_bf16 v[28:31], v[176:179], v[192:195], v[28:31]
	v_mfma_f32_16x16x32_bf16 v[16:19], v[168:171], v[204:207], v[16:19]
	v_mfma_f32_16x16x32_bf16 v[12:15], v[176:179], v[204:207], v[12:15]
	v_mfma_f32_16x16x32_bf16 v[8:11], v[168:171], v[212:215], v[8:11]
	v_mfma_f32_16x16x32_bf16 v[4:7], v[176:179], v[212:215], v[4:7]
	s_setprio 0
	s_barrier
	s_add_i32 s69, s69, 2
	s_add_u32 s44, s44, 0x100
	s_addc_u32 s45, s45, 0
	s_cmp_gt_u32 s69, 13
.LBB0_1206:
	s_add_u32 s4, s22, s44
	s_addc_u32 s5, s23, s45
	s_add_u32 s98, s4, 0x40080
	s_addc_u32 s99, s5, 0
	s_add_u32 s70, s4, 0x100
	s_addc_u32 s71, s5, 0
	s_add_u32 s48, s65, s44
	s_addc_u32 s49, s68, s45
	s_add_u32 s4, s4, 0x180
	s_addc_u32 s5, s5, 0
	s_add_i32 s72, 0, 0x10000
	s_add_i32 s73, 0, 0x14000
	v_add_u32_e32 v160, s72, v146
	v_add_u32_e32 v176, s73, v146
	ds_read_b128 v[148:151], v160
	ds_read_b128 v[152:155], v160 offset:1024
	ds_read_b128 v[156:159], v160 offset:2048
	ds_read_b128 v[160:163], v160 offset:3072
	ds_read_b128 v[164:167], v176
	ds_read_b128 v[168:171], v176 offset:1024
	ds_read_b128 v[172:175], v176 offset:2048
	ds_read_b128 v[176:179], v176 offset:3072
	s_cmpk_eq_i32 s44, 0x700
	s_cselect_b32 s13, s64, s5
	s_cselect_b32 s12, s63, s4
	s_cselect_b32 s49, s21, s49
	s_cselect_b32 s48, s62, s48
	s_cselect_b32 s5, s37, s71
	s_cselect_b32 s4, s61, s70
	s_add_i32 m0, s17, 0xc000
	ds_read_b128 v[180:183], v147
	ds_read_b128 v[184:187], v147 offset:1024
	ds_read_b128 v[188:191], v147 offset:2048
	ds_read_b128 v[192:195], v147 offset:3072
	ds_read_b128 v[196:199], v147 offset:4096
	ds_read_b128 v[204:207], v147 offset:5120
	ds_read_b128 v[208:211], v147 offset:6144
	ds_read_b128 v[212:215], v147 offset:7168
	global_load_lds_dwordx4 v138, s[98:99]
	s_add_i32 m0, s17, 0xe000
	s_nop 0
	global_load_lds_dwordx4 v140, s[98:99]
	s_waitcnt vmcnt(8)
	s_waitcnt lgkmcnt(0)
	s_barrier
	s_setprio 1
	v_mfma_f32_16x16x32_bf16 v[128:131], v[148:151], v[180:183], v[128:131]
	v_mfma_f32_16x16x32_bf16 v[124:127], v[156:159], v[180:183], v[124:127]
	v_mfma_f32_16x16x32_bf16 v[120:123], v[148:151], v[188:191], v[120:123]
	v_mfma_f32_16x16x32_bf16 v[116:119], v[156:159], v[188:191], v[116:119]
	v_mfma_f32_16x16x32_bf16 v[104:107], v[148:151], v[196:199], v[104:107]
	v_mfma_f32_16x16x32_bf16 v[100:103], v[156:159], v[196:199], v[100:103]
	v_mfma_f32_16x16x32_bf16 v[88:91], v[148:151], v[208:211], v[88:91]
	v_mfma_f32_16x16x32_bf16 v[84:87], v[156:159], v[208:211], v[84:87]
	v_mfma_f32_16x16x32_bf16 v[128:131], v[152:155], v[184:187], v[128:131]
	v_mfma_f32_16x16x32_bf16 v[124:127], v[160:163], v[184:187], v[124:127]
	v_mfma_f32_16x16x32_bf16 v[120:123], v[152:155], v[192:195], v[120:123]
	v_mfma_f32_16x16x32_bf16 v[116:119], v[160:163], v[192:195], v[116:119]
	v_mfma_f32_16x16x32_bf16 v[104:107], v[152:155], v[204:207], v[104:107]
	v_mfma_f32_16x16x32_bf16 v[100:103], v[160:163], v[204:207], v[100:103]
	v_mfma_f32_16x16x32_bf16 v[88:91], v[152:155], v[212:215], v[88:91]
	v_mfma_f32_16x16x32_bf16 v[84:87], v[160:163], v[212:215], v[84:87]
	v_mfma_f32_16x16x32_bf16 v[112:115], v[164:167], v[180:183], v[112:115]
	v_mfma_f32_16x16x32_bf16 v[108:111], v[172:175], v[180:183], v[108:111]
	v_mfma_f32_16x16x32_bf16 v[96:99], v[164:167], v[188:191], v[96:99]
	v_mfma_f32_16x16x32_bf16 v[92:95], v[172:175], v[188:191], v[92:95]
	v_mfma_f32_16x16x32_bf16 v[80:83], v[164:167], v[196:199], v[80:83]
	v_mfma_f32_16x16x32_bf16 v[76:79], v[172:175], v[196:199], v[76:79]
	v_mfma_f32_16x16x32_bf16 v[72:75], v[164:167], v[208:211], v[72:75]
	v_mfma_f32_16x16x32_bf16 v[68:71], v[172:175], v[208:211], v[68:71]
	v_mfma_f32_16x16x32_bf16 v[112:115], v[168:171], v[184:187], v[112:115]
	v_mfma_f32_16x16x32_bf16 v[108:111], v[176:179], v[184:187], v[108:111]
	v_mfma_f32_16x16x32_bf16 v[96:99], v[168:171], v[192:195], v[96:99]
	v_mfma_f32_16x16x32_bf16 v[92:95], v[176:179], v[192:195], v[92:95]
	v_mfma_f32_16x16x32_bf16 v[80:83], v[168:171], v[204:207], v[80:83]
	v_mfma_f32_16x16x32_bf16 v[76:79], v[176:179], v[204:207], v[76:79]
	v_mfma_f32_16x16x32_bf16 v[72:75], v[168:171], v[212:215], v[72:75]
	v_mfma_f32_16x16x32_bf16 v[68:71], v[176:179], v[212:215], v[68:71]
	s_setprio 0
	s_barrier
	s_add_i32 s70, s72, s16
	s_mov_b32 m0, s70
	ds_read_b128 v[180:183], v147 offset:16384
	ds_read_b128 v[184:187], v147 offset:17408
	ds_read_b128 v[188:191], v147 offset:18432
	ds_read_b128 v[192:195], v147 offset:19456
	ds_read_b128 v[196:199], v147 offset:20480
	ds_read_b128 v[204:207], v147 offset:21504
	ds_read_b128 v[208:211], v147 offset:22528
	ds_read_b128 v[212:215], v147 offset:23552
	global_load_lds_dwordx4 v2, s[48:49]
	s_add_i32 m0, s70, 0x2000
	s_add_u32 s70, s48, 0x40000
	s_addc_u32 s71, s49, 0
	s_add_i32 s72, s73, s16
	global_load_lds_dwordx4 v132, s[48:49]
	s_mov_b32 m0, s72
	s_nop 0
	global_load_lds_dwordx4 v2, s[70:71]
	s_add_i32 m0, s72, 0x2000
	s_nop 0
	global_load_lds_dwordx4 v132, s[70:71]
	s_mov_b32 m0, s17
	s_nop 0
	global_load_lds_dwordx4 v136, s[4:5]
	s_mov_b32 m0, s46
	s_nop 0
	global_load_lds_dwordx4 v134, s[4:5]
	s_waitcnt vmcnt(8)
	s_waitcnt lgkmcnt(0)
	s_barrier
	s_setprio 1
	v_mfma_f32_16x16x32_bf16 v[64:67], v[148:151], v[180:183], v[64:67]
	v_mfma_f32_16x16x32_bf16 v[60:63], v[156:159], v[180:183], v[60:63]
	v_mfma_f32_16x16x32_bf16 v[56:59], v[148:151], v[188:191], v[56:59]
	v_mfma_f32_16x16x32_bf16 v[52:55], v[156:159], v[188:191], v[52:55]
	v_mfma_f32_16x16x32_bf16 v[40:43], v[148:151], v[196:199], v[40:43]
	v_mfma_f32_16x16x32_bf16 v[36:39], v[156:159], v[196:199], v[36:39]
	v_mfma_f32_16x16x32_bf16 v[24:27], v[148:151], v[208:211], v[24:27]
	v_mfma_f32_16x16x32_bf16 v[20:23], v[156:159], v[208:211], v[20:23]
	v_mfma_f32_16x16x32_bf16 v[64:67], v[152:155], v[184:187], v[64:67]
	v_mfma_f32_16x16x32_bf16 v[60:63], v[160:163], v[184:187], v[60:63]
	v_mfma_f32_16x16x32_bf16 v[56:59], v[152:155], v[192:195], v[56:59]
	v_mfma_f32_16x16x32_bf16 v[52:55], v[160:163], v[192:195], v[52:55]
	v_mfma_f32_16x16x32_bf16 v[40:43], v[152:155], v[204:207], v[40:43]
	v_mfma_f32_16x16x32_bf16 v[36:39], v[160:163], v[204:207], v[36:39]
	v_mfma_f32_16x16x32_bf16 v[24:27], v[152:155], v[212:215], v[24:27]
	v_mfma_f32_16x16x32_bf16 v[20:23], v[160:163], v[212:215], v[20:23]
	v_mfma_f32_16x16x32_bf16 v[48:51], v[164:167], v[180:183], v[48:51]
	v_mfma_f32_16x16x32_bf16 v[44:47], v[172:175], v[180:183], v[44:47]
	v_mfma_f32_16x16x32_bf16 v[32:35], v[164:167], v[188:191], v[32:35]
	v_mfma_f32_16x16x32_bf16 v[28:31], v[172:175], v[188:191], v[28:31]
	v_mfma_f32_16x16x32_bf16 v[16:19], v[164:167], v[196:199], v[16:19]
	v_mfma_f32_16x16x32_bf16 v[12:15], v[172:175], v[196:199], v[12:15]
	v_mfma_f32_16x16x32_bf16 v[8:11], v[164:167], v[208:211], v[8:11]
	v_mfma_f32_16x16x32_bf16 v[4:7], v[172:175], v[208:211], v[4:7]
	v_mfma_f32_16x16x32_bf16 v[48:51], v[168:171], v[184:187], v[48:51]
	v_mfma_f32_16x16x32_bf16 v[44:47], v[176:179], v[184:187], v[44:47]
	v_mfma_f32_16x16x32_bf16 v[32:35], v[168:171], v[192:195], v[32:35]
	v_mfma_f32_16x16x32_bf16 v[28:31], v[176:179], v[192:195], v[28:31]
	v_mfma_f32_16x16x32_bf16 v[16:19], v[168:171], v[204:207], v[16:19]
	v_mfma_f32_16x16x32_bf16 v[12:15], v[176:179], v[204:207], v[12:15]
	v_mfma_f32_16x16x32_bf16 v[8:11], v[168:171], v[212:215], v[8:11]
	v_mfma_f32_16x16x32_bf16 v[4:7], v[176:179], v[212:215], v[4:7]
	s_setprio 0
	s_barrier
	s_add_i32 s70, 0, 0x18000
	s_add_i32 s71, 0, 0x1c000
	v_add_u32_e32 v160, s70, v146
	v_add_u32_e32 v176, s71, v146
	ds_read_b128 v[148:151], v160
	ds_read_b128 v[152:155], v160 offset:1024
	ds_read_b128 v[156:159], v160 offset:2048
	ds_read_b128 v[160:163], v160 offset:3072
	ds_read_b128 v[164:167], v176
	ds_read_b128 v[168:171], v176 offset:1024
	ds_read_b128 v[172:175], v176 offset:2048
	ds_read_b128 v[176:179], v176 offset:3072
	s_add_u32 s4, s4, 0x40000
	s_addc_u32 s5, s5, 0
	s_mov_b32 m0, s47
	ds_read_b128 v[180:183], v147 offset:32768
	ds_read_b128 v[184:187], v147 offset:33792
	ds_read_b128 v[188:191], v147 offset:34816
	ds_read_b128 v[192:195], v147 offset:35840
	ds_read_b128 v[196:199], v147 offset:36864
	ds_read_b128 v[204:207], v147 offset:37888
	ds_read_b128 v[208:211], v147 offset:38912
	ds_read_b128 v[212:215], v147 offset:39936
	global_load_lds_dwordx4 v136, s[4:5]
	s_mov_b32 m0, s50
	s_nop 0
	global_load_lds_dwordx4 v134, s[4:5]
	s_waitcnt vmcnt(8)
	s_waitcnt lgkmcnt(0)
	s_barrier
	s_setprio 1
	v_mfma_f32_16x16x32_bf16 v[128:131], v[148:151], v[180:183], v[128:131]
	v_mfma_f32_16x16x32_bf16 v[124:127], v[156:159], v[180:183], v[124:127]
	v_mfma_f32_16x16x32_bf16 v[120:123], v[148:151], v[188:191], v[120:123]
	v_mfma_f32_16x16x32_bf16 v[116:119], v[156:159], v[188:191], v[116:119]
	v_mfma_f32_16x16x32_bf16 v[104:107], v[148:151], v[196:199], v[104:107]
	v_mfma_f32_16x16x32_bf16 v[100:103], v[156:159], v[196:199], v[100:103]
	v_mfma_f32_16x16x32_bf16 v[88:91], v[148:151], v[208:211], v[88:91]
	v_mfma_f32_16x16x32_bf16 v[84:87], v[156:159], v[208:211], v[84:87]
	v_mfma_f32_16x16x32_bf16 v[128:131], v[152:155], v[184:187], v[128:131]
	v_mfma_f32_16x16x32_bf16 v[124:127], v[160:163], v[184:187], v[124:127]
	v_mfma_f32_16x16x32_bf16 v[120:123], v[152:155], v[192:195], v[120:123]
	v_mfma_f32_16x16x32_bf16 v[116:119], v[160:163], v[192:195], v[116:119]
	v_mfma_f32_16x16x32_bf16 v[104:107], v[152:155], v[204:207], v[104:107]
	v_mfma_f32_16x16x32_bf16 v[100:103], v[160:163], v[204:207], v[100:103]
	v_mfma_f32_16x16x32_bf16 v[88:91], v[152:155], v[212:215], v[88:91]
	v_mfma_f32_16x16x32_bf16 v[84:87], v[160:163], v[212:215], v[84:87]
	v_mfma_f32_16x16x32_bf16 v[112:115], v[164:167], v[180:183], v[112:115]
	v_mfma_f32_16x16x32_bf16 v[108:111], v[172:175], v[180:183], v[108:111]
	v_mfma_f32_16x16x32_bf16 v[96:99], v[164:167], v[188:191], v[96:99]
	v_mfma_f32_16x16x32_bf16 v[92:95], v[172:175], v[188:191], v[92:95]
	v_mfma_f32_16x16x32_bf16 v[80:83], v[164:167], v[196:199], v[80:83]
	v_mfma_f32_16x16x32_bf16 v[76:79], v[172:175], v[196:199], v[76:79]
	v_mfma_f32_16x16x32_bf16 v[72:75], v[164:167], v[208:211], v[72:75]
	v_mfma_f32_16x16x32_bf16 v[68:71], v[172:175], v[208:211], v[68:71]
	v_mfma_f32_16x16x32_bf16 v[112:115], v[168:171], v[184:187], v[112:115]
	v_mfma_f32_16x16x32_bf16 v[108:111], v[176:179], v[184:187], v[108:111]
	v_mfma_f32_16x16x32_bf16 v[96:99], v[168:171], v[192:195], v[96:99]
	v_mfma_f32_16x16x32_bf16 v[92:95], v[176:179], v[192:195], v[92:95]
	v_mfma_f32_16x16x32_bf16 v[80:83], v[168:171], v[204:207], v[80:83]
	v_mfma_f32_16x16x32_bf16 v[76:79], v[176:179], v[204:207], v[76:79]
	v_mfma_f32_16x16x32_bf16 v[72:75], v[168:171], v[212:215], v[72:75]
	v_mfma_f32_16x16x32_bf16 v[68:71], v[176:179], v[212:215], v[68:71]
	s_setprio 0
	s_barrier
	s_add_i32 s4, s70, s16
	s_add_u32 s98, s48, 0x80
	s_addc_u32 s99, s49, 0
	s_mov_b32 m0, s4
	ds_read_b128 v[180:183], v147 offset:49152
	ds_read_b128 v[184:187], v147 offset:50176
	ds_read_b128 v[188:191], v147 offset:51200
	ds_read_b128 v[192:195], v147 offset:52224
	ds_read_b128 v[196:199], v147 offset:53248
	ds_read_b128 v[204:207], v147 offset:54272
	ds_read_b128 v[208:211], v147 offset:55296
	ds_read_b128 v[212:215], v147 offset:56320
	global_load_lds_dwordx4 v2, s[98:99]
	s_add_i32 m0, s4, 0x2000
	s_add_u32 s4, s48, 0x40080
	s_addc_u32 s5, s49, 0
	s_add_i32 s48, s71, s16
	global_load_lds_dwordx4 v132, s[98:99]
	s_mov_b32 m0, s48
	s_nop 0
	global_load_lds_dwordx4 v2, s[4:5]
	s_add_i32 m0, s48, 0x2000
	s_nop 0
	global_load_lds_dwordx4 v132, s[4:5]
	s_mov_b32 m0, s53
	s_nop 0
	global_load_lds_dwordx4 v136, s[12:13]
	s_mov_b32 m0, s56
	s_nop 0
	global_load_lds_dwordx4 v134, s[12:13]
	s_waitcnt vmcnt(8)
	s_waitcnt lgkmcnt(0)
	s_barrier
	s_setprio 1
	v_mfma_f32_16x16x32_bf16 v[64:67], v[148:151], v[180:183], v[64:67]
	v_mfma_f32_16x16x32_bf16 v[60:63], v[156:159], v[180:183], v[60:63]
	v_mfma_f32_16x16x32_bf16 v[56:59], v[148:151], v[188:191], v[56:59]
	v_mfma_f32_16x16x32_bf16 v[52:55], v[156:159], v[188:191], v[52:55]
	v_mfma_f32_16x16x32_bf16 v[40:43], v[148:151], v[196:199], v[40:43]
	v_mfma_f32_16x16x32_bf16 v[36:39], v[156:159], v[196:199], v[36:39]
	v_mfma_f32_16x16x32_bf16 v[24:27], v[148:151], v[208:211], v[24:27]
	v_mfma_f32_16x16x32_bf16 v[20:23], v[156:159], v[208:211], v[20:23]
	v_mfma_f32_16x16x32_bf16 v[64:67], v[152:155], v[184:187], v[64:67]
	v_mfma_f32_16x16x32_bf16 v[60:63], v[160:163], v[184:187], v[60:63]
	v_mfma_f32_16x16x32_bf16 v[56:59], v[152:155], v[192:195], v[56:59]
	v_mfma_f32_16x16x32_bf16 v[52:55], v[160:163], v[192:195], v[52:55]
	v_mfma_f32_16x16x32_bf16 v[40:43], v[152:155], v[204:207], v[40:43]
	v_mfma_f32_16x16x32_bf16 v[36:39], v[160:163], v[204:207], v[36:39]
	v_mfma_f32_16x16x32_bf16 v[24:27], v[152:155], v[212:215], v[24:27]
	v_mfma_f32_16x16x32_bf16 v[20:23], v[160:163], v[212:215], v[20:23]
	v_mfma_f32_16x16x32_bf16 v[48:51], v[164:167], v[180:183], v[48:51]
	v_mfma_f32_16x16x32_bf16 v[44:47], v[172:175], v[180:183], v[44:47]
	v_mfma_f32_16x16x32_bf16 v[32:35], v[164:167], v[188:191], v[32:35]
	v_mfma_f32_16x16x32_bf16 v[28:31], v[172:175], v[188:191], v[28:31]
	v_mfma_f32_16x16x32_bf16 v[16:19], v[164:167], v[196:199], v[16:19]
	v_mfma_f32_16x16x32_bf16 v[12:15], v[172:175], v[196:199], v[12:15]
	v_mfma_f32_16x16x32_bf16 v[8:11], v[164:167], v[208:211], v[8:11]
	v_mfma_f32_16x16x32_bf16 v[4:7], v[172:175], v[208:211], v[4:7]
	v_mfma_f32_16x16x32_bf16 v[48:51], v[168:171], v[184:187], v[48:51]
	v_mfma_f32_16x16x32_bf16 v[44:47], v[176:179], v[184:187], v[44:47]
	v_mfma_f32_16x16x32_bf16 v[32:35], v[168:171], v[192:195], v[32:35]
	v_mfma_f32_16x16x32_bf16 v[28:31], v[176:179], v[192:195], v[28:31]
	v_mfma_f32_16x16x32_bf16 v[16:19], v[168:171], v[204:207], v[16:19]
	v_mfma_f32_16x16x32_bf16 v[12:15], v[176:179], v[204:207], v[12:15]
	v_mfma_f32_16x16x32_bf16 v[8:11], v[168:171], v[212:215], v[8:11]
	v_mfma_f32_16x16x32_bf16 v[4:7], v[176:179], v[212:215], v[4:7]
	s_setprio 0
	s_barrier
	s_add_i32 s69, s69, 2
	s_add_u32 s44, s44, 0x100
	s_addc_u32 s45, s45, 0
	s_cmp_gt_u32 s69, 13
	s_cbranch_scc0 .LBB0_1206
	s_and_b64 vcc, exec, s[18:19]
	s_mov_b32 s62, 0x18000
	s_mov_b32 s63, 0x1a000
	s_cbranch_vccz .LBB0_1209
	s_barrier

.LBB0_1379:
	s_ashr_i32 s43, s42, 31
	s_lshl_b64 s[4:5], s[42:43], 19
	s_add_u32 s44, s6, s4
	s_addc_u32 s45, s7, s5
	s_and_b64 s[4:5], s[38:39], exec
	s_cselect_b32 s43, s45, s41
	s_cselect_b32 s68, s44, s40
	s_ashr_i32 s37, s36, 31
	s_lshl_b64 s[4:5], s[36:37], 19
	s_add_u32 s48, s8, s4
	s_addc_u32 s49, s9, s5
	s_and_b64 s[4:5], s[38:39], exec
	s_cselect_b32 s37, s49, s51
	s_cselect_b32 s69, s48, s50
	s_add_u32 s70, s68, 0x80
	s_addc_u32 s71, s43, 0
	s_add_u32 s4, s40, 0x40080
	s_addc_u32 s5, s41, 0
	s_add_u32 s72, s50, 0x100
	v_lshl_add_u64 v[144:145], s[4:5], 0, v[140:141]
	v_lshl_add_u64 v[146:147], s[4:5], 0, v[142:143]
	s_addc_u32 s73, s51, 0
	s_mov_b32 s74, -2
	s_mov_b64 s[50:51], 0
	s_waitcnt vmcnt(0)
	s_add_u32 s4, s40, s50
	s_addc_u32 s5, s41, s51
	s_add_u32 s98, s4, 0x40080
	s_addc_u32 s99, s5, 0
	s_add_u32 s75, s4, 0x100
	s_addc_u32 s76, s5, 0
	s_add_u32 s52, s72, s50
	s_addc_u32 s53, s73, s51
	s_add_u32 s4, s4, 0x180
	s_addc_u32 s5, s5, 0
	s_add_i32 s77, 0, 0x10000
	s_add_i32 s78, 0, 0x14000
	v_add_u32_e32 v2, s77, v160
	ds_read_b128 v[148:151], v2
	ds_read_b128 v[152:155], v2 offset:1024
	ds_read_b128 v[156:159], v2 offset:2048
	ds_read_b128 v[162:165], v2 offset:3072
	v_add_u32_e32 v2, s78, v160
	ds_read_b128 v[166:169], v2
	s_waitcnt lgkmcnt(0)
	ds_read_b128 v[170:173], v2 offset:1024
	ds_read_b128 v[174:177], v2 offset:2048
	ds_read_b128 v[178:181], v2 offset:3072
	s_cmpk_eq_i32 s50, 0x700
	s_cselect_b32 s13, s71, s5
	s_cselect_b32 s12, s70, s4
	s_cselect_b32 s53, s37, s53
	s_cselect_b32 s52, s69, s52
	s_cselect_b32 s5, s43, s76
	s_cselect_b32 s4, s68, s75
	s_add_i32 m0, s17, 0xc000
	ds_read_b128 v[182:185], v161
	ds_read_b128 v[186:189], v161 offset:1024
	ds_read_b128 v[190:193], v161 offset:2048
	ds_read_b128 v[194:197], v161 offset:3072
	ds_read_b128 v[204:207], v161 offset:4096
	ds_read_b128 v[208:211], v161 offset:5120
	ds_read_b128 v[212:215], v161 offset:6144
	ds_read_b128 v[216:219], v161 offset:7168
	global_load_lds_dwordx4 v140, s[98:99]
	s_add_i32 m0, s17, 0xe000
	s_nop 0
	global_load_lds_dwordx4 v142, s[98:99]
	s_waitcnt vmcnt(8)
	s_waitcnt lgkmcnt(0)
	s_barrier
	s_setprio 1
	v_mfma_f32_16x16x32_bf16 v[128:131], v[148:151], v[182:185], 0
	v_mfma_f32_16x16x32_bf16 v[124:127], v[156:159], v[182:185], 0
	v_mfma_f32_16x16x32_bf16 v[112:115], v[148:151], v[190:193], 0
	v_mfma_f32_16x16x32_bf16 v[108:111], v[156:159], v[190:193], 0
	v_mfma_f32_16x16x32_bf16 v[96:99], v[148:151], v[204:207], 0
	v_mfma_f32_16x16x32_bf16 v[92:95], v[156:159], v[204:207], 0
	v_mfma_f32_16x16x32_bf16 v[80:83], v[148:151], v[212:215], 0
	v_mfma_f32_16x16x32_bf16 v[76:79], v[156:159], v[212:215], 0
	v_mfma_f32_16x16x32_bf16 v[128:131], v[152:155], v[186:189], v[128:131]
	v_mfma_f32_16x16x32_bf16 v[124:127], v[162:165], v[186:189], v[124:127]
	v_mfma_f32_16x16x32_bf16 v[112:115], v[152:155], v[194:197], v[112:115]
	v_mfma_f32_16x16x32_bf16 v[108:111], v[162:165], v[194:197], v[108:111]
	v_mfma_f32_16x16x32_bf16 v[96:99], v[152:155], v[208:211], v[96:99]
	v_mfma_f32_16x16x32_bf16 v[92:95], v[162:165], v[208:211], v[92:95]
	v_mfma_f32_16x16x32_bf16 v[80:83], v[152:155], v[216:219], v[80:83]
	v_mfma_f32_16x16x32_bf16 v[76:79], v[162:165], v[216:219], v[76:79]
	v_mfma_f32_16x16x32_bf16 v[120:123], v[166:169], v[182:185], 0
	v_mfma_f32_16x16x32_bf16 v[116:119], v[174:177], v[182:185], 0
	v_mfma_f32_16x16x32_bf16 v[104:107], v[166:169], v[190:193], 0
	v_mfma_f32_16x16x32_bf16 v[100:103], v[174:177], v[190:193], 0
	v_mfma_f32_16x16x32_bf16 v[88:91], v[166:169], v[204:207], 0
	v_mfma_f32_16x16x32_bf16 v[84:87], v[174:177], v[204:207], 0
	v_mfma_f32_16x16x32_bf16 v[72:75], v[166:169], v[212:215], 0
	v_mfma_f32_16x16x32_bf16 v[68:71], v[174:177], v[212:215], 0
	v_mfma_f32_16x16x32_bf16 v[120:123], v[170:173], v[186:189], v[120:123]
	v_mfma_f32_16x16x32_bf16 v[116:119], v[178:181], v[186:189], v[116:119]
	v_mfma_f32_16x16x32_bf16 v[104:107], v[170:173], v[194:197], v[104:107]
	v_mfma_f32_16x16x32_bf16 v[100:103], v[178:181], v[194:197], v[100:103]
	v_mfma_f32_16x16x32_bf16 v[88:91], v[170:173], v[208:211], v[88:91]
	v_mfma_f32_16x16x32_bf16 v[84:87], v[178:181], v[208:211], v[84:87]
	v_mfma_f32_16x16x32_bf16 v[72:75], v[170:173], v[216:219], v[72:75]
	v_mfma_f32_16x16x32_bf16 v[68:71], v[178:181], v[216:219], v[68:71]
	s_setprio 0
	s_barrier
	s_add_i32 s75, s77, s16
	s_mov_b32 m0, s75
	ds_read_b128 v[182:185], v161 offset:16384
	ds_read_b128 v[186:189], v161 offset:17408
	ds_read_b128 v[190:193], v161 offset:18432
	ds_read_b128 v[194:197], v161 offset:19456
	ds_read_b128 v[204:207], v161 offset:20480
	ds_read_b128 v[208:211], v161 offset:21504
	ds_read_b128 v[212:215], v161 offset:22528
	ds_read_b128 v[216:219], v161 offset:23552
	global_load_lds_dwordx4 v136, s[52:53]
	s_add_i32 m0, s75, 0x2000
	s_add_u32 s76, s52, 0x40000
	s_addc_u32 s77, s53, 0
	s_add_i32 s75, s78, s16
	global_load_lds_dwordx4 v132, s[52:53]
	s_mov_b32 m0, s75
	s_nop 0
	global_load_lds_dwordx4 v136, s[76:77]
	s_add_i32 m0, s75, 0x2000
	s_nop 0
	global_load_lds_dwordx4 v132, s[76:77]
	s_mov_b32 m0, s17
	s_nop 0
	global_load_lds_dwordx4 v138, s[4:5]
	s_mov_b32 m0, s46
	s_nop 0
	global_load_lds_dwordx4 v134, s[4:5]
	s_waitcnt vmcnt(8)
	s_waitcnt lgkmcnt(0)
	s_barrier
	s_setprio 1
	v_mfma_f32_16x16x32_bf16 v[64:67], v[148:151], v[182:185], 0
	v_mfma_f32_16x16x32_bf16 v[60:63], v[156:159], v[182:185], 0
	v_mfma_f32_16x16x32_bf16 v[48:51], v[148:151], v[190:193], 0
	v_mfma_f32_16x16x32_bf16 v[44:47], v[156:159], v[190:193], 0
	v_mfma_f32_16x16x32_bf16 v[32:35], v[148:151], v[204:207], 0
	v_mfma_f32_16x16x32_bf16 v[28:31], v[156:159], v[204:207], 0
	v_mfma_f32_16x16x32_bf16 v[16:19], v[148:151], v[212:215], 0
	v_mfma_f32_16x16x32_bf16 v[12:15], v[156:159], v[212:215], 0
	v_mfma_f32_16x16x32_bf16 v[64:67], v[152:155], v[186:189], v[64:67]
	v_mfma_f32_16x16x32_bf16 v[60:63], v[162:165], v[186:189], v[60:63]
	v_mfma_f32_16x16x32_bf16 v[48:51], v[152:155], v[194:197], v[48:51]
	v_mfma_f32_16x16x32_bf16 v[44:47], v[162:165], v[194:197], v[44:47]
	v_mfma_f32_16x16x32_bf16 v[32:35], v[152:155], v[208:211], v[32:35]
	v_mfma_f32_16x16x32_bf16 v[28:31], v[162:165], v[208:211], v[28:31]
	v_mfma_f32_16x16x32_bf16 v[16:19], v[152:155], v[216:219], v[16:19]
	v_mfma_f32_16x16x32_bf16 v[12:15], v[162:165], v[216:219], v[12:15]
	v_mfma_f32_16x16x32_bf16 v[56:59], v[166:169], v[182:185], 0
	v_mfma_f32_16x16x32_bf16 v[52:55], v[174:177], v[182:185], 0
	v_mfma_f32_16x16x32_bf16 v[40:43], v[166:169], v[190:193], 0
	v_mfma_f32_16x16x32_bf16 v[36:39], v[174:177], v[190:193], 0
	v_mfma_f32_16x16x32_bf16 v[24:27], v[166:169], v[204:207], 0
	v_mfma_f32_16x16x32_bf16 v[20:23], v[174:177], v[204:207], 0
	v_mfma_f32_16x16x32_bf16 v[8:11], v[166:169], v[212:215], 0
	v_mfma_f32_16x16x32_bf16 v[4:7], v[174:177], v[212:215], 0
	v_mfma_f32_16x16x32_bf16 v[56:59], v[170:173], v[186:189], v[56:59]
	v_mfma_f32_16x16x32_bf16 v[52:55], v[178:181], v[186:189], v[52:55]
	v_mfma_f32_16x16x32_bf16 v[40:43], v[170:173], v[194:197], v[40:43]
	v_mfma_f32_16x16x32_bf16 v[36:39], v[178:181], v[194:197], v[36:39]
	v_mfma_f32_16x16x32_bf16 v[24:27], v[170:173], v[208:211], v[24:27]
	v_mfma_f32_16x16x32_bf16 v[20:23], v[178:181], v[208:211], v[20:23]
	v_mfma_f32_16x16x32_bf16 v[8:11], v[170:173], v[216:219], v[8:11]
	v_mfma_f32_16x16x32_bf16 v[4:7], v[178:181], v[216:219], v[4:7]
	s_setprio 0
	s_barrier
	s_add_i32 s75, 0, 0x18000
	v_add_u32_e32 v2, s75, v160
	s_add_i32 s76, 0, 0x1c000
	ds_read_b128 v[148:151], v2
	ds_read_b128 v[152:155], v2 offset:1024
	ds_read_b128 v[156:159], v2 offset:2048
	ds_read_b128 v[162:165], v2 offset:3072
	v_add_u32_e32 v2, s76, v160
	ds_read_b128 v[166:169], v2
	ds_read_b128 v[170:173], v2 offset:1024
	ds_read_b128 v[174:177], v2 offset:2048
	ds_read_b128 v[178:181], v2 offset:3072
	s_add_u32 s4, s4, 0x40000
	s_addc_u32 s5, s5, 0
	s_mov_b32 m0, s47
	ds_read_b128 v[182:185], v161 offset:32768
	ds_read_b128 v[186:189], v161 offset:33792
	ds_read_b128 v[190:193], v161 offset:34816
	ds_read_b128 v[194:197], v161 offset:35840
	ds_read_b128 v[204:207], v161 offset:36864
	ds_read_b128 v[208:211], v161 offset:37888
	ds_read_b128 v[212:215], v161 offset:38912
	ds_read_b128 v[216:219], v161 offset:39936
	global_load_lds_dwordx4 v138, s[4:5]
	s_mov_b32 m0, s56
	s_nop 0
	global_load_lds_dwordx4 v134, s[4:5]
	s_waitcnt vmcnt(8)
	s_waitcnt lgkmcnt(0)
	s_barrier
	s_setprio 1
	v_mfma_f32_16x16x32_bf16 v[128:131], v[148:151], v[182:185], v[128:131]
	v_mfma_f32_16x16x32_bf16 v[124:127], v[156:159], v[182:185], v[124:127]
	v_mfma_f32_16x16x32_bf16 v[112:115], v[148:151], v[190:193], v[112:115]
	v_mfma_f32_16x16x32_bf16 v[108:111], v[156:159], v[190:193], v[108:111]
	v_mfma_f32_16x16x32_bf16 v[96:99], v[148:151], v[204:207], v[96:99]
	v_mfma_f32_16x16x32_bf16 v[92:95], v[156:159], v[204:207], v[92:95]
	v_mfma_f32_16x16x32_bf16 v[80:83], v[148:151], v[212:215], v[80:83]
	v_mfma_f32_16x16x32_bf16 v[76:79], v[156:159], v[212:215], v[76:79]
	v_mfma_f32_16x16x32_bf16 v[128:131], v[152:155], v[186:189], v[128:131]
	v_mfma_f32_16x16x32_bf16 v[124:127], v[162:165], v[186:189], v[124:127]
	v_mfma_f32_16x16x32_bf16 v[112:115], v[152:155], v[194:197], v[112:115]
	v_mfma_f32_16x16x32_bf16 v[108:111], v[162:165], v[194:197], v[108:111]
	v_mfma_f32_16x16x32_bf16 v[96:99], v[152:155], v[208:211], v[96:99]
	v_mfma_f32_16x16x32_bf16 v[92:95], v[162:165], v[208:211], v[92:95]
	v_mfma_f32_16x16x32_bf16 v[80:83], v[152:155], v[216:219], v[80:83]
	v_mfma_f32_16x16x32_bf16 v[76:79], v[162:165], v[216:219], v[76:79]
	v_mfma_f32_16x16x32_bf16 v[120:123], v[166:169], v[182:185], v[120:123]
	v_mfma_f32_16x16x32_bf16 v[116:119], v[174:177], v[182:185], v[116:119]
	v_mfma_f32_16x16x32_bf16 v[104:107], v[166:169], v[190:193], v[104:107]
	v_mfma_f32_16x16x32_bf16 v[100:103], v[174:177], v[190:193], v[100:103]
	v_mfma_f32_16x16x32_bf16 v[88:91], v[166:169], v[204:207], v[88:91]
	v_mfma_f32_16x16x32_bf16 v[84:87], v[174:177], v[204:207], v[84:87]
	v_mfma_f32_16x16x32_bf16 v[72:75], v[166:169], v[212:215], v[72:75]
	v_mfma_f32_16x16x32_bf16 v[68:71], v[174:177], v[212:215], v[68:71]
	v_mfma_f32_16x16x32_bf16 v[120:123], v[170:173], v[186:189], v[120:123]
	v_mfma_f32_16x16x32_bf16 v[116:119], v[178:181], v[186:189], v[116:119]
	v_mfma_f32_16x16x32_bf16 v[104:107], v[170:173], v[194:197], v[104:107]
	v_mfma_f32_16x16x32_bf16 v[100:103], v[178:181], v[194:197], v[100:103]
	v_mfma_f32_16x16x32_bf16 v[88:91], v[170:173], v[208:211], v[88:91]
	v_mfma_f32_16x16x32_bf16 v[84:87], v[178:181], v[208:211], v[84:87]
	v_mfma_f32_16x16x32_bf16 v[72:75], v[170:173], v[216:219], v[72:75]
	v_mfma_f32_16x16x32_bf16 v[68:71], v[178:181], v[216:219], v[68:71]
	s_setprio 0
	s_barrier
	s_add_i32 s4, s75, s16
	s_add_u32 s98, s52, 0x80
	s_addc_u32 s99, s53, 0
	s_mov_b32 m0, s4
	ds_read_b128 v[182:185], v161 offset:49152
	ds_read_b128 v[186:189], v161 offset:50176
	ds_read_b128 v[190:193], v161 offset:51200
	ds_read_b128 v[194:197], v161 offset:52224
	ds_read_b128 v[204:207], v161 offset:53248
	ds_read_b128 v[208:211], v161 offset:54272
	ds_read_b128 v[212:215], v161 offset:55296
	ds_read_b128 v[216:219], v161 offset:56320
	global_load_lds_dwordx4 v136, s[98:99]
	s_add_i32 m0, s4, 0x2000
	s_add_u32 s4, s52, 0x40080
	s_addc_u32 s5, s53, 0
	s_add_i32 s52, s76, s16
	global_load_lds_dwordx4 v132, s[98:99]
	s_mov_b32 m0, s52
	s_nop 0
	global_load_lds_dwordx4 v136, s[4:5]
	s_add_i32 m0, s52, 0x2000
	s_nop 0
	global_load_lds_dwordx4 v132, s[4:5]
	s_mov_b32 m0, s61
	s_nop 0
	global_load_lds_dwordx4 v138, s[12:13]
	s_mov_b32 m0, s62
	s_nop 0
	global_load_lds_dwordx4 v134, s[12:13]
	s_waitcnt vmcnt(8)
	s_waitcnt lgkmcnt(0)
	s_barrier
	s_setprio 1
	v_mfma_f32_16x16x32_bf16 v[64:67], v[148:151], v[182:185], v[64:67]
	v_mfma_f32_16x16x32_bf16 v[60:63], v[156:159], v[182:185], v[60:63]
	v_mfma_f32_16x16x32_bf16 v[48:51], v[148:151], v[190:193], v[48:51]
	v_mfma_f32_16x16x32_bf16 v[44:47], v[156:159], v[190:193], v[44:47]
	v_mfma_f32_16x16x32_bf16 v[32:35], v[148:151], v[204:207], v[32:35]
	v_mfma_f32_16x16x32_bf16 v[28:31], v[156:159], v[204:207], v[28:31]
	v_mfma_f32_16x16x32_bf16 v[16:19], v[148:151], v[212:215], v[16:19]
	v_mfma_f32_16x16x32_bf16 v[12:15], v[156:159], v[212:215], v[12:15]
	v_mfma_f32_16x16x32_bf16 v[64:67], v[152:155], v[186:189], v[64:67]
	v_mfma_f32_16x16x32_bf16 v[60:63], v[162:165], v[186:189], v[60:63]
	v_mfma_f32_16x16x32_bf16 v[48:51], v[152:155], v[194:197], v[48:51]
	v_mfma_f32_16x16x32_bf16 v[44:47], v[162:165], v[194:197], v[44:47]
	v_mfma_f32_16x16x32_bf16 v[32:35], v[152:155], v[208:211], v[32:35]
	v_mfma_f32_16x16x32_bf16 v[28:31], v[162:165], v[208:211], v[28:31]
	v_mfma_f32_16x16x32_bf16 v[16:19], v[152:155], v[216:219], v[16:19]
	v_mfma_f32_16x16x32_bf16 v[12:15], v[162:165], v[216:219], v[12:15]
	v_mfma_f32_16x16x32_bf16 v[56:59], v[166:169], v[182:185], v[56:59]
	v_mfma_f32_16x16x32_bf16 v[52:55], v[174:177], v[182:185], v[52:55]
	v_mfma_f32_16x16x32_bf16 v[40:43], v[166:169], v[190:193], v[40:43]
	v_mfma_f32_16x16x32_bf16 v[36:39], v[174:177], v[190:193], v[36:39]
	v_mfma_f32_16x16x32_bf16 v[24:27], v[166:169], v[204:207], v[24:27]
	v_mfma_f32_16x16x32_bf16 v[20:23], v[174:177], v[204:207], v[20:23]
	v_mfma_f32_16x16x32_bf16 v[8:11], v[166:169], v[212:215], v[8:11]
	v_mfma_f32_16x16x32_bf16 v[4:7], v[174:177], v[212:215], v[4:7]
	v_mfma_f32_16x16x32_bf16 v[56:59], v[170:173], v[186:189], v[56:59]
	v_mfma_f32_16x16x32_bf16 v[52:55], v[178:181], v[186:189], v[52:55]
	v_mfma_f32_16x16x32_bf16 v[40:43], v[170:173], v[194:197], v[40:43]
	v_mfma_f32_16x16x32_bf16 v[36:39], v[178:181], v[194:197], v[36:39]
	v_mfma_f32_16x16x32_bf16 v[24:27], v[170:173], v[208:211], v[24:27]
	v_mfma_f32_16x16x32_bf16 v[20:23], v[178:181], v[208:211], v[20:23]
	v_mfma_f32_16x16x32_bf16 v[8:11], v[170:173], v[216:219], v[8:11]
	v_mfma_f32_16x16x32_bf16 v[4:7], v[178:181], v[216:219], v[4:7]
	s_setprio 0
	s_barrier
	s_add_i32 s74, s74, 2
	s_add_u32 s50, s50, 0x100
	s_addc_u32 s51, s51, 0
	s_cmp_gt_u32 s74, 13
.LBB0_1380:
	s_add_u32 s4, s40, s50
	s_addc_u32 s5, s41, s51
	s_add_u32 s98, s4, 0x40080
	s_addc_u32 s99, s5, 0
	s_add_u32 s75, s4, 0x100
	s_addc_u32 s76, s5, 0
	s_add_u32 s52, s72, s50
	s_addc_u32 s53, s73, s51
	s_add_u32 s4, s4, 0x180
	s_addc_u32 s5, s5, 0
	s_add_i32 s77, 0, 0x10000
	s_add_i32 s78, 0, 0x14000
	v_add_u32_e32 v2, s77, v160
	ds_read_b128 v[148:151], v2
	ds_read_b128 v[152:155], v2 offset:1024
	ds_read_b128 v[156:159], v2 offset:2048
	ds_read_b128 v[162:165], v2 offset:3072
	v_add_u32_e32 v2, s78, v160
	ds_read_b128 v[166:169], v2
	s_waitcnt lgkmcnt(0)
	ds_read_b128 v[170:173], v2 offset:1024
	ds_read_b128 v[174:177], v2 offset:2048
	ds_read_b128 v[178:181], v2 offset:3072
	s_cmpk_eq_i32 s50, 0x700
	s_cselect_b32 s13, s71, s5
	s_cselect_b32 s12, s70, s4
	s_cselect_b32 s53, s37, s53
	s_cselect_b32 s52, s69, s52
	s_cselect_b32 s5, s43, s76
	s_cselect_b32 s4, s68, s75
	s_add_i32 m0, s17, 0xc000
	ds_read_b128 v[182:185], v161
	ds_read_b128 v[186:189], v161 offset:1024
	ds_read_b128 v[190:193], v161 offset:2048
	ds_read_b128 v[194:197], v161 offset:3072
	ds_read_b128 v[204:207], v161 offset:4096
	ds_read_b128 v[208:211], v161 offset:5120
	ds_read_b128 v[212:215], v161 offset:6144
	ds_read_b128 v[216:219], v161 offset:7168
	global_load_lds_dwordx4 v140, s[98:99]
	s_add_i32 m0, s17, 0xe000
	s_nop 0
	global_load_lds_dwordx4 v142, s[98:99]
	s_waitcnt vmcnt(8)
	s_waitcnt lgkmcnt(0)
	s_barrier
	s_setprio 1
	v_mfma_f32_16x16x32_bf16 v[128:131], v[148:151], v[182:185], v[128:131]
	v_mfma_f32_16x16x32_bf16 v[124:127], v[156:159], v[182:185], v[124:127]
	v_mfma_f32_16x16x32_bf16 v[112:115], v[148:151], v[190:193], v[112:115]
	v_mfma_f32_16x16x32_bf16 v[108:111], v[156:159], v[190:193], v[108:111]
	v_mfma_f32_16x16x32_bf16 v[96:99], v[148:151], v[204:207], v[96:99]
	v_mfma_f32_16x16x32_bf16 v[92:95], v[156:159], v[204:207], v[92:95]
	v_mfma_f32_16x16x32_bf16 v[80:83], v[148:151], v[212:215], v[80:83]
	v_mfma_f32_16x16x32_bf16 v[76:79], v[156:159], v[212:215], v[76:79]
	v_mfma_f32_16x16x32_bf16 v[128:131], v[152:155], v[186:189], v[128:131]
	v_mfma_f32_16x16x32_bf16 v[124:127], v[162:165], v[186:189], v[124:127]
	v_mfma_f32_16x16x32_bf16 v[112:115], v[152:155], v[194:197], v[112:115]
	v_mfma_f32_16x16x32_bf16 v[108:111], v[162:165], v[194:197], v[108:111]
	v_mfma_f32_16x16x32_bf16 v[96:99], v[152:155], v[208:211], v[96:99]
	v_mfma_f32_16x16x32_bf16 v[92:95], v[162:165], v[208:211], v[92:95]
	v_mfma_f32_16x16x32_bf16 v[80:83], v[152:155], v[216:219], v[80:83]
	v_mfma_f32_16x16x32_bf16 v[76:79], v[162:165], v[216:219], v[76:79]
	v_mfma_f32_16x16x32_bf16 v[120:123], v[166:169], v[182:185], v[120:123]
	v_mfma_f32_16x16x32_bf16 v[116:119], v[174:177], v[182:185], v[116:119]
	v_mfma_f32_16x16x32_bf16 v[104:107], v[166:169], v[190:193], v[104:107]
	v_mfma_f32_16x16x32_bf16 v[100:103], v[174:177], v[190:193], v[100:103]
	v_mfma_f32_16x16x32_bf16 v[88:91], v[166:169], v[204:207], v[88:91]
	v_mfma_f32_16x16x32_bf16 v[84:87], v[174:177], v[204:207], v[84:87]
	v_mfma_f32_16x16x32_bf16 v[72:75], v[166:169], v[212:215], v[72:75]
	v_mfma_f32_16x16x32_bf16 v[68:71], v[174:177], v[212:215], v[68:71]
	v_mfma_f32_16x16x32_bf16 v[120:123], v[170:173], v[186:189], v[120:123]
	v_mfma_f32_16x16x32_bf16 v[116:119], v[178:181], v[186:189], v[116:119]
	v_mfma_f32_16x16x32_bf16 v[104:107], v[170:173], v[194:197], v[104:107]
	v_mfma_f32_16x16x32_bf16 v[100:103], v[178:181], v[194:197], v[100:103]
	v_mfma_f32_16x16x32_bf16 v[88:91], v[170:173], v[208:211], v[88:91]
	v_mfma_f32_16x16x32_bf16 v[84:87], v[178:181], v[208:211], v[84:87]
	v_mfma_f32_16x16x32_bf16 v[72:75], v[170:173], v[216:219], v[72:75]
	v_mfma_f32_16x16x32_bf16 v[68:71], v[178:181], v[216:219], v[68:71]
	s_setprio 0
	s_barrier
	s_add_i32 s75, s77, s16
	s_mov_b32 m0, s75
	ds_read_b128 v[182:185], v161 offset:16384
	ds_read_b128 v[186:189], v161 offset:17408
	ds_read_b128 v[190:193], v161 offset:18432
	ds_read_b128 v[194:197], v161 offset:19456
	ds_read_b128 v[204:207], v161 offset:20480
	ds_read_b128 v[208:211], v161 offset:21504
	ds_read_b128 v[212:215], v161 offset:22528
	ds_read_b128 v[216:219], v161 offset:23552
	global_load_lds_dwordx4 v136, s[52:53]
	s_add_i32 m0, s75, 0x2000
	s_add_u32 s76, s52, 0x40000
	s_addc_u32 s77, s53, 0
	s_add_i32 s75, s78, s16
	global_load_lds_dwordx4 v132, s[52:53]
	s_mov_b32 m0, s75
	s_nop 0
	global_load_lds_dwordx4 v136, s[76:77]
	s_add_i32 m0, s75, 0x2000
	s_nop 0
	global_load_lds_dwordx4 v132, s[76:77]
	s_mov_b32 m0, s17
	s_nop 0
	global_load_lds_dwordx4 v138, s[4:5]
	s_mov_b32 m0, s46
	s_nop 0
	global_load_lds_dwordx4 v134, s[4:5]
	s_waitcnt vmcnt(8)
	s_waitcnt lgkmcnt(0)
	s_barrier
	s_setprio 1
	v_mfma_f32_16x16x32_bf16 v[64:67], v[148:151], v[182:185], v[64:67]
	v_mfma_f32_16x16x32_bf16 v[60:63], v[156:159], v[182:185], v[60:63]
	v_mfma_f32_16x16x32_bf16 v[48:51], v[148:151], v[190:193], v[48:51]
	v_mfma_f32_16x16x32_bf16 v[44:47], v[156:159], v[190:193], v[44:47]
	v_mfma_f32_16x16x32_bf16 v[32:35], v[148:151], v[204:207], v[32:35]
	v_mfma_f32_16x16x32_bf16 v[28:31], v[156:159], v[204:207], v[28:31]
	v_mfma_f32_16x16x32_bf16 v[16:19], v[148:151], v[212:215], v[16:19]
	v_mfma_f32_16x16x32_bf16 v[12:15], v[156:159], v[212:215], v[12:15]
	v_mfma_f32_16x16x32_bf16 v[64:67], v[152:155], v[186:189], v[64:67]
	v_mfma_f32_16x16x32_bf16 v[60:63], v[162:165], v[186:189], v[60:63]
	v_mfma_f32_16x16x32_bf16 v[48:51], v[152:155], v[194:197], v[48:51]
	v_mfma_f32_16x16x32_bf16 v[44:47], v[162:165], v[194:197], v[44:47]
	v_mfma_f32_16x16x32_bf16 v[32:35], v[152:155], v[208:211], v[32:35]
	v_mfma_f32_16x16x32_bf16 v[28:31], v[162:165], v[208:211], v[28:31]
	v_mfma_f32_16x16x32_bf16 v[16:19], v[152:155], v[216:219], v[16:19]
	v_mfma_f32_16x16x32_bf16 v[12:15], v[162:165], v[216:219], v[12:15]
	v_mfma_f32_16x16x32_bf16 v[56:59], v[166:169], v[182:185], v[56:59]
	v_mfma_f32_16x16x32_bf16 v[52:55], v[174:177], v[182:185], v[52:55]
	v_mfma_f32_16x16x32_bf16 v[40:43], v[166:169], v[190:193], v[40:43]
	v_mfma_f32_16x16x32_bf16 v[36:39], v[174:177], v[190:193], v[36:39]
	v_mfma_f32_16x16x32_bf16 v[24:27], v[166:169], v[204:207], v[24:27]
	v_mfma_f32_16x16x32_bf16 v[20:23], v[174:177], v[204:207], v[20:23]
	v_mfma_f32_16x16x32_bf16 v[8:11], v[166:169], v[212:215], v[8:11]
	v_mfma_f32_16x16x32_bf16 v[4:7], v[174:177], v[212:215], v[4:7]
	v_mfma_f32_16x16x32_bf16 v[56:59], v[170:173], v[186:189], v[56:59]
	v_mfma_f32_16x16x32_bf16 v[52:55], v[178:181], v[186:189], v[52:55]
	v_mfma_f32_16x16x32_bf16 v[40:43], v[170:173], v[194:197], v[40:43]
	v_mfma_f32_16x16x32_bf16 v[36:39], v[178:181], v[194:197], v[36:39]
	v_mfma_f32_16x16x32_bf16 v[24:27], v[170:173], v[208:211], v[24:27]
	v_mfma_f32_16x16x32_bf16 v[20:23], v[178:181], v[208:211], v[20:23]
	v_mfma_f32_16x16x32_bf16 v[8:11], v[170:173], v[216:219], v[8:11]
	v_mfma_f32_16x16x32_bf16 v[4:7], v[178:181], v[216:219], v[4:7]
	s_setprio 0
	s_barrier
	s_add_i32 s75, 0, 0x18000
	v_add_u32_e32 v2, s75, v160
	s_add_i32 s76, 0, 0x1c000
	ds_read_b128 v[148:151], v2
	ds_read_b128 v[152:155], v2 offset:1024
	ds_read_b128 v[156:159], v2 offset:2048
	ds_read_b128 v[162:165], v2 offset:3072
	v_add_u32_e32 v2, s76, v160
	ds_read_b128 v[166:169], v2
	ds_read_b128 v[170:173], v2 offset:1024
	ds_read_b128 v[174:177], v2 offset:2048
	ds_read_b128 v[178:181], v2 offset:3072
	s_add_u32 s4, s4, 0x40000
	s_addc_u32 s5, s5, 0
	s_mov_b32 m0, s47
	ds_read_b128 v[182:185], v161 offset:32768
	ds_read_b128 v[186:189], v161 offset:33792
	ds_read_b128 v[190:193], v161 offset:34816
	ds_read_b128 v[194:197], v161 offset:35840
	ds_read_b128 v[204:207], v161 offset:36864
	ds_read_b128 v[208:211], v161 offset:37888
	ds_read_b128 v[212:215], v161 offset:38912
	ds_read_b128 v[216:219], v161 offset:39936
	global_load_lds_dwordx4 v138, s[4:5]
	s_mov_b32 m0, s56
	s_nop 0
	global_load_lds_dwordx4 v134, s[4:5]
	s_waitcnt vmcnt(8)
	s_waitcnt lgkmcnt(0)
	s_barrier
	s_setprio 1
	v_mfma_f32_16x16x32_bf16 v[128:131], v[148:151], v[182:185], v[128:131]
	v_mfma_f32_16x16x32_bf16 v[124:127], v[156:159], v[182:185], v[124:127]
	v_mfma_f32_16x16x32_bf16 v[112:115], v[148:151], v[190:193], v[112:115]
	v_mfma_f32_16x16x32_bf16 v[108:111], v[156:159], v[190:193], v[108:111]
	v_mfma_f32_16x16x32_bf16 v[96:99], v[148:151], v[204:207], v[96:99]
	v_mfma_f32_16x16x32_bf16 v[92:95], v[156:159], v[204:207], v[92:95]
	v_mfma_f32_16x16x32_bf16 v[80:83], v[148:151], v[212:215], v[80:83]
	v_mfma_f32_16x16x32_bf16 v[76:79], v[156:159], v[212:215], v[76:79]
	v_mfma_f32_16x16x32_bf16 v[128:131], v[152:155], v[186:189], v[128:131]
	v_mfma_f32_16x16x32_bf16 v[124:127], v[162:165], v[186:189], v[124:127]
	v_mfma_f32_16x16x32_bf16 v[112:115], v[152:155], v[194:197], v[112:115]
	v_mfma_f32_16x16x32_bf16 v[108:111], v[162:165], v[194:197], v[108:111]
	v_mfma_f32_16x16x32_bf16 v[96:99], v[152:155], v[208:211], v[96:99]
	v_mfma_f32_16x16x32_bf16 v[92:95], v[162:165], v[208:211], v[92:95]
	v_mfma_f32_16x16x32_bf16 v[80:83], v[152:155], v[216:219], v[80:83]
	v_mfma_f32_16x16x32_bf16 v[76:79], v[162:165], v[216:219], v[76:79]
	v_mfma_f32_16x16x32_bf16 v[120:123], v[166:169], v[182:185], v[120:123]
	v_mfma_f32_16x16x32_bf16 v[116:119], v[174:177], v[182:185], v[116:119]
	v_mfma_f32_16x16x32_bf16 v[104:107], v[166:169], v[190:193], v[104:107]
	v_mfma_f32_16x16x32_bf16 v[100:103], v[174:177], v[190:193], v[100:103]
	v_mfma_f32_16x16x32_bf16 v[88:91], v[166:169], v[204:207], v[88:91]
	v_mfma_f32_16x16x32_bf16 v[84:87], v[174:177], v[204:207], v[84:87]
	v_mfma_f32_16x16x32_bf16 v[72:75], v[166:169], v[212:215], v[72:75]
	v_mfma_f32_16x16x32_bf16 v[68:71], v[174:177], v[212:215], v[68:71]
	v_mfma_f32_16x16x32_bf16 v[120:123], v[170:173], v[186:189], v[120:123]
	v_mfma_f32_16x16x32_bf16 v[116:119], v[178:181], v[186:189], v[116:119]
	v_mfma_f32_16x16x32_bf16 v[104:107], v[170:173], v[194:197], v[104:107]
	v_mfma_f32_16x16x32_bf16 v[100:103], v[178:181], v[194:197], v[100:103]
	v_mfma_f32_16x16x32_bf16 v[88:91], v[170:173], v[208:211], v[88:91]
	v_mfma_f32_16x16x32_bf16 v[84:87], v[178:181], v[208:211], v[84:87]
	v_mfma_f32_16x16x32_bf16 v[72:75], v[170:173], v[216:219], v[72:75]
	v_mfma_f32_16x16x32_bf16 v[68:71], v[178:181], v[216:219], v[68:71]
	s_setprio 0
	s_barrier
	s_add_i32 s4, s75, s16
	s_add_u32 s98, s52, 0x80
	s_addc_u32 s99, s53, 0
	s_mov_b32 m0, s4
	ds_read_b128 v[182:185], v161 offset:49152
	ds_read_b128 v[186:189], v161 offset:50176
	ds_read_b128 v[190:193], v161 offset:51200
	ds_read_b128 v[194:197], v161 offset:52224
	ds_read_b128 v[204:207], v161 offset:53248
	ds_read_b128 v[208:211], v161 offset:54272
	ds_read_b128 v[212:215], v161 offset:55296
	ds_read_b128 v[216:219], v161 offset:56320
	global_load_lds_dwordx4 v136, s[98:99]
	s_add_i32 m0, s4, 0x2000
	s_add_u32 s4, s52, 0x40080
	s_addc_u32 s5, s53, 0
	s_add_i32 s52, s76, s16
	global_load_lds_dwordx4 v132, s[98:99]
	s_mov_b32 m0, s52
	s_nop 0
	global_load_lds_dwordx4 v136, s[4:5]
	s_add_i32 m0, s52, 0x2000
	s_nop 0
	global_load_lds_dwordx4 v132, s[4:5]
	s_mov_b32 m0, s61
	s_nop 0
	global_load_lds_dwordx4 v138, s[12:13]
	s_mov_b32 m0, s62
	s_nop 0
	global_load_lds_dwordx4 v134, s[12:13]
	s_waitcnt vmcnt(8)
	s_waitcnt lgkmcnt(0)
	s_barrier
	s_setprio 1
	v_mfma_f32_16x16x32_bf16 v[64:67], v[148:151], v[182:185], v[64:67]
	v_mfma_f32_16x16x32_bf16 v[60:63], v[156:159], v[182:185], v[60:63]
	v_mfma_f32_16x16x32_bf16 v[48:51], v[148:151], v[190:193], v[48:51]
	v_mfma_f32_16x16x32_bf16 v[44:47], v[156:159], v[190:193], v[44:47]
	v_mfma_f32_16x16x32_bf16 v[32:35], v[148:151], v[204:207], v[32:35]
	v_mfma_f32_16x16x32_bf16 v[28:31], v[156:159], v[204:207], v[28:31]
	v_mfma_f32_16x16x32_bf16 v[16:19], v[148:151], v[212:215], v[16:19]
	v_mfma_f32_16x16x32_bf16 v[12:15], v[156:159], v[212:215], v[12:15]
	v_mfma_f32_16x16x32_bf16 v[64:67], v[152:155], v[186:189], v[64:67]
	v_mfma_f32_16x16x32_bf16 v[60:63], v[162:165], v[186:189], v[60:63]
	v_mfma_f32_16x16x32_bf16 v[48:51], v[152:155], v[194:197], v[48:51]
	v_mfma_f32_16x16x32_bf16 v[44:47], v[162:165], v[194:197], v[44:47]
	v_mfma_f32_16x16x32_bf16 v[32:35], v[152:155], v[208:211], v[32:35]
	v_mfma_f32_16x16x32_bf16 v[28:31], v[162:165], v[208:211], v[28:31]
	v_mfma_f32_16x16x32_bf16 v[16:19], v[152:155], v[216:219], v[16:19]
	v_mfma_f32_16x16x32_bf16 v[12:15], v[162:165], v[216:219], v[12:15]
	v_mfma_f32_16x16x32_bf16 v[56:59], v[166:169], v[182:185], v[56:59]
	v_mfma_f32_16x16x32_bf16 v[52:55], v[174:177], v[182:185], v[52:55]
	v_mfma_f32_16x16x32_bf16 v[40:43], v[166:169], v[190:193], v[40:43]
	v_mfma_f32_16x16x32_bf16 v[36:39], v[174:177], v[190:193], v[36:39]
	v_mfma_f32_16x16x32_bf16 v[24:27], v[166:169], v[204:207], v[24:27]
	v_mfma_f32_16x16x32_bf16 v[20:23], v[174:177], v[204:207], v[20:23]
	v_mfma_f32_16x16x32_bf16 v[8:11], v[166:169], v[212:215], v[8:11]
	v_mfma_f32_16x16x32_bf16 v[4:7], v[174:177], v[212:215], v[4:7]
	v_mfma_f32_16x16x32_bf16 v[56:59], v[170:173], v[186:189], v[56:59]
	v_mfma_f32_16x16x32_bf16 v[52:55], v[178:181], v[186:189], v[52:55]
	v_mfma_f32_16x16x32_bf16 v[40:43], v[170:173], v[194:197], v[40:43]
	v_mfma_f32_16x16x32_bf16 v[36:39], v[178:181], v[194:197], v[36:39]
	v_mfma_f32_16x16x32_bf16 v[24:27], v[170:173], v[208:211], v[24:27]
	v_mfma_f32_16x16x32_bf16 v[20:23], v[178:181], v[208:211], v[20:23]
	v_mfma_f32_16x16x32_bf16 v[8:11], v[170:173], v[216:219], v[8:11]
	v_mfma_f32_16x16x32_bf16 v[4:7], v[178:181], v[216:219], v[4:7]
	s_setprio 0
	s_barrier
	s_add_i32 s74, s74, 2
	s_add_u32 s50, s50, 0x100
	s_addc_u32 s51, s51, 0
	s_cmp_gt_u32 s74, 13
	s_cbranch_scc0 .LBB0_1380
	s_and_b64 vcc, exec, s[22:23]
	s_cbranch_vccz .LBB0_1383
	s_barrier

.LBB0_1458:
	s_ashr_i32 s41, s40, 31
	s_lshl_b64 s[4:5], s[40:41], 21
	s_add_u32 s42, s6, s4
	s_addc_u32 s43, s7, s5
	s_and_b64 s[4:5], s[38:39], exec
	s_cselect_b32 s41, s43, s49
	s_cselect_b32 s68, s42, s48
	s_ashr_i32 s37, s36, 31
	s_lshl_b64 s[4:5], s[36:37], 21
	s_add_u32 s44, s8, s4
	s_addc_u32 s45, s9, s5
	s_and_b64 s[4:5], s[38:39], exec
	s_cselect_b32 s37, s45, s51
	s_cselect_b32 s69, s44, s50
	s_add_u32 s70, s68, 0x80
	s_addc_u32 s71, s41, 0
	s_add_u32 s72, s50, 0x100
	s_addc_u32 s73, s51, 0
	s_add_u32 s4, s48, 0x100080
	s_addc_u32 s5, s49, 0
	v_lshl_add_u64 v[112:113], s[4:5], 0, v[210:211]
	v_lshl_add_u64 v[114:115], s[4:5], 0, v[212:213]
	s_mov_b32 s74, -2
	s_mov_b64 s[50:51], 0
	s_waitcnt lgkmcnt(0)
	s_waitcnt vmcnt(0)
	s_add_u32 s4, s48, s50
	s_addc_u32 s5, s49, s51
	s_add_u32 s98, s4, 0x100080
	s_addc_u32 s99, s5, 0
	s_add_u32 s75, s4, 0x100
	s_addc_u32 s76, s5, 0
	s_add_u32 s52, s72, s50
	s_addc_u32 s53, s73, s51
	s_add_u32 s4, s4, 0x180
	s_addc_u32 s5, s5, 0
	s_add_i32 s77, 0, 0x10000
	s_add_i32 s78, 0, 0x14000
	v_add_u32_e32 v148, s77, v203
	v_add_u32_e32 v164, s78, v203
	ds_read_b128 v[120:123], v148
	ds_read_b128 v[132:135], v148 offset:1024
	ds_read_b128 v[144:147], v148 offset:2048
	ds_read_b128 v[148:151], v148 offset:3072
	ds_read_b128 v[152:155], v164
	ds_read_b128 v[156:159], v164 offset:1024
	ds_read_b128 v[160:163], v164 offset:2048
	ds_read_b128 v[164:167], v164 offset:3072
	s_cmpk_eq_i32 s50, 0x1f00
	s_cselect_b32 s13, s71, s5
	s_cselect_b32 s12, s70, s4
	s_cselect_b32 s53, s37, s53
	s_cselect_b32 s52, s69, s52
	s_cselect_b32 s5, s41, s76
	s_cselect_b32 s4, s68, s75
	s_add_i32 m0, s17, 0xc000
	ds_read_b128 v[168:171], v233
	ds_read_b128 v[172:175], v233 offset:1024
	ds_read_b128 v[176:179], v233 offset:2048
	ds_read_b128 v[180:183], v233 offset:3072
	ds_read_b128 v[184:187], v233 offset:4096
	ds_read_b128 v[188:191], v233 offset:5120
	ds_read_b128 v[192:195], v233 offset:6144
	ds_read_b128 v[196:199], v233 offset:7168
	global_load_lds_dwordx4 v210, s[98:99]
	s_add_i32 m0, s17, 0xe000
	s_nop 0
	global_load_lds_dwordx4 v212, s[98:99]
	s_waitcnt vmcnt(8)
	s_waitcnt lgkmcnt(0)
	s_barrier
	s_setprio 1
	v_mfma_f32_16x16x32_bf16 v[140:143], v[120:123], v[168:171], 0
	v_mfma_f32_16x16x32_bf16 v[136:139], v[144:147], v[168:171], 0
	v_mfma_f32_16x16x32_bf16 v[116:119], v[120:123], v[176:179], 0
	v_mfma_f32_16x16x32_bf16 v[108:111], v[144:147], v[176:179], 0
	v_mfma_f32_16x16x32_bf16 v[96:99], v[120:123], v[184:187], 0
	v_mfma_f32_16x16x32_bf16 v[92:95], v[144:147], v[184:187], 0
	v_mfma_f32_16x16x32_bf16 v[80:83], v[120:123], v[192:195], 0
	v_mfma_f32_16x16x32_bf16 v[76:79], v[144:147], v[192:195], 0
	v_mfma_f32_16x16x32_bf16 v[140:143], v[132:135], v[172:175], v[140:143]
	v_mfma_f32_16x16x32_bf16 v[136:139], v[148:151], v[172:175], v[136:139]
	v_mfma_f32_16x16x32_bf16 v[116:119], v[132:135], v[180:183], v[116:119]
	v_mfma_f32_16x16x32_bf16 v[108:111], v[148:151], v[180:183], v[108:111]
	v_mfma_f32_16x16x32_bf16 v[96:99], v[132:135], v[188:191], v[96:99]
	v_mfma_f32_16x16x32_bf16 v[92:95], v[148:151], v[188:191], v[92:95]
	v_mfma_f32_16x16x32_bf16 v[80:83], v[132:135], v[196:199], v[80:83]
	v_mfma_f32_16x16x32_bf16 v[76:79], v[148:151], v[196:199], v[76:79]
	v_mfma_f32_16x16x32_bf16 v[128:131], v[152:155], v[168:171], 0
	v_mfma_f32_16x16x32_bf16 v[124:127], v[160:163], v[168:171], 0
	v_mfma_f32_16x16x32_bf16 v[104:107], v[152:155], v[176:179], 0
	v_mfma_f32_16x16x32_bf16 v[100:103], v[160:163], v[176:179], 0
	v_mfma_f32_16x16x32_bf16 v[88:91], v[152:155], v[184:187], 0
	v_mfma_f32_16x16x32_bf16 v[84:87], v[160:163], v[184:187], 0
	v_mfma_f32_16x16x32_bf16 v[72:75], v[152:155], v[192:195], 0
	v_mfma_f32_16x16x32_bf16 v[68:71], v[160:163], v[192:195], 0
	v_mfma_f32_16x16x32_bf16 v[128:131], v[156:159], v[172:175], v[128:131]
	v_mfma_f32_16x16x32_bf16 v[124:127], v[164:167], v[172:175], v[124:127]
	v_mfma_f32_16x16x32_bf16 v[104:107], v[156:159], v[180:183], v[104:107]
	v_mfma_f32_16x16x32_bf16 v[100:103], v[164:167], v[180:183], v[100:103]
	v_mfma_f32_16x16x32_bf16 v[88:91], v[156:159], v[188:191], v[88:91]
	v_mfma_f32_16x16x32_bf16 v[84:87], v[164:167], v[188:191], v[84:87]
	v_mfma_f32_16x16x32_bf16 v[72:75], v[156:159], v[196:199], v[72:75]
	v_mfma_f32_16x16x32_bf16 v[68:71], v[164:167], v[196:199], v[68:71]
	s_setprio 0
	s_barrier
	s_add_i32 s75, s77, s16
	s_mov_b32 m0, s75
	ds_read_b128 v[168:171], v233 offset:16384
	ds_read_b128 v[172:175], v233 offset:17408
	ds_read_b128 v[176:179], v233 offset:18432
	ds_read_b128 v[180:183], v233 offset:19456
	ds_read_b128 v[184:187], v233 offset:20480
	ds_read_b128 v[188:191], v233 offset:21504
	ds_read_b128 v[192:195], v233 offset:22528
	ds_read_b128 v[196:199], v233 offset:23552
	global_load_lds_dwordx4 v2, s[52:53]
	s_add_i32 m0, s75, 0x2000
	s_add_u32 s76, s52, 0x100000
	s_addc_u32 s77, s53, 0
	s_add_i32 s75, s78, s16
	global_load_lds_dwordx4 v204, s[52:53]
	s_mov_b32 m0, s75
	s_nop 0
	global_load_lds_dwordx4 v2, s[76:77]
	s_add_i32 m0, s75, 0x2000
	s_nop 0
	global_load_lds_dwordx4 v204, s[76:77]
	s_mov_b32 m0, s17
	s_nop 0
	global_load_lds_dwordx4 v208, s[4:5]
	s_mov_b32 m0, s46
	s_nop 0
	global_load_lds_dwordx4 v206, s[4:5]
	s_waitcnt vmcnt(8)
	s_waitcnt lgkmcnt(0)
	s_barrier
	s_setprio 1
	v_mfma_f32_16x16x32_bf16 v[64:67], v[120:123], v[168:171], 0
	v_mfma_f32_16x16x32_bf16 v[60:63], v[144:147], v[168:171], 0
	v_mfma_f32_16x16x32_bf16 v[48:51], v[120:123], v[176:179], 0
	v_mfma_f32_16x16x32_bf16 v[44:47], v[144:147], v[176:179], 0
	v_mfma_f32_16x16x32_bf16 v[32:35], v[120:123], v[184:187], 0
	v_mfma_f32_16x16x32_bf16 v[28:31], v[144:147], v[184:187], 0
	v_mfma_f32_16x16x32_bf16 v[16:19], v[120:123], v[192:195], 0
	v_mfma_f32_16x16x32_bf16 v[12:15], v[144:147], v[192:195], 0
	v_mfma_f32_16x16x32_bf16 v[64:67], v[132:135], v[172:175], v[64:67]
	v_mfma_f32_16x16x32_bf16 v[60:63], v[148:151], v[172:175], v[60:63]
	v_mfma_f32_16x16x32_bf16 v[48:51], v[132:135], v[180:183], v[48:51]
	v_mfma_f32_16x16x32_bf16 v[44:47], v[148:151], v[180:183], v[44:47]
	v_mfma_f32_16x16x32_bf16 v[32:35], v[132:135], v[188:191], v[32:35]
	v_mfma_f32_16x16x32_bf16 v[28:31], v[148:151], v[188:191], v[28:31]
	v_mfma_f32_16x16x32_bf16 v[16:19], v[132:135], v[196:199], v[16:19]
	v_mfma_f32_16x16x32_bf16 v[12:15], v[148:151], v[196:199], v[12:15]
	v_mfma_f32_16x16x32_bf16 v[56:59], v[152:155], v[168:171], 0
	v_mfma_f32_16x16x32_bf16 v[52:55], v[160:163], v[168:171], 0
	v_mfma_f32_16x16x32_bf16 v[40:43], v[152:155], v[176:179], 0
	v_mfma_f32_16x16x32_bf16 v[36:39], v[160:163], v[176:179], 0
	v_mfma_f32_16x16x32_bf16 v[24:27], v[152:155], v[184:187], 0
	v_mfma_f32_16x16x32_bf16 v[20:23], v[160:163], v[184:187], 0
	v_mfma_f32_16x16x32_bf16 v[8:11], v[152:155], v[192:195], 0
	v_mfma_f32_16x16x32_bf16 v[4:7], v[160:163], v[192:195], 0
	v_mfma_f32_16x16x32_bf16 v[56:59], v[156:159], v[172:175], v[56:59]
	v_mfma_f32_16x16x32_bf16 v[52:55], v[164:167], v[172:175], v[52:55]
	v_mfma_f32_16x16x32_bf16 v[40:43], v[156:159], v[180:183], v[40:43]
	v_mfma_f32_16x16x32_bf16 v[36:39], v[164:167], v[180:183], v[36:39]
	v_mfma_f32_16x16x32_bf16 v[24:27], v[156:159], v[188:191], v[24:27]
	v_mfma_f32_16x16x32_bf16 v[20:23], v[164:167], v[188:191], v[20:23]
	v_mfma_f32_16x16x32_bf16 v[8:11], v[156:159], v[196:199], v[8:11]
	v_mfma_f32_16x16x32_bf16 v[4:7], v[164:167], v[196:199], v[4:7]
	s_setprio 0
	s_barrier
	s_add_i32 s75, 0, 0x18000
	s_add_i32 s76, 0, 0x1c000
	v_add_u32_e32 v148, s75, v203
	v_add_u32_e32 v164, s76, v203
	ds_read_b128 v[120:123], v148
	ds_read_b128 v[132:135], v148 offset:1024
	ds_read_b128 v[144:147], v148 offset:2048
	ds_read_b128 v[148:151], v148 offset:3072
	ds_read_b128 v[152:155], v164
	ds_read_b128 v[156:159], v164 offset:1024
	ds_read_b128 v[160:163], v164 offset:2048
	ds_read_b128 v[164:167], v164 offset:3072
	s_add_u32 s4, s4, 0x100000
	s_addc_u32 s5, s5, 0
	s_mov_b32 m0, s47
	ds_read_b128 v[168:171], v233 offset:32768
	ds_read_b128 v[172:175], v233 offset:33792
	ds_read_b128 v[176:179], v233 offset:34816
	ds_read_b128 v[180:183], v233 offset:35840
	ds_read_b128 v[184:187], v233 offset:36864
	ds_read_b128 v[188:191], v233 offset:37888
	ds_read_b128 v[192:195], v233 offset:38912
	ds_read_b128 v[196:199], v233 offset:39936
	global_load_lds_dwordx4 v208, s[4:5]
	s_mov_b32 m0, s58
	s_nop 0
	global_load_lds_dwordx4 v206, s[4:5]
	s_waitcnt vmcnt(8)
	s_waitcnt lgkmcnt(0)
	s_barrier
	s_setprio 1
	v_mfma_f32_16x16x32_bf16 v[140:143], v[120:123], v[168:171], v[140:143]
	v_mfma_f32_16x16x32_bf16 v[136:139], v[144:147], v[168:171], v[136:139]
	v_mfma_f32_16x16x32_bf16 v[116:119], v[120:123], v[176:179], v[116:119]
	v_mfma_f32_16x16x32_bf16 v[108:111], v[144:147], v[176:179], v[108:111]
	v_mfma_f32_16x16x32_bf16 v[96:99], v[120:123], v[184:187], v[96:99]
	v_mfma_f32_16x16x32_bf16 v[92:95], v[144:147], v[184:187], v[92:95]
	v_mfma_f32_16x16x32_bf16 v[80:83], v[120:123], v[192:195], v[80:83]
	v_mfma_f32_16x16x32_bf16 v[76:79], v[144:147], v[192:195], v[76:79]
	v_mfma_f32_16x16x32_bf16 v[140:143], v[132:135], v[172:175], v[140:143]
	v_mfma_f32_16x16x32_bf16 v[136:139], v[148:151], v[172:175], v[136:139]
	v_mfma_f32_16x16x32_bf16 v[116:119], v[132:135], v[180:183], v[116:119]
	v_mfma_f32_16x16x32_bf16 v[108:111], v[148:151], v[180:183], v[108:111]
	v_mfma_f32_16x16x32_bf16 v[96:99], v[132:135], v[188:191], v[96:99]
	v_mfma_f32_16x16x32_bf16 v[92:95], v[148:151], v[188:191], v[92:95]
	v_mfma_f32_16x16x32_bf16 v[80:83], v[132:135], v[196:199], v[80:83]
	v_mfma_f32_16x16x32_bf16 v[76:79], v[148:151], v[196:199], v[76:79]
	v_mfma_f32_16x16x32_bf16 v[128:131], v[152:155], v[168:171], v[128:131]
	v_mfma_f32_16x16x32_bf16 v[124:127], v[160:163], v[168:171], v[124:127]
	v_mfma_f32_16x16x32_bf16 v[104:107], v[152:155], v[176:179], v[104:107]
	v_mfma_f32_16x16x32_bf16 v[100:103], v[160:163], v[176:179], v[100:103]
	v_mfma_f32_16x16x32_bf16 v[88:91], v[152:155], v[184:187], v[88:91]
	v_mfma_f32_16x16x32_bf16 v[84:87], v[160:163], v[184:187], v[84:87]
	v_mfma_f32_16x16x32_bf16 v[72:75], v[152:155], v[192:195], v[72:75]
	v_mfma_f32_16x16x32_bf16 v[68:71], v[160:163], v[192:195], v[68:71]
	v_mfma_f32_16x16x32_bf16 v[128:131], v[156:159], v[172:175], v[128:131]
	v_mfma_f32_16x16x32_bf16 v[124:127], v[164:167], v[172:175], v[124:127]
	v_mfma_f32_16x16x32_bf16 v[104:107], v[156:159], v[180:183], v[104:107]
	v_mfma_f32_16x16x32_bf16 v[100:103], v[164:167], v[180:183], v[100:103]
	v_mfma_f32_16x16x32_bf16 v[88:91], v[156:159], v[188:191], v[88:91]
	v_mfma_f32_16x16x32_bf16 v[84:87], v[164:167], v[188:191], v[84:87]
	v_mfma_f32_16x16x32_bf16 v[72:75], v[156:159], v[196:199], v[72:75]
	v_mfma_f32_16x16x32_bf16 v[68:71], v[164:167], v[196:199], v[68:71]
	s_setprio 0
	s_barrier
	s_add_i32 s4, s75, s16
	s_add_u32 s98, s52, 0x80
	s_addc_u32 s99, s53, 0
	s_mov_b32 m0, s4
	ds_read_b128 v[168:171], v233 offset:49152
	ds_read_b128 v[172:175], v233 offset:50176
	ds_read_b128 v[176:179], v233 offset:51200
	ds_read_b128 v[180:183], v233 offset:52224
	ds_read_b128 v[184:187], v233 offset:53248
	ds_read_b128 v[188:191], v233 offset:54272
	ds_read_b128 v[192:195], v233 offset:55296
	ds_read_b128 v[196:199], v233 offset:56320
	global_load_lds_dwordx4 v2, s[98:99]
	s_add_i32 m0, s4, 0x2000
	s_add_u32 s4, s52, 0x100080
	s_addc_u32 s5, s53, 0
	s_add_i32 s52, s76, s16
	global_load_lds_dwordx4 v204, s[98:99]
	s_mov_b32 m0, s52
	s_nop 0
	global_load_lds_dwordx4 v2, s[4:5]
	s_add_i32 m0, s52, 0x2000
	s_nop 0
	global_load_lds_dwordx4 v204, s[4:5]
	s_mov_b32 m0, s62
	s_nop 0
	global_load_lds_dwordx4 v208, s[12:13]
	s_mov_b32 m0, s63
	s_nop 0
	global_load_lds_dwordx4 v206, s[12:13]
	s_waitcnt vmcnt(8)
	s_waitcnt lgkmcnt(0)
	s_barrier
	s_setprio 1
	v_mfma_f32_16x16x32_bf16 v[64:67], v[120:123], v[168:171], v[64:67]
	v_mfma_f32_16x16x32_bf16 v[60:63], v[144:147], v[168:171], v[60:63]
	v_mfma_f32_16x16x32_bf16 v[48:51], v[120:123], v[176:179], v[48:51]
	v_mfma_f32_16x16x32_bf16 v[44:47], v[144:147], v[176:179], v[44:47]
	v_mfma_f32_16x16x32_bf16 v[32:35], v[120:123], v[184:187], v[32:35]
	v_mfma_f32_16x16x32_bf16 v[28:31], v[144:147], v[184:187], v[28:31]
	v_mfma_f32_16x16x32_bf16 v[16:19], v[120:123], v[192:195], v[16:19]
	v_mfma_f32_16x16x32_bf16 v[12:15], v[144:147], v[192:195], v[12:15]
	v_mfma_f32_16x16x32_bf16 v[64:67], v[132:135], v[172:175], v[64:67]
	v_mfma_f32_16x16x32_bf16 v[60:63], v[148:151], v[172:175], v[60:63]
	v_mfma_f32_16x16x32_bf16 v[48:51], v[132:135], v[180:183], v[48:51]
	v_mfma_f32_16x16x32_bf16 v[44:47], v[148:151], v[180:183], v[44:47]
	v_mfma_f32_16x16x32_bf16 v[32:35], v[132:135], v[188:191], v[32:35]
	v_mfma_f32_16x16x32_bf16 v[28:31], v[148:151], v[188:191], v[28:31]
	v_mfma_f32_16x16x32_bf16 v[16:19], v[132:135], v[196:199], v[16:19]
	v_mfma_f32_16x16x32_bf16 v[12:15], v[148:151], v[196:199], v[12:15]
	v_mfma_f32_16x16x32_bf16 v[56:59], v[152:155], v[168:171], v[56:59]
	v_mfma_f32_16x16x32_bf16 v[52:55], v[160:163], v[168:171], v[52:55]
	v_mfma_f32_16x16x32_bf16 v[40:43], v[152:155], v[176:179], v[40:43]
	v_mfma_f32_16x16x32_bf16 v[36:39], v[160:163], v[176:179], v[36:39]
	v_mfma_f32_16x16x32_bf16 v[24:27], v[152:155], v[184:187], v[24:27]
	v_mfma_f32_16x16x32_bf16 v[20:23], v[160:163], v[184:187], v[20:23]
	v_mfma_f32_16x16x32_bf16 v[8:11], v[152:155], v[192:195], v[8:11]
	v_mfma_f32_16x16x32_bf16 v[4:7], v[160:163], v[192:195], v[4:7]
	v_mfma_f32_16x16x32_bf16 v[56:59], v[156:159], v[172:175], v[56:59]
	v_mfma_f32_16x16x32_bf16 v[52:55], v[164:167], v[172:175], v[52:55]
	v_mfma_f32_16x16x32_bf16 v[40:43], v[156:159], v[180:183], v[40:43]
	v_mfma_f32_16x16x32_bf16 v[36:39], v[164:167], v[180:183], v[36:39]
	v_mfma_f32_16x16x32_bf16 v[24:27], v[156:159], v[188:191], v[24:27]
	v_mfma_f32_16x16x32_bf16 v[20:23], v[164:167], v[188:191], v[20:23]
	v_mfma_f32_16x16x32_bf16 v[8:11], v[156:159], v[196:199], v[8:11]
	v_mfma_f32_16x16x32_bf16 v[4:7], v[164:167], v[196:199], v[4:7]
	s_setprio 0
	s_barrier
	s_add_i32 s74, s74, 2
	s_add_u32 s50, s50, 0x100
	s_addc_u32 s51, s51, 0
	s_cmp_gt_u32 s74, 61
.LBB0_1459:
	s_add_u32 s4, s48, s50
	s_addc_u32 s5, s49, s51
	s_add_u32 s98, s4, 0x100080
	s_addc_u32 s99, s5, 0
	s_add_u32 s75, s4, 0x100
	s_addc_u32 s76, s5, 0
	s_add_u32 s52, s72, s50
	s_addc_u32 s53, s73, s51
	s_add_u32 s4, s4, 0x180
	s_addc_u32 s5, s5, 0
	s_add_i32 s77, 0, 0x10000
	s_add_i32 s78, 0, 0x14000
	v_add_u32_e32 v148, s77, v203
	v_add_u32_e32 v164, s78, v203
	ds_read_b128 v[120:123], v148
	ds_read_b128 v[132:135], v148 offset:1024
	ds_read_b128 v[144:147], v148 offset:2048
	ds_read_b128 v[148:151], v148 offset:3072
	ds_read_b128 v[152:155], v164
	ds_read_b128 v[156:159], v164 offset:1024
	ds_read_b128 v[160:163], v164 offset:2048
	ds_read_b128 v[164:167], v164 offset:3072
	s_cmpk_eq_i32 s50, 0x1f00
	s_cselect_b32 s13, s71, s5
	s_cselect_b32 s12, s70, s4
	s_cselect_b32 s53, s37, s53
	s_cselect_b32 s52, s69, s52
	s_cselect_b32 s5, s41, s76
	s_cselect_b32 s4, s68, s75
	s_add_i32 m0, s17, 0xc000
	ds_read_b128 v[168:171], v233
	ds_read_b128 v[172:175], v233 offset:1024
	ds_read_b128 v[176:179], v233 offset:2048
	ds_read_b128 v[180:183], v233 offset:3072
	ds_read_b128 v[184:187], v233 offset:4096
	ds_read_b128 v[188:191], v233 offset:5120
	ds_read_b128 v[192:195], v233 offset:6144
	ds_read_b128 v[196:199], v233 offset:7168
	global_load_lds_dwordx4 v210, s[98:99]
	s_add_i32 m0, s17, 0xe000
	s_nop 0
	global_load_lds_dwordx4 v212, s[98:99]
	s_waitcnt vmcnt(8)
	s_waitcnt lgkmcnt(0)
	s_barrier
	s_setprio 1
	v_mfma_f32_16x16x32_bf16 v[140:143], v[120:123], v[168:171], v[140:143]
	v_mfma_f32_16x16x32_bf16 v[136:139], v[144:147], v[168:171], v[136:139]
	v_mfma_f32_16x16x32_bf16 v[116:119], v[120:123], v[176:179], v[116:119]
	v_mfma_f32_16x16x32_bf16 v[108:111], v[144:147], v[176:179], v[108:111]
	v_mfma_f32_16x16x32_bf16 v[96:99], v[120:123], v[184:187], v[96:99]
	v_mfma_f32_16x16x32_bf16 v[92:95], v[144:147], v[184:187], v[92:95]
	v_mfma_f32_16x16x32_bf16 v[80:83], v[120:123], v[192:195], v[80:83]
	v_mfma_f32_16x16x32_bf16 v[76:79], v[144:147], v[192:195], v[76:79]
	v_mfma_f32_16x16x32_bf16 v[140:143], v[132:135], v[172:175], v[140:143]
	v_mfma_f32_16x16x32_bf16 v[136:139], v[148:151], v[172:175], v[136:139]
	v_mfma_f32_16x16x32_bf16 v[116:119], v[132:135], v[180:183], v[116:119]
	v_mfma_f32_16x16x32_bf16 v[108:111], v[148:151], v[180:183], v[108:111]
	v_mfma_f32_16x16x32_bf16 v[96:99], v[132:135], v[188:191], v[96:99]
	v_mfma_f32_16x16x32_bf16 v[92:95], v[148:151], v[188:191], v[92:95]
	v_mfma_f32_16x16x32_bf16 v[80:83], v[132:135], v[196:199], v[80:83]
	v_mfma_f32_16x16x32_bf16 v[76:79], v[148:151], v[196:199], v[76:79]
	v_mfma_f32_16x16x32_bf16 v[128:131], v[152:155], v[168:171], v[128:131]
	v_mfma_f32_16x16x32_bf16 v[124:127], v[160:163], v[168:171], v[124:127]
	v_mfma_f32_16x16x32_bf16 v[104:107], v[152:155], v[176:179], v[104:107]
	v_mfma_f32_16x16x32_bf16 v[100:103], v[160:163], v[176:179], v[100:103]
	v_mfma_f32_16x16x32_bf16 v[88:91], v[152:155], v[184:187], v[88:91]
	v_mfma_f32_16x16x32_bf16 v[84:87], v[160:163], v[184:187], v[84:87]
	v_mfma_f32_16x16x32_bf16 v[72:75], v[152:155], v[192:195], v[72:75]
	v_mfma_f32_16x16x32_bf16 v[68:71], v[160:163], v[192:195], v[68:71]
	v_mfma_f32_16x16x32_bf16 v[128:131], v[156:159], v[172:175], v[128:131]
	v_mfma_f32_16x16x32_bf16 v[124:127], v[164:167], v[172:175], v[124:127]
	v_mfma_f32_16x16x32_bf16 v[104:107], v[156:159], v[180:183], v[104:107]
	v_mfma_f32_16x16x32_bf16 v[100:103], v[164:167], v[180:183], v[100:103]
	v_mfma_f32_16x16x32_bf16 v[88:91], v[156:159], v[188:191], v[88:91]
	v_mfma_f32_16x16x32_bf16 v[84:87], v[164:167], v[188:191], v[84:87]
	v_mfma_f32_16x16x32_bf16 v[72:75], v[156:159], v[196:199], v[72:75]
	v_mfma_f32_16x16x32_bf16 v[68:71], v[164:167], v[196:199], v[68:71]
	s_setprio 0
	s_barrier
	s_add_i32 s75, s77, s16
	s_mov_b32 m0, s75
	ds_read_b128 v[168:171], v233 offset:16384
	ds_read_b128 v[172:175], v233 offset:17408
	ds_read_b128 v[176:179], v233 offset:18432
	ds_read_b128 v[180:183], v233 offset:19456
	ds_read_b128 v[184:187], v233 offset:20480
	ds_read_b128 v[188:191], v233 offset:21504
	ds_read_b128 v[192:195], v233 offset:22528
	ds_read_b128 v[196:199], v233 offset:23552
	global_load_lds_dwordx4 v2, s[52:53]
	s_add_i32 m0, s75, 0x2000
	s_add_u32 s76, s52, 0x100000
	s_addc_u32 s77, s53, 0
	s_add_i32 s75, s78, s16
	global_load_lds_dwordx4 v204, s[52:53]
	s_mov_b32 m0, s75
	s_nop 0
	global_load_lds_dwordx4 v2, s[76:77]
	s_add_i32 m0, s75, 0x2000
	s_nop 0
	global_load_lds_dwordx4 v204, s[76:77]
	s_mov_b32 m0, s17
	s_nop 0
	global_load_lds_dwordx4 v208, s[4:5]
	s_mov_b32 m0, s46
	s_nop 0
	global_load_lds_dwordx4 v206, s[4:5]
	s_waitcnt vmcnt(8)
	s_waitcnt lgkmcnt(0)
	s_barrier
	s_setprio 1
	v_mfma_f32_16x16x32_bf16 v[64:67], v[120:123], v[168:171], v[64:67]
	v_mfma_f32_16x16x32_bf16 v[60:63], v[144:147], v[168:171], v[60:63]
	v_mfma_f32_16x16x32_bf16 v[48:51], v[120:123], v[176:179], v[48:51]
	v_mfma_f32_16x16x32_bf16 v[44:47], v[144:147], v[176:179], v[44:47]
	v_mfma_f32_16x16x32_bf16 v[32:35], v[120:123], v[184:187], v[32:35]
	v_mfma_f32_16x16x32_bf16 v[28:31], v[144:147], v[184:187], v[28:31]
	v_mfma_f32_16x16x32_bf16 v[16:19], v[120:123], v[192:195], v[16:19]
	v_mfma_f32_16x16x32_bf16 v[12:15], v[144:147], v[192:195], v[12:15]
	v_mfma_f32_16x16x32_bf16 v[64:67], v[132:135], v[172:175], v[64:67]
	v_mfma_f32_16x16x32_bf16 v[60:63], v[148:151], v[172:175], v[60:63]
	v_mfma_f32_16x16x32_bf16 v[48:51], v[132:135], v[180:183], v[48:51]
	v_mfma_f32_16x16x32_bf16 v[44:47], v[148:151], v[180:183], v[44:47]
	v_mfma_f32_16x16x32_bf16 v[32:35], v[132:135], v[188:191], v[32:35]
	v_mfma_f32_16x16x32_bf16 v[28:31], v[148:151], v[188:191], v[28:31]
	v_mfma_f32_16x16x32_bf16 v[16:19], v[132:135], v[196:199], v[16:19]
	v_mfma_f32_16x16x32_bf16 v[12:15], v[148:151], v[196:199], v[12:15]
	v_mfma_f32_16x16x32_bf16 v[56:59], v[152:155], v[168:171], v[56:59]
	v_mfma_f32_16x16x32_bf16 v[52:55], v[160:163], v[168:171], v[52:55]
	v_mfma_f32_16x16x32_bf16 v[40:43], v[152:155], v[176:179], v[40:43]
	v_mfma_f32_16x16x32_bf16 v[36:39], v[160:163], v[176:179], v[36:39]
	v_mfma_f32_16x16x32_bf16 v[24:27], v[152:155], v[184:187], v[24:27]
	v_mfma_f32_16x16x32_bf16 v[20:23], v[160:163], v[184:187], v[20:23]
	v_mfma_f32_16x16x32_bf16 v[8:11], v[152:155], v[192:195], v[8:11]
	v_mfma_f32_16x16x32_bf16 v[4:7], v[160:163], v[192:195], v[4:7]
	v_mfma_f32_16x16x32_bf16 v[56:59], v[156:159], v[172:175], v[56:59]
	v_mfma_f32_16x16x32_bf16 v[52:55], v[164:167], v[172:175], v[52:55]
	v_mfma_f32_16x16x32_bf16 v[40:43], v[156:159], v[180:183], v[40:43]
	v_mfma_f32_16x16x32_bf16 v[36:39], v[164:167], v[180:183], v[36:39]
	v_mfma_f32_16x16x32_bf16 v[24:27], v[156:159], v[188:191], v[24:27]
	v_mfma_f32_16x16x32_bf16 v[20:23], v[164:167], v[188:191], v[20:23]
	v_mfma_f32_16x16x32_bf16 v[8:11], v[156:159], v[196:199], v[8:11]
	v_mfma_f32_16x16x32_bf16 v[4:7], v[164:167], v[196:199], v[4:7]
	s_setprio 0
	s_barrier
	s_add_i32 s75, 0, 0x18000
	s_add_i32 s76, 0, 0x1c000
	v_add_u32_e32 v148, s75, v203
	v_add_u32_e32 v164, s76, v203
	ds_read_b128 v[120:123], v148
	ds_read_b128 v[132:135], v148 offset:1024
	ds_read_b128 v[144:147], v148 offset:2048
	ds_read_b128 v[148:151], v148 offset:3072
	ds_read_b128 v[152:155], v164
	ds_read_b128 v[156:159], v164 offset:1024
	ds_read_b128 v[160:163], v164 offset:2048
	ds_read_b128 v[164:167], v164 offset:3072
	s_add_u32 s4, s4, 0x100000
	s_addc_u32 s5, s5, 0
	s_mov_b32 m0, s47
	ds_read_b128 v[168:171], v233 offset:32768
	ds_read_b128 v[172:175], v233 offset:33792
	ds_read_b128 v[176:179], v233 offset:34816
	ds_read_b128 v[180:183], v233 offset:35840
	ds_read_b128 v[184:187], v233 offset:36864
	ds_read_b128 v[188:191], v233 offset:37888
	ds_read_b128 v[192:195], v233 offset:38912
	ds_read_b128 v[196:199], v233 offset:39936
	global_load_lds_dwordx4 v208, s[4:5]
	s_mov_b32 m0, s58
	s_nop 0
	global_load_lds_dwordx4 v206, s[4:5]
	s_waitcnt vmcnt(8)
	s_waitcnt lgkmcnt(0)
	s_barrier
	s_setprio 1
	v_mfma_f32_16x16x32_bf16 v[140:143], v[120:123], v[168:171], v[140:143]
	v_mfma_f32_16x16x32_bf16 v[136:139], v[144:147], v[168:171], v[136:139]
	v_mfma_f32_16x16x32_bf16 v[116:119], v[120:123], v[176:179], v[116:119]
	v_mfma_f32_16x16x32_bf16 v[108:111], v[144:147], v[176:179], v[108:111]
	v_mfma_f32_16x16x32_bf16 v[96:99], v[120:123], v[184:187], v[96:99]
	v_mfma_f32_16x16x32_bf16 v[92:95], v[144:147], v[184:187], v[92:95]
	v_mfma_f32_16x16x32_bf16 v[80:83], v[120:123], v[192:195], v[80:83]
	v_mfma_f32_16x16x32_bf16 v[76:79], v[144:147], v[192:195], v[76:79]
	v_mfma_f32_16x16x32_bf16 v[140:143], v[132:135], v[172:175], v[140:143]
	v_mfma_f32_16x16x32_bf16 v[136:139], v[148:151], v[172:175], v[136:139]
	v_mfma_f32_16x16x32_bf16 v[116:119], v[132:135], v[180:183], v[116:119]
	v_mfma_f32_16x16x32_bf16 v[108:111], v[148:151], v[180:183], v[108:111]
	v_mfma_f32_16x16x32_bf16 v[96:99], v[132:135], v[188:191], v[96:99]
	v_mfma_f32_16x16x32_bf16 v[92:95], v[148:151], v[188:191], v[92:95]
	v_mfma_f32_16x16x32_bf16 v[80:83], v[132:135], v[196:199], v[80:83]
	v_mfma_f32_16x16x32_bf16 v[76:79], v[148:151], v[196:199], v[76:79]
	v_mfma_f32_16x16x32_bf16 v[128:131], v[152:155], v[168:171], v[128:131]
	v_mfma_f32_16x16x32_bf16 v[124:127], v[160:163], v[168:171], v[124:127]
	v_mfma_f32_16x16x32_bf16 v[104:107], v[152:155], v[176:179], v[104:107]
	v_mfma_f32_16x16x32_bf16 v[100:103], v[160:163], v[176:179], v[100:103]
	v_mfma_f32_16x16x32_bf16 v[88:91], v[152:155], v[184:187], v[88:91]
	v_mfma_f32_16x16x32_bf16 v[84:87], v[160:163], v[184:187], v[84:87]
	v_mfma_f32_16x16x32_bf16 v[72:75], v[152:155], v[192:195], v[72:75]
	v_mfma_f32_16x16x32_bf16 v[68:71], v[160:163], v[192:195], v[68:71]
	v_mfma_f32_16x16x32_bf16 v[128:131], v[156:159], v[172:175], v[128:131]
	v_mfma_f32_16x16x32_bf16 v[124:127], v[164:167], v[172:175], v[124:127]
	v_mfma_f32_16x16x32_bf16 v[104:107], v[156:159], v[180:183], v[104:107]
	v_mfma_f32_16x16x32_bf16 v[100:103], v[164:167], v[180:183], v[100:103]
	v_mfma_f32_16x16x32_bf16 v[88:91], v[156:159], v[188:191], v[88:91]
	v_mfma_f32_16x16x32_bf16 v[84:87], v[164:167], v[188:191], v[84:87]
	v_mfma_f32_16x16x32_bf16 v[72:75], v[156:159], v[196:199], v[72:75]
	v_mfma_f32_16x16x32_bf16 v[68:71], v[164:167], v[196:199], v[68:71]
	s_setprio 0
	s_barrier
	s_add_i32 s4, s75, s16
	s_add_u32 s98, s52, 0x80
	s_addc_u32 s99, s53, 0
	s_mov_b32 m0, s4
	ds_read_b128 v[168:171], v233 offset:49152
	ds_read_b128 v[172:175], v233 offset:50176
	ds_read_b128 v[176:179], v233 offset:51200
	ds_read_b128 v[180:183], v233 offset:52224
	ds_read_b128 v[184:187], v233 offset:53248
	ds_read_b128 v[188:191], v233 offset:54272
	ds_read_b128 v[192:195], v233 offset:55296
	ds_read_b128 v[196:199], v233 offset:56320
	global_load_lds_dwordx4 v2, s[98:99]
	s_add_i32 m0, s4, 0x2000
	s_add_u32 s4, s52, 0x100080
	s_addc_u32 s5, s53, 0
	s_add_i32 s52, s76, s16
	global_load_lds_dwordx4 v204, s[98:99]
	s_mov_b32 m0, s52
	s_nop 0
	global_load_lds_dwordx4 v2, s[4:5]
	s_add_i32 m0, s52, 0x2000
	s_nop 0
	global_load_lds_dwordx4 v204, s[4:5]
	s_mov_b32 m0, s62
	s_nop 0
	global_load_lds_dwordx4 v208, s[12:13]
	s_mov_b32 m0, s63
	s_nop 0
	global_load_lds_dwordx4 v206, s[12:13]
	s_waitcnt vmcnt(8)
	s_waitcnt lgkmcnt(0)
	s_barrier
	s_setprio 1
	v_mfma_f32_16x16x32_bf16 v[64:67], v[120:123], v[168:171], v[64:67]
	v_mfma_f32_16x16x32_bf16 v[60:63], v[144:147], v[168:171], v[60:63]
	v_mfma_f32_16x16x32_bf16 v[48:51], v[120:123], v[176:179], v[48:51]
	v_mfma_f32_16x16x32_bf16 v[44:47], v[144:147], v[176:179], v[44:47]
	v_mfma_f32_16x16x32_bf16 v[32:35], v[120:123], v[184:187], v[32:35]
	v_mfma_f32_16x16x32_bf16 v[28:31], v[144:147], v[184:187], v[28:31]
	v_mfma_f32_16x16x32_bf16 v[16:19], v[120:123], v[192:195], v[16:19]
	v_mfma_f32_16x16x32_bf16 v[12:15], v[144:147], v[192:195], v[12:15]
	v_mfma_f32_16x16x32_bf16 v[64:67], v[132:135], v[172:175], v[64:67]
	v_mfma_f32_16x16x32_bf16 v[60:63], v[148:151], v[172:175], v[60:63]
	v_mfma_f32_16x16x32_bf16 v[48:51], v[132:135], v[180:183], v[48:51]
	v_mfma_f32_16x16x32_bf16 v[44:47], v[148:151], v[180:183], v[44:47]
	v_mfma_f32_16x16x32_bf16 v[32:35], v[132:135], v[188:191], v[32:35]
	v_mfma_f32_16x16x32_bf16 v[28:31], v[148:151], v[188:191], v[28:31]
	v_mfma_f32_16x16x32_bf16 v[16:19], v[132:135], v[196:199], v[16:19]
	v_mfma_f32_16x16x32_bf16 v[12:15], v[148:151], v[196:199], v[12:15]
	v_mfma_f32_16x16x32_bf16 v[56:59], v[152:155], v[168:171], v[56:59]
	v_mfma_f32_16x16x32_bf16 v[52:55], v[160:163], v[168:171], v[52:55]
	v_mfma_f32_16x16x32_bf16 v[40:43], v[152:155], v[176:179], v[40:43]
	v_mfma_f32_16x16x32_bf16 v[36:39], v[160:163], v[176:179], v[36:39]
	v_mfma_f32_16x16x32_bf16 v[24:27], v[152:155], v[184:187], v[24:27]
	v_mfma_f32_16x16x32_bf16 v[20:23], v[160:163], v[184:187], v[20:23]
	v_mfma_f32_16x16x32_bf16 v[8:11], v[152:155], v[192:195], v[8:11]
	v_mfma_f32_16x16x32_bf16 v[4:7], v[160:163], v[192:195], v[4:7]
	v_mfma_f32_16x16x32_bf16 v[56:59], v[156:159], v[172:175], v[56:59]
	v_mfma_f32_16x16x32_bf16 v[52:55], v[164:167], v[172:175], v[52:55]
	v_mfma_f32_16x16x32_bf16 v[40:43], v[156:159], v[180:183], v[40:43]
	v_mfma_f32_16x16x32_bf16 v[36:39], v[164:167], v[180:183], v[36:39]
	v_mfma_f32_16x16x32_bf16 v[24:27], v[156:159], v[188:191], v[24:27]
	v_mfma_f32_16x16x32_bf16 v[20:23], v[164:167], v[188:191], v[20:23]
	v_mfma_f32_16x16x32_bf16 v[8:11], v[156:159], v[196:199], v[8:11]
	v_mfma_f32_16x16x32_bf16 v[4:7], v[164:167], v[196:199], v[4:7]
	s_setprio 0
	s_barrier
	s_add_i32 s74, s74, 2
	s_add_u32 s50, s50, 0x100
	s_addc_u32 s51, s51, 0
	s_cmp_gt_u32 s74, 61
	s_cbranch_scc0 .LBB0_1459
	s_and_b64 vcc, exec, s[22:23]
	s_cbranch_vccz .LBB0_1462
	s_barrier
